# P0: w_in (both layers) also converted by the workgroup-cooperative 128x128 transposer (rope row permutation and column remap applied on the store side; bf16 RNE / e4m3 outputs as before)
# speedup vs baseline: 1.0223x; 1.0223x over previous
; #define GAS __attribute__((address_space(1)))
; #define LAS __attribute__((address_space(3)))
; #define LDS_WAIT() asm volatile("s_waitcnt lgkmcnt(0)" ::: "memory")
;     const int pr = item >> 1, kb = 2 * (pr / nblk) + (item & 1), nb = pr % nblk, k0 = 64 * kb, n0 = 32 * nb;
;     const int nr = n0 + (lane & 31); const int sc = MAP == 1 ? src_col_in(nr) : nr;
;     float v[32];
; #pragma unroll
;     for (int i = 0; i < 32; ++i) v[i] = sc >= 0 ? W[(size_t)(k0 + 2 * i + (lane >> 5)) * Nsrc + sc] : 0.f;
; #pragma unroll
;     for (int i = 0; i < 32; ++i) { const int k = k0 + 2 * i + (lane >> 5); float x = v[i] * wscale; if (KS) x *= (k < ksplit ? ksA[k] : ksB[k - ksplit]); scr[(2 * i + (lane >> 5)) * 33 + (lane & 31)] = x; }
;     LDS_WAIT(); asm volatile("" ::: "memory");
;     const int c = lane & 7;
; #pragma unroll
;     for (int j = 0; j < 4; ++j) { const int n = (lane >> 3) + 8 * j; const LAS float* s = scr + (8 * c) * 33 + n;
;         const unsigned long long o = (unsigned long long)pg8::pk4_fp8(s[0 * 33], s[1 * 33], s[2 * 33], s[3 * 33]) | ((unsigned long long)pg8::pk4_fp8(s[4 * 33], s[5 * 33], s[6 * 33], s[7 * 33]) << 32);
;         *(GAS unsigned long long*)(WT + (size_t)(n0 + n) * K + k0 + 8 * c) = o; }
;     LDS_WAIT(); asm volatile("" ::: "memory");
; }
; __global__ void __launch_bounds__(NWAVES * 64, 2) hybrid_fwd(Args args) {
;     ...
;             p0_transpose_item_f8<false>(args.in[16] + (size_t)l * FF * DM, FF, DM, DM / 32, (unsigned char*)(ws + WS_WDN + l * SZ_WDN), 128.f, args.in[16], args.in[16], 0, scr, r, lane);
.Lco_wdn_loop:
	s_waitcnt vmcnt(12)
	v_mul_f32_e32 v144, 0x43000000, v144
	v_mul_f32_e32 v145, 0x43000000, v145
	v_mul_f32_e32 v146, 0x43000000, v146
	v_mul_f32_e32 v147, 0x43000000, v147
	ds_write_b128 v209, v[144:147]
	v_mul_f32_e32 v148, 0x43000000, v148
	v_mul_f32_e32 v149, 0x43000000, v149
	v_mul_f32_e32 v150, 0x43000000, v150
	v_mul_f32_e32 v151, 0x43000000, v151
	ds_write_b128 v209, v[148:151] offset:1024
	v_mul_f32_e32 v152, 0x43000000, v152
	v_mul_f32_e32 v153, 0x43000000, v153
	v_mul_f32_e32 v154, 0x43000000, v154
	v_mul_f32_e32 v155, 0x43000000, v155
	ds_write_b128 v209, v[152:155] offset:2048
	v_mul_f32_e32 v156, 0x43000000, v156
	v_mul_f32_e32 v157, 0x43000000, v157
	v_mul_f32_e32 v158, 0x43000000, v158
	v_mul_f32_e32 v159, 0x43000000, v159
	ds_write_b128 v209, v[156:159] offset:3072
	v_mul_f32_e32 v160, 0x43000000, v160
	v_mul_f32_e32 v161, 0x43000000, v161
	v_mul_f32_e32 v162, 0x43000000, v162
	v_mul_f32_e32 v163, 0x43000000, v163
	ds_write_b128 v209, v[160:163] offset:4096
	v_mul_f32_e32 v164, 0x43000000, v164
	v_mul_f32_e32 v165, 0x43000000, v165
	v_mul_f32_e32 v166, 0x43000000, v166
	v_mul_f32_e32 v167, 0x43000000, v167
	ds_write_b128 v209, v[164:167] offset:5120
	v_mul_f32_e32 v168, 0x43000000, v168
	v_mul_f32_e32 v169, 0x43000000, v169
	v_mul_f32_e32 v170, 0x43000000, v170
	v_mul_f32_e32 v171, 0x43000000, v171
	ds_write_b128 v209, v[168:171] offset:6144
	v_mul_f32_e32 v172, 0x43000000, v172
	v_mul_f32_e32 v173, 0x43000000, v173
	v_mul_f32_e32 v174, 0x43000000, v174
	v_mul_f32_e32 v175, 0x43000000, v175
	ds_write_b128 v209, v[172:175] offset:7168
	s_waitcnt lgkmcnt(0)
	s_barrier
	s_mov_b64 s[8:9], s[4:5]
	global_load_dwordx4 v[144:147], v208, s[8:9]
	s_add_u32 s8, s8, 0x8000
	s_addc_u32 s9, s9, 0
	global_load_dwordx4 v[148:151], v208, s[8:9]
	s_add_u32 s8, s8, 0x8000
	s_addc_u32 s9, s9, 0
	global_load_dwordx4 v[152:155], v208, s[8:9]
	s_add_u32 s8, s8, 0x8000
	s_addc_u32 s9, s9, 0
	global_load_dwordx4 v[156:159], v208, s[8:9]
	s_add_u32 s8, s8, 0x8000
	s_addc_u32 s9, s9, 0
	global_load_dwordx4 v[160:163], v208, s[8:9]
	s_add_u32 s8, s8, 0x8000
	s_addc_u32 s9, s9, 0
	global_load_dwordx4 v[164:167], v208, s[8:9]
	s_add_u32 s8, s8, 0x8000
	s_addc_u32 s9, s9, 0
	global_load_dwordx4 v[168:171], v208, s[8:9]
	s_add_u32 s8, s8, 0x8000
	s_addc_u32 s9, s9, 0
	global_load_dwordx4 v[172:175], v208, s[8:9]
	s_add_i32 s24, s24, 1
	s_and_b32 s26, s24, 3
	s_cmp_eq_u32 s26, 0
	s_mov_b32 s26, 0x3ffd000
	s_cselect_b32 s26, s26, 0x1000
	s_add_u32 s4, s4, s26
	s_addc_u32 s5, s5, 0
	ds_read_b32 v226, v211
	ds_read_b32 v227, v211 offset:512
	ds_read_b32 v228, v211 offset:1024
	ds_read_b32 v229, v211 offset:1536
	ds_read_b32 v230, v211 offset:2048
	ds_read_b32 v231, v211 offset:2560
	ds_read_b32 v232, v211 offset:3072
	ds_read_b32 v233, v211 offset:3584
	ds_read_b32 v234, v211 offset:4096
	ds_read_b32 v235, v211 offset:4608
	ds_read_b32 v236, v211 offset:5120
	ds_read_b32 v237, v211 offset:5632
	ds_read_b32 v238, v211 offset:6144
	ds_read_b32 v239, v211 offset:6656
	ds_read_b32 v240, v211 offset:7168
	ds_read_b32 v241, v211 offset:7680
	s_waitcnt lgkmcnt(0)
	v_max_f32_e32 v226, v226, v226
	v_max_f32_e32 v227, v227, v227
	v_max_f32_e32 v228, v228, v228
	v_max_f32_e32 v229, v229, v229
	v_max_f32_e32 v230, v230, v230
	v_max_f32_e32 v231, v231, v231
	v_max_f32_e32 v232, v232, v232
	v_max_f32_e32 v233, v233, v233
	v_max_f32_e32 v234, v234, v234
	v_max_f32_e32 v235, v235, v235
	v_max_f32_e32 v236, v236, v236
	v_max_f32_e32 v237, v237, v237
	v_max_f32_e32 v238, v238, v238
	v_max_f32_e32 v239, v239, v239
	v_max_f32_e32 v240, v240, v240
	v_max_f32_e32 v241, v241, v241
	v_med3_f32 v226, v226, s44, v246
	v_med3_f32 v227, v227, s44, v246
	v_med3_f32 v228, v228, s44, v246
	v_med3_f32 v229, v229, s44, v246
	v_med3_f32 v230, v230, s44, v246
	v_med3_f32 v231, v231, s44, v246
	v_med3_f32 v232, v232, s44, v246
	v_med3_f32 v233, v233, s44, v246
	v_med3_f32 v234, v234, s44, v246
	v_med3_f32 v235, v235, s44, v246
	v_med3_f32 v236, v236, s44, v246
	v_med3_f32 v237, v237, s44, v246
	v_med3_f32 v238, v238, s44, v246
	v_med3_f32 v239, v239, s44, v246
	v_med3_f32 v240, v240, s44, v246
	v_med3_f32 v241, v241, s44, v246
	v_mov_b32_e32 v242, 0
	v_mov_b32_e32 v243, 0
	v_mov_b32_e32 v244, 0
	v_mov_b32_e32 v245, 0
	v_cvt_pk_fp8_f32 v242, v226, v227
	v_cvt_pk_fp8_f32 v243, v230, v231
	v_cvt_pk_fp8_f32 v244, v234, v235
	v_cvt_pk_fp8_f32 v245, v238, v239
	v_cvt_pk_fp8_f32 v242, v228, v229 op_sel:[0,0,1]
	v_cvt_pk_fp8_f32 v243, v232, v233 op_sel:[0,0,1]
	v_cvt_pk_fp8_f32 v244, v236, v237 op_sel:[0,0,1]
	v_cvt_pk_fp8_f32 v245, v240, v241 op_sel:[0,0,1]
	s_nop 0
	global_store_dwordx4 v215, v[242:245], s[6:7]
	ds_read_b32 v226, v213
	ds_read_b32 v227, v213 offset:512
	ds_read_b32 v228, v213 offset:1024
	ds_read_b32 v229, v213 offset:1536
	ds_read_b32 v230, v213 offset:2048
	ds_read_b32 v231, v213 offset:2560
	ds_read_b32 v232, v213 offset:3072
	ds_read_b32 v233, v213 offset:3584
	ds_read_b32 v234, v213 offset:4096
	ds_read_b32 v235, v213 offset:4608
	ds_read_b32 v236, v213 offset:5120
	ds_read_b32 v237, v213 offset:5632
	ds_read_b32 v238, v213 offset:6144
	ds_read_b32 v239, v213 offset:6656
	ds_read_b32 v240, v213 offset:7168
	ds_read_b32 v241, v213 offset:7680
	s_waitcnt lgkmcnt(0)
; #define GAS __attribute__((address_space(1)))
; #define LAS __attribute__((address_space(3)))
; #define LDS_WAIT() asm volatile("s_waitcnt lgkmcnt(0)" ::: "memory")
;     const int pr = item >> 1, kb = 2 * (pr / nblk) + (item & 1), nb = pr % nblk, k0 = 64 * kb, n0 = 32 * nb;
;     const int nr = n0 + (lane & 31); const int sc = MAP == 1 ? src_col_in(nr) : nr;
;     float v[32];
; #pragma unroll
;     for (int i = 0; i < 32; ++i) v[i] = sc >= 0 ? W[(size_t)(k0 + 2 * i + (lane >> 5)) * Nsrc + sc] : 0.f;
; #pragma unroll
;     for (int i = 0; i < 32; ++i) { const int k = k0 + 2 * i + (lane >> 5); float x = v[i] * wscale; if (KS) x *= (k < ksplit ? ksA[k] : ksB[k - ksplit]); scr[(2 * i + (lane >> 5)) * 33 + (lane & 31)] = x; }
;     LDS_WAIT(); asm volatile("" ::: "memory");
;     const int c = lane & 7;
; #pragma unroll
;     for (int j = 0; j < 4; ++j) { const int n = (lane >> 3) + 8 * j; const LAS float* s = scr + (8 * c) * 33 + n;
;         const unsigned long long o = (unsigned long long)pg8::pk4_fp8(s[0 * 33], s[1 * 33], s[2 * 33], s[3 * 33]) | ((unsigned long long)pg8::pk4_fp8(s[4 * 33], s[5 * 33], s[6 * 33], s[7 * 33]) << 32);
;         *(GAS unsigned long long*)(WT + (size_t)(n0 + n) * K + k0 + 8 * c) = o; }
;     LDS_WAIT(); asm volatile("" ::: "memory");
; }
; __global__ void __launch_bounds__(NWAVES * 64, 2) hybrid_fwd(Args args) {
;     ...
;             p0_transpose_item_f8<false>(args.in[16] + (size_t)l * FF * DM, FF, DM, DM / 32, (unsigned char*)(ws + WS_WDN + l * SZ_WDN), 128.f, args.in[16], args.in[16], 0, scr, r, lane);
	v_max_f32_e32 v226, v226, v226
	v_max_f32_e32 v227, v227, v227
	v_max_f32_e32 v228, v228, v228
	v_max_f32_e32 v229, v229, v229
	v_max_f32_e32 v230, v230, v230
	v_max_f32_e32 v231, v231, v231
	v_max_f32_e32 v232, v232, v232
	v_max_f32_e32 v233, v233, v233
	v_max_f32_e32 v234, v234, v234
	v_max_f32_e32 v235, v235, v235
	v_max_f32_e32 v236, v236, v236
	v_max_f32_e32 v237, v237, v237
	v_max_f32_e32 v238, v238, v238
	v_max_f32_e32 v239, v239, v239
	v_max_f32_e32 v240, v240, v240
	v_max_f32_e32 v241, v241, v241
	v_med3_f32 v226, v226, s44, v246
	v_med3_f32 v227, v227, s44, v246
	v_med3_f32 v228, v228, s44, v246
	v_med3_f32 v229, v229, s44, v246
	v_med3_f32 v230, v230, s44, v246
	v_med3_f32 v231, v231, s44, v246
	v_med3_f32 v232, v232, s44, v246
	v_med3_f32 v233, v233, s44, v246
	v_med3_f32 v234, v234, s44, v246
	v_med3_f32 v235, v235, s44, v246
	v_med3_f32 v236, v236, s44, v246
	v_med3_f32 v237, v237, s44, v246
	v_med3_f32 v238, v238, s44, v246
	v_med3_f32 v239, v239, s44, v246
	v_med3_f32 v240, v240, s44, v246
	v_med3_f32 v241, v241, s44, v246
	v_mov_b32_e32 v242, 0
	v_mov_b32_e32 v243, 0
	v_mov_b32_e32 v244, 0
	v_mov_b32_e32 v245, 0
	v_cvt_pk_fp8_f32 v242, v226, v227
	v_cvt_pk_fp8_f32 v243, v230, v231
	v_cvt_pk_fp8_f32 v244, v234, v235
	v_cvt_pk_fp8_f32 v245, v238, v239
	v_cvt_pk_fp8_f32 v242, v228, v229 op_sel:[0,0,1]
	v_cvt_pk_fp8_f32 v243, v232, v233 op_sel:[0,0,1]
	v_cvt_pk_fp8_f32 v244, v236, v237 op_sel:[0,0,1]
	v_cvt_pk_fp8_f32 v245, v240, v241 op_sel:[0,0,1]
	s_nop 0
	global_store_dwordx4 v216, v[242:245], s[6:7]
	s_add_i32 s25, s25, 1
	s_and_b32 s26, s25, 3
	s_cmp_eq_u32 s26, 0
	s_mov_b32 s26, 0xfd001000
	s_cselect_b32 s26, s26, 0x1000000
	s_cselect_b32 s27, -1, 0
	s_add_u32 s6, s6, s26
	s_addc_u32 s7, s7, s27
	s_waitcnt vmcnt(12)
	v_mul_f32_e32 v176, 0x43000000, v176
	v_mul_f32_e32 v177, 0x43000000, v177
	v_mul_f32_e32 v178, 0x43000000, v178
	v_mul_f32_e32 v179, 0x43000000, v179
	ds_write_b128 v210, v[176:179]
	v_mul_f32_e32 v180, 0x43000000, v180
	v_mul_f32_e32 v181, 0x43000000, v181
	v_mul_f32_e32 v182, 0x43000000, v182
	v_mul_f32_e32 v183, 0x43000000, v183
	ds_write_b128 v210, v[180:183] offset:1024
	v_mul_f32_e32 v184, 0x43000000, v184
	v_mul_f32_e32 v185, 0x43000000, v185
	v_mul_f32_e32 v186, 0x43000000, v186
	v_mul_f32_e32 v187, 0x43000000, v187
	ds_write_b128 v210, v[184:187] offset:2048
	v_mul_f32_e32 v188, 0x43000000, v188
	v_mul_f32_e32 v189, 0x43000000, v189
	v_mul_f32_e32 v190, 0x43000000, v190
	v_mul_f32_e32 v191, 0x43000000, v191
	ds_write_b128 v210, v[188:191] offset:3072
	v_mul_f32_e32 v192, 0x43000000, v192
	v_mul_f32_e32 v193, 0x43000000, v193
	v_mul_f32_e32 v194, 0x43000000, v194
	v_mul_f32_e32 v195, 0x43000000, v195
	ds_write_b128 v210, v[192:195] offset:4096
	v_mul_f32_e32 v196, 0x43000000, v196
	v_mul_f32_e32 v197, 0x43000000, v197
	v_mul_f32_e32 v198, 0x43000000, v198
	v_mul_f32_e32 v199, 0x43000000, v199
	ds_write_b128 v210, v[196:199] offset:5120
	v_mul_f32_e32 v200, 0x43000000, v200
	v_mul_f32_e32 v201, 0x43000000, v201
	v_mul_f32_e32 v202, 0x43000000, v202
	v_mul_f32_e32 v203, 0x43000000, v203
	ds_write_b128 v210, v[200:203] offset:6144
	v_mul_f32_e32 v204, 0x43000000, v204
	v_mul_f32_e32 v205, 0x43000000, v205
	v_mul_f32_e32 v206, 0x43000000, v206
	v_mul_f32_e32 v207, 0x43000000, v207
	ds_write_b128 v210, v[204:207] offset:7168
	s_waitcnt lgkmcnt(0)
	s_barrier
	s_mov_b64 s[8:9], s[4:5]
	global_load_dwordx4 v[176:179], v208, s[8:9]
	s_add_u32 s8, s8, 0x8000
	s_addc_u32 s9, s9, 0
	global_load_dwordx4 v[180:183], v208, s[8:9]
	s_add_u32 s8, s8, 0x8000
	s_addc_u32 s9, s9, 0
	global_load_dwordx4 v[184:187], v208, s[8:9]
	s_add_u32 s8, s8, 0x8000
	s_addc_u32 s9, s9, 0
	global_load_dwordx4 v[188:191], v208, s[8:9]
	s_add_u32 s8, s8, 0x8000
	s_addc_u32 s9, s9, 0
	global_load_dwordx4 v[192:195], v208, s[8:9]
	s_add_u32 s8, s8, 0x8000
	s_addc_u32 s9, s9, 0
	global_load_dwordx4 v[196:199], v208, s[8:9]
	s_add_u32 s8, s8, 0x8000
	s_addc_u32 s9, s9, 0
	global_load_dwordx4 v[200:203], v208, s[8:9]
	s_add_u32 s8, s8, 0x8000
	s_addc_u32 s9, s9, 0
	global_load_dwordx4 v[204:207], v208, s[8:9]
	s_add_i32 s24, s24, 1
	s_and_b32 s26, s24, 3
	s_cmp_eq_u32 s26, 0
	s_mov_b32 s26, 0x3ffd000
	s_cselect_b32 s26, s26, 0x1000
	s_add_u32 s4, s4, s26
	s_addc_u32 s5, s5, 0
	ds_read_b32 v226, v212
	ds_read_b32 v227, v212 offset:512
	ds_read_b32 v228, v212 offset:1024
	ds_read_b32 v229, v212 offset:1536
	ds_read_b32 v230, v212 offset:2048
	ds_read_b32 v231, v212 offset:2560
	ds_read_b32 v232, v212 offset:3072
	ds_read_b32 v233, v212 offset:3584
	ds_read_b32 v234, v212 offset:4096
	ds_read_b32 v235, v212 offset:4608
	ds_read_b32 v236, v212 offset:5120
	ds_read_b32 v237, v212 offset:5632
	ds_read_b32 v238, v212 offset:6144
	ds_read_b32 v239, v212 offset:6656
	ds_read_b32 v240, v212 offset:7168
	ds_read_b32 v241, v212 offset:7680
	s_waitcnt lgkmcnt(0)
; #define GAS __attribute__((address_space(1)))
; #define LAS __attribute__((address_space(3)))
; #define LDS_WAIT() asm volatile("s_waitcnt lgkmcnt(0)" ::: "memory")
;     const int pr = item >> 1, kb = 2 * (pr / nblk) + (item & 1), nb = pr % nblk, k0 = 64 * kb, n0 = 32 * nb;
;     const int nr = n0 + (lane & 31); const int sc = MAP == 1 ? src_col_in(nr) : nr;
;     float v[32];
; #pragma unroll
;     for (int i = 0; i < 32; ++i) v[i] = sc >= 0 ? W[(size_t)(k0 + 2 * i + (lane >> 5)) * Nsrc + sc] : 0.f;
; #pragma unroll
;     for (int i = 0; i < 32; ++i) { const int k = k0 + 2 * i + (lane >> 5); float x = v[i] * wscale; if (KS) x *= (k < ksplit ? ksA[k] : ksB[k - ksplit]); scr[(2 * i + (lane >> 5)) * 33 + (lane & 31)] = x; }
;     LDS_WAIT(); asm volatile("" ::: "memory");
;     const int c = lane & 7;
; #pragma unroll
;     for (int j = 0; j < 4; ++j) { const int n = (lane >> 3) + 8 * j; const LAS float* s = scr + (8 * c) * 33 + n;
;         const unsigned long long o = (unsigned long long)pg8::pk4_fp8(s[0 * 33], s[1 * 33], s[2 * 33], s[3 * 33]) | ((unsigned long long)pg8::pk4_fp8(s[4 * 33], s[5 * 33], s[6 * 33], s[7 * 33]) << 32);
;         *(GAS unsigned long long*)(WT + (size_t)(n0 + n) * K + k0 + 8 * c) = o; }
;     LDS_WAIT(); asm volatile("" ::: "memory");
; }
; __global__ void __launch_bounds__(NWAVES * 64, 2) hybrid_fwd(Args args) {
;     ...
;             p0_transpose_item_f8<false>(args.in[16] + (size_t)l * FF * DM, FF, DM, DM / 32, (unsigned char*)(ws + WS_WDN + l * SZ_WDN), 128.f, args.in[16], args.in[16], 0, scr, r, lane);
	v_max_f32_e32 v226, v226, v226
	v_max_f32_e32 v227, v227, v227
	v_max_f32_e32 v228, v228, v228
	v_max_f32_e32 v229, v229, v229
	v_max_f32_e32 v230, v230, v230
	v_max_f32_e32 v231, v231, v231
	v_max_f32_e32 v232, v232, v232
	v_max_f32_e32 v233, v233, v233
	v_max_f32_e32 v234, v234, v234
	v_max_f32_e32 v235, v235, v235
	v_max_f32_e32 v236, v236, v236
	v_max_f32_e32 v237, v237, v237
	v_max_f32_e32 v238, v238, v238
	v_max_f32_e32 v239, v239, v239
	v_max_f32_e32 v240, v240, v240
	v_max_f32_e32 v241, v241, v241
	v_med3_f32 v226, v226, s44, v246
	v_med3_f32 v227, v227, s44, v246
	v_med3_f32 v228, v228, s44, v246
	v_med3_f32 v229, v229, s44, v246
	v_med3_f32 v230, v230, s44, v246
	v_med3_f32 v231, v231, s44, v246
	v_med3_f32 v232, v232, s44, v246
	v_med3_f32 v233, v233, s44, v246
	v_med3_f32 v234, v234, s44, v246
	v_med3_f32 v235, v235, s44, v246
	v_med3_f32 v236, v236, s44, v246
	v_med3_f32 v237, v237, s44, v246
	v_med3_f32 v238, v238, s44, v246
	v_med3_f32 v239, v239, s44, v246
	v_med3_f32 v240, v240, s44, v246
	v_med3_f32 v241, v241, s44, v246
	v_mov_b32_e32 v242, 0
	v_mov_b32_e32 v243, 0
	v_mov_b32_e32 v244, 0
	v_mov_b32_e32 v245, 0
	v_cvt_pk_fp8_f32 v242, v226, v227
	v_cvt_pk_fp8_f32 v243, v230, v231
	v_cvt_pk_fp8_f32 v244, v234, v235
	v_cvt_pk_fp8_f32 v245, v238, v239
	v_cvt_pk_fp8_f32 v242, v228, v229 op_sel:[0,0,1]
	v_cvt_pk_fp8_f32 v243, v232, v233 op_sel:[0,0,1]
	v_cvt_pk_fp8_f32 v244, v236, v237 op_sel:[0,0,1]
	v_cvt_pk_fp8_f32 v245, v240, v241 op_sel:[0,0,1]
	s_nop 0
	global_store_dwordx4 v215, v[242:245], s[6:7]
	ds_read_b32 v226, v214
	ds_read_b32 v227, v214 offset:512
	ds_read_b32 v228, v214 offset:1024
	ds_read_b32 v229, v214 offset:1536
	ds_read_b32 v230, v214 offset:2048
	ds_read_b32 v231, v214 offset:2560
	ds_read_b32 v232, v214 offset:3072
	ds_read_b32 v233, v214 offset:3584
	ds_read_b32 v234, v214 offset:4096
	ds_read_b32 v235, v214 offset:4608
	ds_read_b32 v236, v214 offset:5120
	ds_read_b32 v237, v214 offset:5632
	ds_read_b32 v238, v214 offset:6144
	ds_read_b32 v239, v214 offset:6656
	ds_read_b32 v240, v214 offset:7168
	ds_read_b32 v241, v214 offset:7680
	s_waitcnt lgkmcnt(0)
	v_max_f32_e32 v226, v226, v226
	v_max_f32_e32 v227, v227, v227
	v_max_f32_e32 v228, v228, v228
	v_max_f32_e32 v229, v229, v229
	v_max_f32_e32 v230, v230, v230
	v_max_f32_e32 v231, v231, v231
	v_max_f32_e32 v232, v232, v232
	v_max_f32_e32 v233, v233, v233
	v_max_f32_e32 v234, v234, v234
	v_max_f32_e32 v235, v235, v235
	v_max_f32_e32 v236, v236, v236
	v_max_f32_e32 v237, v237, v237
	v_max_f32_e32 v238, v238, v238
	v_max_f32_e32 v239, v239, v239
	v_max_f32_e32 v240, v240, v240
	v_max_f32_e32 v241, v241, v241
	v_med3_f32 v226, v226, s44, v246
	v_med3_f32 v227, v227, s44, v246
	v_med3_f32 v228, v228, s44, v246
	v_med3_f32 v229, v229, s44, v246
	v_med3_f32 v230, v230, s44, v246
	v_med3_f32 v231, v231, s44, v246
	v_med3_f32 v232, v232, s44, v246
	v_med3_f32 v233, v233, s44, v246
	v_med3_f32 v234, v234, s44, v246
	v_med3_f32 v235, v235, s44, v246
	v_med3_f32 v236, v236, s44, v246
	v_med3_f32 v237, v237, s44, v246
	v_med3_f32 v238, v238, s44, v246
	v_med3_f32 v239, v239, s44, v246
	v_med3_f32 v240, v240, s44, v246
	v_med3_f32 v241, v241, s44, v246
	v_mov_b32_e32 v242, 0
	v_mov_b32_e32 v243, 0
	v_mov_b32_e32 v244, 0
	v_mov_b32_e32 v245, 0
	v_cvt_pk_fp8_f32 v242, v226, v227
	v_cvt_pk_fp8_f32 v243, v230, v231
	v_cvt_pk_fp8_f32 v244, v234, v235
	v_cvt_pk_fp8_f32 v245, v238, v239
	v_cvt_pk_fp8_f32 v242, v228, v229 op_sel:[0,0,1]
	v_cvt_pk_fp8_f32 v243, v232, v233 op_sel:[0,0,1]
	v_cvt_pk_fp8_f32 v244, v236, v237 op_sel:[0,0,1]
	v_cvt_pk_fp8_f32 v245, v240, v241 op_sel:[0,0,1]
	s_nop 0
	global_store_dwordx4 v216, v[242:245], s[6:7]
	s_add_i32 s25, s25, 1
	s_and_b32 s26, s25, 3
	s_cmp_eq_u32 s26, 0
	s_mov_b32 s26, 0xfd001000
	s_cselect_b32 s26, s26, 0x1000000
	s_cselect_b32 s27, -1, 0
	s_add_u32 s6, s6, s26
	s_addc_u32 s7, s7, s27
	s_sub_i32 s12, s12, 1
	s_cmp_lg_u32 s12, 0
	s_cbranch_scc1 .Lco_wdn_loop
	s_waitcnt vmcnt(12)
	v_mul_f32_e32 v144, 0x43000000, v144
	v_mul_f32_e32 v145, 0x43000000, v145
	v_mul_f32_e32 v146, 0x43000000, v146
	v_mul_f32_e32 v147, 0x43000000, v147
	ds_write_b128 v209, v[144:147]
	v_mul_f32_e32 v148, 0x43000000, v148
	v_mul_f32_e32 v149, 0x43000000, v149
	v_mul_f32_e32 v150, 0x43000000, v150
	v_mul_f32_e32 v151, 0x43000000, v151
	ds_write_b128 v209, v[148:151] offset:1024
	v_mul_f32_e32 v152, 0x43000000, v152
	v_mul_f32_e32 v153, 0x43000000, v153
	v_mul_f32_e32 v154, 0x43000000, v154
	v_mul_f32_e32 v155, 0x43000000, v155
	ds_write_b128 v209, v[152:155] offset:2048
	v_mul_f32_e32 v156, 0x43000000, v156
	v_mul_f32_e32 v157, 0x43000000, v157
	v_mul_f32_e32 v158, 0x43000000, v158
	v_mul_f32_e32 v159, 0x43000000, v159
	ds_write_b128 v209, v[156:159] offset:3072
	v_mul_f32_e32 v160, 0x43000000, v160
	v_mul_f32_e32 v161, 0x43000000, v161
	v_mul_f32_e32 v162, 0x43000000, v162
	v_mul_f32_e32 v163, 0x43000000, v163
	ds_write_b128 v209, v[160:163] offset:4096
	v_mul_f32_e32 v164, 0x43000000, v164
	v_mul_f32_e32 v165, 0x43000000, v165
	v_mul_f32_e32 v166, 0x43000000, v166
	v_mul_f32_e32 v167, 0x43000000, v167
	ds_write_b128 v209, v[164:167] offset:5120
	v_mul_f32_e32 v168, 0x43000000, v168
	v_mul_f32_e32 v169, 0x43000000, v169
	v_mul_f32_e32 v170, 0x43000000, v170
	v_mul_f32_e32 v171, 0x43000000, v171
	ds_write_b128 v209, v[168:171] offset:6144
	v_mul_f32_e32 v172, 0x43000000, v172
	v_mul_f32_e32 v173, 0x43000000, v173
	v_mul_f32_e32 v174, 0x43000000, v174
	v_mul_f32_e32 v175, 0x43000000, v175
	ds_write_b128 v209, v[172:175] offset:7168
	s_waitcnt lgkmcnt(0)
	s_barrier
; #define GAS __attribute__((address_space(1)))
; #define LAS __attribute__((address_space(3)))
; __device__ __forceinline__ unsigned pk4_fp8(float a, float b, float c, float d) {
;     a = fminf(fmaxf(a, -448.f), 448.f); b = fminf(fmaxf(b, -448.f), 448.f); c = fminf(fmaxf(c, -448.f), 448.f); d = fminf(fmaxf(d, -448.f), 448.f);
;     int w = __builtin_amdgcn_cvt_pk_fp8_f32(a, b, 0, false); w = __builtin_amdgcn_cvt_pk_fp8_f32(c, d, w, true); return (unsigned)w; }
;     ...
;     const int c = lane & 7;
; #pragma unroll
;     for (int j = 0; j < 4; ++j) { const int n = (lane >> 3) + 8 * j; const LAS float* s = scr + (8 * c) * 33 + n;
;         const unsigned long long o = (unsigned long long)pg8::pk4_fp8(s[0 * 33], s[1 * 33], s[2 * 33], s[3 * 33]) | ((unsigned long long)pg8::pk4_fp8(s[4 * 33], s[5 * 33], s[6 * 33], s[7 * 33]) << 32);
;         *(GAS unsigned long long*)(WT + (size_t)(n0 + n) * K + k0 + 8 * c) = o; }
	ds_read_b32 v226, v211
	ds_read_b32 v227, v211 offset:512
	ds_read_b32 v228, v211 offset:1024
	ds_read_b32 v229, v211 offset:1536
	ds_read_b32 v230, v211 offset:2048
	ds_read_b32 v231, v211 offset:2560
	ds_read_b32 v232, v211 offset:3072
	ds_read_b32 v233, v211 offset:3584
	ds_read_b32 v234, v211 offset:4096
	ds_read_b32 v235, v211 offset:4608
	ds_read_b32 v236, v211 offset:5120
	ds_read_b32 v237, v211 offset:5632
	ds_read_b32 v238, v211 offset:6144
	ds_read_b32 v239, v211 offset:6656
	ds_read_b32 v240, v211 offset:7168
	ds_read_b32 v241, v211 offset:7680
	s_waitcnt lgkmcnt(0)
	v_max_f32_e32 v226, v226, v226
	v_max_f32_e32 v227, v227, v227
	v_max_f32_e32 v228, v228, v228
	v_max_f32_e32 v229, v229, v229
	v_max_f32_e32 v230, v230, v230
	v_max_f32_e32 v231, v231, v231
	v_max_f32_e32 v232, v232, v232
	v_max_f32_e32 v233, v233, v233
	v_max_f32_e32 v234, v234, v234
	v_max_f32_e32 v235, v235, v235
	v_max_f32_e32 v236, v236, v236
	v_max_f32_e32 v237, v237, v237
	v_max_f32_e32 v238, v238, v238
	v_max_f32_e32 v239, v239, v239
	v_max_f32_e32 v240, v240, v240
	v_max_f32_e32 v241, v241, v241
	v_med3_f32 v226, v226, s44, v246
	v_med3_f32 v227, v227, s44, v246
	v_med3_f32 v228, v228, s44, v246
	v_med3_f32 v229, v229, s44, v246
	v_med3_f32 v230, v230, s44, v246
	v_med3_f32 v231, v231, s44, v246
	v_med3_f32 v232, v232, s44, v246
	v_med3_f32 v233, v233, s44, v246
	v_med3_f32 v234, v234, s44, v246
	v_med3_f32 v235, v235, s44, v246
	v_med3_f32 v236, v236, s44, v246
	v_med3_f32 v237, v237, s44, v246
	v_med3_f32 v238, v238, s44, v246
	v_med3_f32 v239, v239, s44, v246
	v_med3_f32 v240, v240, s44, v246
	v_med3_f32 v241, v241, s44, v246
	v_mov_b32_e32 v242, 0
	v_mov_b32_e32 v243, 0
	v_mov_b32_e32 v244, 0
	v_mov_b32_e32 v245, 0
	v_cvt_pk_fp8_f32 v242, v226, v227
	v_cvt_pk_fp8_f32 v243, v230, v231
	v_cvt_pk_fp8_f32 v244, v234, v235
	v_cvt_pk_fp8_f32 v245, v238, v239
	v_cvt_pk_fp8_f32 v242, v228, v229 op_sel:[0,0,1]
	v_cvt_pk_fp8_f32 v243, v232, v233 op_sel:[0,0,1]
	v_cvt_pk_fp8_f32 v244, v236, v237 op_sel:[0,0,1]
	v_cvt_pk_fp8_f32 v245, v240, v241 op_sel:[0,0,1]
	s_nop 0
	global_store_dwordx4 v215, v[242:245], s[6:7]
	ds_read_b32 v226, v213
	ds_read_b32 v227, v213 offset:512
	ds_read_b32 v228, v213 offset:1024
	ds_read_b32 v229, v213 offset:1536
	ds_read_b32 v230, v213 offset:2048
	ds_read_b32 v231, v213 offset:2560
	ds_read_b32 v232, v213 offset:3072
	ds_read_b32 v233, v213 offset:3584
	ds_read_b32 v234, v213 offset:4096
	ds_read_b32 v235, v213 offset:4608
	ds_read_b32 v236, v213 offset:5120
	ds_read_b32 v237, v213 offset:5632
	ds_read_b32 v238, v213 offset:6144
	ds_read_b32 v239, v213 offset:6656
	ds_read_b32 v240, v213 offset:7168
	ds_read_b32 v241, v213 offset:7680
	s_waitcnt lgkmcnt(0)
	v_max_f32_e32 v226, v226, v226
	v_max_f32_e32 v227, v227, v227
	v_max_f32_e32 v228, v228, v228
	v_max_f32_e32 v229, v229, v229
	v_max_f32_e32 v230, v230, v230
	v_max_f32_e32 v231, v231, v231
	v_max_f32_e32 v232, v232, v232
	v_max_f32_e32 v233, v233, v233
	v_max_f32_e32 v234, v234, v234
	v_max_f32_e32 v235, v235, v235
	v_max_f32_e32 v236, v236, v236
	v_max_f32_e32 v237, v237, v237
	v_max_f32_e32 v238, v238, v238
	v_max_f32_e32 v239, v239, v239
	v_max_f32_e32 v240, v240, v240
	v_max_f32_e32 v241, v241, v241
	v_med3_f32 v226, v226, s44, v246
	v_med3_f32 v227, v227, s44, v246
	v_med3_f32 v228, v228, s44, v246
	v_med3_f32 v229, v229, s44, v246
	v_med3_f32 v230, v230, s44, v246
	v_med3_f32 v231, v231, s44, v246
	v_med3_f32 v232, v232, s44, v246
	v_med3_f32 v233, v233, s44, v246
	v_med3_f32 v234, v234, s44, v246
	v_med3_f32 v235, v235, s44, v246
	v_med3_f32 v236, v236, s44, v246
	v_med3_f32 v237, v237, s44, v246
	v_med3_f32 v238, v238, s44, v246
	v_med3_f32 v239, v239, s44, v246
	v_med3_f32 v240, v240, s44, v246
	v_med3_f32 v241, v241, s44, v246
	v_mov_b32_e32 v242, 0
	v_mov_b32_e32 v243, 0
	v_mov_b32_e32 v244, 0
	v_mov_b32_e32 v245, 0
	v_cvt_pk_fp8_f32 v242, v226, v227
	v_cvt_pk_fp8_f32 v243, v230, v231
	v_cvt_pk_fp8_f32 v244, v234, v235
	v_cvt_pk_fp8_f32 v245, v238, v239
	v_cvt_pk_fp8_f32 v242, v228, v229 op_sel:[0,0,1]
	v_cvt_pk_fp8_f32 v243, v232, v233 op_sel:[0,0,1]
	v_cvt_pk_fp8_f32 v244, v236, v237 op_sel:[0,0,1]
	v_cvt_pk_fp8_f32 v245, v240, v241 op_sel:[0,0,1]
	s_nop 0
	global_store_dwordx4 v216, v[242:245], s[6:7]
	s_add_i32 s25, s25, 1
	s_and_b32 s26, s25, 3
	s_cmp_eq_u32 s26, 0
	s_mov_b32 s26, 0xfd001000
	s_cselect_b32 s26, s26, 0x1000000
	s_cselect_b32 s27, -1, 0
	s_add_u32 s6, s6, s26
	s_addc_u32 s7, s7, s27
	s_waitcnt vmcnt(4)
	v_mul_f32_e32 v176, 0x43000000, v176
	v_mul_f32_e32 v177, 0x43000000, v177
	v_mul_f32_e32 v178, 0x43000000, v178
	v_mul_f32_e32 v179, 0x43000000, v179
	ds_write_b128 v210, v[176:179]
	v_mul_f32_e32 v180, 0x43000000, v180
	v_mul_f32_e32 v181, 0x43000000, v181
	v_mul_f32_e32 v182, 0x43000000, v182
	v_mul_f32_e32 v183, 0x43000000, v183
	ds_write_b128 v210, v[180:183] offset:1024
	v_mul_f32_e32 v184, 0x43000000, v184
	v_mul_f32_e32 v185, 0x43000000, v185
	v_mul_f32_e32 v186, 0x43000000, v186
	v_mul_f32_e32 v187, 0x43000000, v187
	ds_write_b128 v210, v[184:187] offset:2048
	v_mul_f32_e32 v188, 0x43000000, v188
	v_mul_f32_e32 v189, 0x43000000, v189
	v_mul_f32_e32 v190, 0x43000000, v190
	v_mul_f32_e32 v191, 0x43000000, v191
	ds_write_b128 v210, v[188:191] offset:3072
	v_mul_f32_e32 v192, 0x43000000, v192
	v_mul_f32_e32 v193, 0x43000000, v193
	v_mul_f32_e32 v194, 0x43000000, v194
	v_mul_f32_e32 v195, 0x43000000, v195
	ds_write_b128 v210, v[192:195] offset:4096
	v_mul_f32_e32 v196, 0x43000000, v196
	v_mul_f32_e32 v197, 0x43000000, v197
	v_mul_f32_e32 v198, 0x43000000, v198
	v_mul_f32_e32 v199, 0x43000000, v199
	ds_write_b128 v210, v[196:199] offset:5120
	v_mul_f32_e32 v200, 0x43000000, v200
	v_mul_f32_e32 v201, 0x43000000, v201
	v_mul_f32_e32 v202, 0x43000000, v202
	v_mul_f32_e32 v203, 0x43000000, v203
	ds_write_b128 v210, v[200:203] offset:6144
	v_mul_f32_e32 v204, 0x43000000, v204
	v_mul_f32_e32 v205, 0x43000000, v205
	v_mul_f32_e32 v206, 0x43000000, v206
	v_mul_f32_e32 v207, 0x43000000, v207
	ds_write_b128 v210, v[204:207] offset:7168
	s_waitcnt lgkmcnt(0)
	s_barrier
; #define GAS __attribute__((address_space(1)))
; #define LAS __attribute__((address_space(3)))
;     ...
;     const int c = lane & 7;
; #pragma unroll
;     for (int j = 0; j < 4; ++j) { const int n = (lane >> 3) + 8 * j; const LAS float* s = scr + (8 * c) * 33 + n;
;         const unsigned long long o = (unsigned long long)pg8::pk4_fp8(s[0 * 33], s[1 * 33], s[2 * 33], s[3 * 33]) | ((unsigned long long)pg8::pk4_fp8(s[4 * 33], s[5 * 33], s[6 * 33], s[7 * 33]) << 32);
;         *(GAS unsigned long long*)(WT + (size_t)(n0 + n) * K + k0 + 8 * c) = o; }
; __global__ void __launch_bounds__(NWAVES * 64, 2) hybrid_fwd(Args args) {
;     ...
;         for (int rep = 0; rep < REP_PRO; ++rep)
;         for (int it = gw; it < DEPTH * I_L; it += NGW) {
;             const int l = it / I_L; int r = it % I_L;
;             if (r < I_IN) { if (l >= PROJ_F8_FROM) p0_transpose_item_f8<true, 1>(args.in[2] + (size_t)l * DM * NSRC, DM, NSRC, NPROJ / 32, (unsigned char*)(ws + WS_WIN + l * SZ_WIN), WUP8_SCALE, args.in[1] + l * DM, args.in[1] + l * DM, DM, scr, r, lane);
;                 else p0_transpose_item<1, true>(args.in[2] + (size_t)l * DM * NSRC, DM, NSRC, NPROJ / 32, (bf16*)(ws + WS_WIN + l * SZ_WIN), args.in[1] + l * DM, args.in[1] + l * DM, DM, scr, r, lane); continue; } r -= I_IN;
;             if (r < I_O) { if (l >= WO_F8_FROM) p0_transpose_item_f8<true>(args.in[13] + (size_t)l * DM * DM, DM, DM, DM / 32, (unsigned char*)(ws + WS_WO + l * SZ_WO), 64.f, args.in[6] + l * 2048, args.in[12] + l * 2048, 2048, scr, r, lane);
;                 else p0_transpose_item<0, true>(args.in[13] + (size_t)l * DM * DM, DM, DM, DM / 32, (bf16*)(ws + WS_WO + l * SZ_WO), args.in[6] + l * 2048, args.in[12] + l * 2048, 2048, scr, r, lane); continue; } r -= I_O;
;             if (r < I_UP) { p0_transpose_item_f8<true>(args.in[15] + (size_t)l * DM * FF, DM, FF, FF / 32, (unsigned char*)(ws + WS_WUP + l * SZ_WUP), WUP8_SCALE, args.in[14] + l * DM, args.in[14] + l * DM, DM, scr, r, lane); continue; } r -= I_UP;
;             p0_transpose_item_f8<false>(args.in[16] + (size_t)l * FF * DM, FF, DM, DM / 32, (unsigned char*)(ws + WS_WDN + l * SZ_WDN), 128.f, args.in[16], args.in[16], 0, scr, r, lane);
;         }
	ds_read_b32 v226, v212
	ds_read_b32 v227, v212 offset:512
	ds_read_b32 v228, v212 offset:1024
	ds_read_b32 v229, v212 offset:1536
	ds_read_b32 v230, v212 offset:2048
	ds_read_b32 v231, v212 offset:2560
	ds_read_b32 v232, v212 offset:3072
	ds_read_b32 v233, v212 offset:3584
	ds_read_b32 v234, v212 offset:4096
	ds_read_b32 v235, v212 offset:4608
	ds_read_b32 v236, v212 offset:5120
	ds_read_b32 v237, v212 offset:5632
	ds_read_b32 v238, v212 offset:6144
	ds_read_b32 v239, v212 offset:6656
	ds_read_b32 v240, v212 offset:7168
	ds_read_b32 v241, v212 offset:7680
	s_waitcnt lgkmcnt(0)
	v_max_f32_e32 v226, v226, v226
	v_max_f32_e32 v227, v227, v227
	v_max_f32_e32 v228, v228, v228
	v_max_f32_e32 v229, v229, v229
	v_max_f32_e32 v230, v230, v230
	v_max_f32_e32 v231, v231, v231
	v_max_f32_e32 v232, v232, v232
	v_max_f32_e32 v233, v233, v233
	v_max_f32_e32 v234, v234, v234
	v_max_f32_e32 v235, v235, v235
	v_max_f32_e32 v236, v236, v236
	v_max_f32_e32 v237, v237, v237
	v_max_f32_e32 v238, v238, v238
	v_max_f32_e32 v239, v239, v239
	v_max_f32_e32 v240, v240, v240
	v_max_f32_e32 v241, v241, v241
	v_med3_f32 v226, v226, s44, v246
	v_med3_f32 v227, v227, s44, v246
	v_med3_f32 v228, v228, s44, v246
	v_med3_f32 v229, v229, s44, v246
	v_med3_f32 v230, v230, s44, v246
	v_med3_f32 v231, v231, s44, v246
	v_med3_f32 v232, v232, s44, v246
	v_med3_f32 v233, v233, s44, v246
	v_med3_f32 v234, v234, s44, v246
	v_med3_f32 v235, v235, s44, v246
	v_med3_f32 v236, v236, s44, v246
	v_med3_f32 v237, v237, s44, v246
	v_med3_f32 v238, v238, s44, v246
	v_med3_f32 v239, v239, s44, v246
	v_med3_f32 v240, v240, s44, v246
	v_med3_f32 v241, v241, s44, v246
	v_mov_b32_e32 v242, 0
	v_mov_b32_e32 v243, 0
	v_mov_b32_e32 v244, 0
	v_mov_b32_e32 v245, 0
	v_cvt_pk_fp8_f32 v242, v226, v227
	v_cvt_pk_fp8_f32 v243, v230, v231
	v_cvt_pk_fp8_f32 v244, v234, v235
	v_cvt_pk_fp8_f32 v245, v238, v239
	v_cvt_pk_fp8_f32 v242, v228, v229 op_sel:[0,0,1]
	v_cvt_pk_fp8_f32 v243, v232, v233 op_sel:[0,0,1]
	v_cvt_pk_fp8_f32 v244, v236, v237 op_sel:[0,0,1]
	v_cvt_pk_fp8_f32 v245, v240, v241 op_sel:[0,0,1]
	s_nop 0
	global_store_dwordx4 v215, v[242:245], s[6:7]
	ds_read_b32 v226, v214
	ds_read_b32 v227, v214 offset:512
	ds_read_b32 v228, v214 offset:1024
	ds_read_b32 v229, v214 offset:1536
	ds_read_b32 v230, v214 offset:2048
	ds_read_b32 v231, v214 offset:2560
	ds_read_b32 v232, v214 offset:3072
	ds_read_b32 v233, v214 offset:3584
	ds_read_b32 v234, v214 offset:4096
	ds_read_b32 v235, v214 offset:4608
	ds_read_b32 v236, v214 offset:5120
	ds_read_b32 v237, v214 offset:5632
	ds_read_b32 v238, v214 offset:6144
	ds_read_b32 v239, v214 offset:6656
	ds_read_b32 v240, v214 offset:7168
	ds_read_b32 v241, v214 offset:7680
	s_waitcnt lgkmcnt(0)
	v_max_f32_e32 v226, v226, v226
	v_max_f32_e32 v227, v227, v227
	v_max_f32_e32 v228, v228, v228
	v_max_f32_e32 v229, v229, v229
	v_max_f32_e32 v230, v230, v230
	v_max_f32_e32 v231, v231, v231
	v_max_f32_e32 v232, v232, v232
	v_max_f32_e32 v233, v233, v233
	v_max_f32_e32 v234, v234, v234
	v_max_f32_e32 v235, v235, v235
	v_max_f32_e32 v236, v236, v236
	v_max_f32_e32 v237, v237, v237
	v_max_f32_e32 v238, v238, v238
	v_max_f32_e32 v239, v239, v239
	v_max_f32_e32 v240, v240, v240
	v_max_f32_e32 v241, v241, v241
	v_med3_f32 v226, v226, s44, v246
	v_med3_f32 v227, v227, s44, v246
	v_med3_f32 v228, v228, s44, v246
	v_med3_f32 v229, v229, s44, v246
	v_med3_f32 v230, v230, s44, v246
	v_med3_f32 v231, v231, s44, v246
	v_med3_f32 v232, v232, s44, v246
	v_med3_f32 v233, v233, s44, v246
	v_med3_f32 v234, v234, s44, v246
	v_med3_f32 v235, v235, s44, v246
	v_med3_f32 v236, v236, s44, v246
	v_med3_f32 v237, v237, s44, v246
	v_med3_f32 v238, v238, s44, v246
	v_med3_f32 v239, v239, s44, v246
	v_med3_f32 v240, v240, s44, v246
	v_med3_f32 v241, v241, s44, v246
	v_mov_b32_e32 v242, 0
	v_mov_b32_e32 v243, 0
	v_mov_b32_e32 v244, 0
	v_mov_b32_e32 v245, 0
	v_cvt_pk_fp8_f32 v242, v226, v227
	v_cvt_pk_fp8_f32 v243, v230, v231
	v_cvt_pk_fp8_f32 v244, v234, v235
	v_cvt_pk_fp8_f32 v245, v238, v239
	v_cvt_pk_fp8_f32 v242, v228, v229 op_sel:[0,0,1]
	v_cvt_pk_fp8_f32 v243, v232, v233 op_sel:[0,0,1]
	v_cvt_pk_fp8_f32 v244, v236, v237 op_sel:[0,0,1]
	v_cvt_pk_fp8_f32 v245, v240, v241 op_sel:[0,0,1]
	s_nop 0
	global_store_dwordx4 v216, v[242:245], s[6:7]
	s_add_i32 s25, s25, 1
	s_and_b32 s26, s25, 3
	s_cmp_eq_u32 s26, 0
	s_mov_b32 s26, 0xfd001000
	s_cselect_b32 s26, s26, 0x1000000
	s_cselect_b32 s27, -1, 0
	s_add_u32 s6, s6, s26
	s_addc_u32 s7, s7, s27
	s_add_u32 s16, s16, 0x10000000
	s_addc_u32 s17, s17, 0
	s_add_u32 s18, s18, 0x8000000
	s_addc_u32 s19, s19, 0
	s_add_i32 s13, s13, 1
	s_cmp_lg_u32 s13, 2
	s_cbranch_scc1 .Lco_wdn_layer
; #define LAS __attribute__((address_space(3)))
; __device__ __forceinline__ int nat_dim(int p) { return (p >> 1) + 64 * (p & 1); }
; __device__ __forceinline__ int src_col_in(int c) {
;     if (c < 5120) { const int blk = c >> 7, p = c & 127; const bool rope = blk < 16 || ((((blk - 16) >> 2) & 1) == 0); const int d = rope ? (p >> 1) + 64 * (p & 1) : p; return blk * 128 + d; }
;     if (c < OFF_Z) return c + 2096;
;     if (c < OFF_G) return c - 4048;
;     if (c < OFF_DT) return 5120 + (c - OFF_G);
;     if (c < NSRC) return c;
;     return -1;
; }
; template <int MAP, bool KS, bool KPERM = false>
; __device__ __forceinline__ void p0_transpose_item(const float* W, int K, int Nsrc, int nblk, bf16* WT, const float* ksA, const float* ksB, int ksplit, LAS float* scr, int item, int lane) {
;     const int kb = item / nblk, nb = item % nblk, k0 = 64 * kb, n0 = 32 * nb;
;     const int nr = n0 + (lane & 31); const int sc = MAP == 1 ? src_col_in(nr) : (MAP == 2 ? nat_dim(nr) : nr);
;     float v[32];
; #pragma unroll
;     for (int i = 0; i < 32; ++i) { const int k = k0 + 2 * i + (lane >> 5); const int ksrc = KPERM ? ((k & ~127) + nat_dim(k & 127)) : k;
;         v[i] = sc >= 0 ? W[(size_t)ksrc * Nsrc + sc] : 0.f; }
; #pragma unroll
;     for (int i = 0; i < 32; ++i) { const int kk = 2 * i + (lane >> 5); const int k = k0 + kk;
;         if (KS) v[i] *= (k < ksplit ? ksA[k] : ksB[k - ksplit]);
	v_lshrrev_b32_e32 v246, 5, v249
	v_lshl_add_u32 v246, v250, 4, v246
	v_and_b32_e32 v247, 31, v249
	v_lshlrev_b32_e32 v247, 4, v247
	s_mov_b32 s20, 0xb140
	v_mad_u32_u24 v208, v246, s20, v247
	v_lshrrev_b32_e32 v246, 4, v249
	v_lshl_add_u32 v246, v250, 4, v246
	v_and_b32_e32 v247, 15, v249
	v_lshlrev_b32_e32 v247, 4, v247
	v_lshl_add_u32 v100, v246, 13, v247
	v_and_b32_e32 v248, 63, v246
	v_lshlrev_b32_e32 v248, 1, v248
	v_lshrrev_b32_e32 v246, 6, v246
	v_or_b32_e32 v248, v248, v246
	v_lshl_add_u32 v104, v248, 13, v247
	v_lshrrev_b32_e32 v246, 4, v249
	v_lshl_add_u32 v246, v250, 4, v246
	v_add_u32_e32 v246, 4, v246
	v_and_b32_e32 v247, 15, v249
	v_lshlrev_b32_e32 v247, 4, v247
	v_lshl_add_u32 v101, v246, 13, v247
	v_and_b32_e32 v248, 63, v246
	v_lshlrev_b32_e32 v248, 1, v248
	v_lshrrev_b32_e32 v246, 6, v246
	v_or_b32_e32 v248, v248, v246
	v_lshl_add_u32 v105, v248, 13, v247
	v_lshrrev_b32_e32 v246, 4, v249
	v_lshl_add_u32 v246, v250, 4, v246
	v_add_u32_e32 v246, 8, v246
	v_and_b32_e32 v247, 15, v249
	v_lshlrev_b32_e32 v247, 4, v247
	v_lshl_add_u32 v102, v246, 13, v247
	v_and_b32_e32 v248, 63, v246
	v_lshlrev_b32_e32 v248, 1, v248
	v_lshrrev_b32_e32 v246, 6, v246
	v_or_b32_e32 v248, v248, v246
	v_lshl_add_u32 v106, v248, 13, v247
	v_lshrrev_b32_e32 v246, 4, v249
	v_lshl_add_u32 v246, v250, 4, v246
	v_add_u32_e32 v246, 12, v246
	v_and_b32_e32 v247, 15, v249
	v_lshlrev_b32_e32 v247, 4, v247
	v_lshl_add_u32 v103, v246, 13, v247
	v_and_b32_e32 v248, 63, v246
	v_lshlrev_b32_e32 v248, 1, v248
	v_lshrrev_b32_e32 v246, 6, v246
	v_or_b32_e32 v248, v248, v246
	v_lshl_add_u32 v107, v248, 13, v247
	v_and_b32_e32 v246, 15, v249
	v_lshrrev_b32_e32 v247, 1, v246
	v_lshlrev_b32_e32 v248, 2, v250
	v_xor_b32_e32 v248, v248, v247
	v_lshlrev_b32_e32 v248, 4, v248
	v_lshl_add_u32 v248, v246, 12, v248
	v_lshrrev_b32_e32 v247, 4, v249
	v_lshl_add_u32 v112, v247, 2, v248
	v_add_u32_e32 v113, 0x10000, v112
	v_and_b32_e32 v246, 15, v249
	v_lshrrev_b32_e32 v247, 1, v246
	v_lshlrev_b32_e32 v248, 2, v250
	v_add_u32_e32 v248, 1, v248
	v_xor_b32_e32 v248, v248, v247
	v_lshlrev_b32_e32 v248, 4, v248
	v_lshl_add_u32 v248, v246, 12, v248
	v_lshrrev_b32_e32 v247, 4, v249
	v_lshl_add_u32 v114, v247, 2, v248
	v_add_u32_e32 v115, 0x10000, v114
	v_and_b32_e32 v246, 15, v249
	v_lshrrev_b32_e32 v247, 1, v246
	v_lshlrev_b32_e32 v248, 2, v250
	v_add_u32_e32 v248, 2, v248
	v_xor_b32_e32 v248, v248, v247
	v_lshlrev_b32_e32 v248, 4, v248
	v_lshl_add_u32 v248, v246, 12, v248
	v_lshrrev_b32_e32 v247, 4, v249
	v_lshl_add_u32 v116, v247, 2, v248
	v_add_u32_e32 v117, 0x10000, v116
	v_and_b32_e32 v246, 15, v249
	v_lshrrev_b32_e32 v247, 1, v246
	v_lshlrev_b32_e32 v248, 2, v250
	v_add_u32_e32 v248, 3, v248
	v_xor_b32_e32 v248, v248, v247
	v_lshlrev_b32_e32 v248, 4, v248
	v_lshl_add_u32 v248, v246, 12, v248
	v_lshrrev_b32_e32 v247, 4, v249
	v_lshl_add_u32 v118, v247, 2, v248
	v_add_u32_e32 v119, 0x10000, v118
	s_lshr_b32 s22, s15, 3
	s_and_b32 s23, s15, 7
	v_readlane_b32 s16, v253, 7
	v_readlane_b32 s17, v253, 8
	v_readlane_b32 s18, v253, 41
	v_readlane_b32 s19, v253, 42
	s_mul_i32 s20, s22, 0x58a000
	s_add_u32 s16, s16, s20
	s_addc_u32 s17, s17, 0
	s_add_u32 s18, s18, 0x200000
	s_addc_u32 s19, s19, 0
	s_lshl_b32 s20, s22, 8
	s_add_u32 s18, s18, s20
	s_addc_u32 s19, s19, 0
	v_readlane_b32 s10, v253, 5
	v_readlane_b32 s11, v253, 6
	s_lshl_b32 s20, s22, 9
	s_add_u32 s10, s10, s20
	s_addc_u32 s11, s11, 0
	s_mov_b32 s44, 0xc3e00000
	v_mov_b32_e32 v246, 0x43e00000
	s_mov_b32 s28, 0x7fff
	s_mov_b32 s29, 0x07060302
	global_load_dword v218, v217, s[10:11] offset:0
	global_load_dword v219, v217, s[10:11] offset:8
	global_load_dword v220, v217, s[10:11] offset:16
	global_load_dword v221, v217, s[10:11] offset:24
	global_load_dword v222, v217, s[10:11] offset:32
	global_load_dword v223, v217, s[10:11] offset:40
	global_load_dword v224, v217, s[10:11] offset:48
	global_load_dword v225, v217, s[10:11] offset:56
	s_waitcnt vmcnt(0)
	s_mov_b32 s24, s23
	s_add_i32 s25, s23, 8
	s_lshl_b32 s20, s24, 7
	s_cmp_lt_u32 s24, 40
	s_cselect_b32 s21, 0, 0x830
	s_cmp_lt_u32 s24, 72
	s_cselect_b32 s21, s21, 0xfffff030
	s_add_i32 s20, s20, s21
	s_lshl_b32 s20, s20, 2
	s_add_u32 s8, s16, s20
	s_addc_u32 s9, s17, 0
	global_load_dwordx4 v[144:147], v208, s[8:9]
	s_add_u32 s8, s8, 0x16280
	s_addc_u32 s9, s9, 0
	global_load_dwordx4 v[148:151], v208, s[8:9]
	s_add_u32 s8, s8, 0x16280
	s_addc_u32 s9, s9, 0
	global_load_dwordx4 v[152:155], v208, s[8:9]
	s_add_u32 s8, s8, 0x16280
	s_addc_u32 s9, s9, 0
	global_load_dwordx4 v[156:159], v208, s[8:9]
	s_add_u32 s8, s8, 0x16280
	s_addc_u32 s9, s9, 0
	global_load_dwordx4 v[160:163], v208, s[8:9]
	s_add_u32 s8, s8, 0x16280
	s_addc_u32 s9, s9, 0
	global_load_dwordx4 v[164:167], v208, s[8:9]
	s_add_u32 s8, s8, 0x16280
	s_addc_u32 s9, s9, 0
	global_load_dwordx4 v[168:171], v208, s[8:9]
	s_add_u32 s8, s8, 0x16280
	s_addc_u32 s9, s9, 0
	global_load_dwordx4 v[172:175], v208, s[8:9]
	s_lshl_b32 s20, s25, 7
	s_cmp_lt_u32 s25, 40
	s_cselect_b32 s21, 0, 0x830
	s_cmp_lt_u32 s25, 72
	s_cselect_b32 s21, s21, 0xfffff030
	s_add_i32 s20, s20, s21
	s_lshl_b32 s20, s20, 2
	s_add_u32 s8, s16, s20
	s_addc_u32 s9, s17, 0
	global_load_dwordx4 v[176:179], v208, s[8:9]
	s_add_u32 s8, s8, 0x16280
	s_addc_u32 s9, s9, 0
	global_load_dwordx4 v[180:183], v208, s[8:9]
	s_add_u32 s8, s8, 0x16280
	s_addc_u32 s9, s9, 0
	global_load_dwordx4 v[184:187], v208, s[8:9]
	s_add_u32 s8, s8, 0x16280
	s_addc_u32 s9, s9, 0
	global_load_dwordx4 v[188:191], v208, s[8:9]
	s_add_u32 s8, s8, 0x16280
	s_addc_u32 s9, s9, 0
	global_load_dwordx4 v[192:195], v208, s[8:9]
	s_add_u32 s8, s8, 0x16280
	s_addc_u32 s9, s9, 0
	global_load_dwordx4 v[196:199], v208, s[8:9]
	s_add_u32 s8, s8, 0x16280
	s_addc_u32 s9, s9, 0
	global_load_dwordx4 v[200:203], v208, s[8:9]
	s_add_u32 s8, s8, 0x16280
	s_addc_u32 s9, s9, 0
	global_load_dwordx4 v[204:207], v208, s[8:9]
	s_add_i32 s26, s23, 0
	s_add_i32 s27, s23, 16
	s_waitcnt vmcnt(8)
; #define GAS __attribute__((address_space(1)))
; #define LAS __attribute__((address_space(3)))
; #define LDS_WAIT() asm volatile("s_waitcnt lgkmcnt(0)" ::: "memory")
; __device__ __forceinline__ unsigned f2bf(float f) { unsigned u = __builtin_bit_cast(unsigned, f); return (u + 0x7fffu + ((u >> 16) & 1u)) >> 16; }
; __device__ __forceinline__ unsigned pk2(float lo, float hi) { return f2bf(lo) | (f2bf(hi) << 16); }
; template <int MAP, bool KS, bool KPERM = false>
; __device__ __forceinline__ void p0_transpose_item(const float* W, int K, int Nsrc, int nblk, bf16* WT, const float* ksA, const float* ksB, int ksplit, LAS float* scr, int item, int lane) {
;     ...
;     for (int i = 0; i < 32; ++i) { const int kk = 2 * i + (lane >> 5); const int k = k0 + kk;
;         if (KS) v[i] *= (k < ksplit ? ksA[k] : ksB[k - ksplit]);
;         scr[kk * 33 + (lane & 31)] = v[i]; }
;     LDS_WAIT(); asm volatile("" ::: "memory");
;     const int c = lane & 7;
; #pragma unroll
;     for (int j = 0; j < 4; ++j) { const int n = (lane >> 3) + 8 * j; const LAS float* s = scr + (8 * c) * 33 + n;
;         v4u o; o.x = pk2(s[0 * 33], s[1 * 33]); o.y = pk2(s[2 * 33], s[3 * 33]); o.z = pk2(s[4 * 33], s[5 * 33]); o.w = pk2(s[6 * 33], s[7 * 33]);
;         *(GAS v4u*)(WT + (size_t)(n0 + n) * K + k0 + 8 * c) = o; }
	v_mul_f32_e32 v144, v218, v144
	v_mul_f32_e32 v145, v218, v145
	v_mul_f32_e32 v146, v218, v146
	v_mul_f32_e32 v147, v218, v147
	ds_write_b128 v209, v[144:147]
	v_mul_f32_e32 v148, v219, v148
	v_mul_f32_e32 v149, v219, v149
	v_mul_f32_e32 v150, v219, v150
	v_mul_f32_e32 v151, v219, v151
	ds_write_b128 v209, v[148:151] offset:1024
	v_mul_f32_e32 v152, v220, v152
	v_mul_f32_e32 v153, v220, v153
	v_mul_f32_e32 v154, v220, v154
	v_mul_f32_e32 v155, v220, v155
	ds_write_b128 v209, v[152:155] offset:2048
	v_mul_f32_e32 v156, v221, v156
	v_mul_f32_e32 v157, v221, v157
	v_mul_f32_e32 v158, v221, v158
	v_mul_f32_e32 v159, v221, v159
	ds_write_b128 v209, v[156:159] offset:3072
	v_mul_f32_e32 v160, v222, v160
	v_mul_f32_e32 v161, v222, v161
	v_mul_f32_e32 v162, v222, v162
	v_mul_f32_e32 v163, v222, v163
	ds_write_b128 v209, v[160:163] offset:4096
	v_mul_f32_e32 v164, v223, v164
	v_mul_f32_e32 v165, v223, v165
	v_mul_f32_e32 v166, v223, v166
	v_mul_f32_e32 v167, v223, v167
	ds_write_b128 v209, v[164:167] offset:5120
	v_mul_f32_e32 v168, v224, v168
	v_mul_f32_e32 v169, v224, v169
	v_mul_f32_e32 v170, v224, v170
	v_mul_f32_e32 v171, v224, v171
	ds_write_b128 v209, v[168:171] offset:6144
	v_mul_f32_e32 v172, v225, v172
	v_mul_f32_e32 v173, v225, v173
	v_mul_f32_e32 v174, v225, v174
	v_mul_f32_e32 v175, v225, v175
	ds_write_b128 v209, v[172:175] offset:7168
	s_waitcnt lgkmcnt(0)
	s_barrier
	s_lshl_b32 s20, s27, 7
	s_cmp_lt_u32 s27, 40
	s_cselect_b32 s21, 0, 0x830
	s_cmp_lt_u32 s27, 72
	s_cselect_b32 s21, s21, 0xfffff030
	s_add_i32 s20, s20, s21
	s_lshl_b32 s20, s20, 2
	s_add_u32 s8, s16, s20
	s_addc_u32 s9, s17, 0
	global_load_dwordx4 v[144:147], v208, s[8:9]
	s_add_u32 s8, s8, 0x16280
	s_addc_u32 s9, s9, 0
	global_load_dwordx4 v[148:151], v208, s[8:9]
	s_add_u32 s8, s8, 0x16280
	s_addc_u32 s9, s9, 0
	global_load_dwordx4 v[152:155], v208, s[8:9]
	s_add_u32 s8, s8, 0x16280
	s_addc_u32 s9, s9, 0
	global_load_dwordx4 v[156:159], v208, s[8:9]
	s_add_u32 s8, s8, 0x16280
	s_addc_u32 s9, s9, 0
	global_load_dwordx4 v[160:163], v208, s[8:9]
	s_add_u32 s8, s8, 0x16280
	s_addc_u32 s9, s9, 0
	global_load_dwordx4 v[164:167], v208, s[8:9]
	s_add_u32 s8, s8, 0x16280
	s_addc_u32 s9, s9, 0
	global_load_dwordx4 v[168:171], v208, s[8:9]
	s_add_u32 s8, s8, 0x16280
	s_addc_u32 s9, s9, 0
	global_load_dwordx4 v[172:175], v208, s[8:9]
	s_mul_i32 s20, s26, 0x100000
	s_add_u32 s6, s18, s20
	s_addc_u32 s7, s19, 0
	s_cmp_lt_u32 s26, 16
	s_cselect_b32 s20, 1, 0
	s_sub_i32 s21, s26, 16
	s_bitcmp0_b32 s21, 2
	s_cselect_b32 s21, 1, 0
	s_cmp_lt_u32 s26, 40
	s_cselect_b32 s21, s21, 0
	s_or_b32 s20, s20, s21
	s_cmp_lg_u32 s20, 0
	s_cselect_b64 s[20:21], -1, 0
	v_cndmask_b32_e64 v108, v100, v104, s[20:21]
	v_cndmask_b32_e64 v109, v101, v105, s[20:21]
	v_cndmask_b32_e64 v110, v102, v106, s[20:21]
	v_cndmask_b32_e64 v111, v103, v107, s[20:21]
	ds_read_b32 v226, v112
	ds_read_b32 v227, v112 offset:512
	ds_read_b32 v228, v112 offset:1024
	ds_read_b32 v229, v112 offset:1536
	ds_read_b32 v230, v112 offset:2048
	ds_read_b32 v231, v112 offset:2560
	ds_read_b32 v232, v112 offset:3072
	ds_read_b32 v233, v112 offset:3584
	s_waitcnt lgkmcnt(0)
	v_bfe_u32 v120, v226, 16, 1
	v_bfe_u32 v121, v227, 16, 1
	v_bfe_u32 v122, v228, 16, 1
	v_bfe_u32 v123, v229, 16, 1
	v_bfe_u32 v124, v230, 16, 1
	v_bfe_u32 v125, v231, 16, 1
	v_bfe_u32 v126, v232, 16, 1
	v_bfe_u32 v127, v233, 16, 1
	v_add3_u32 v226, v226, v120, s28
	v_add3_u32 v227, v227, v121, s28
	v_add3_u32 v228, v228, v122, s28
	v_add3_u32 v229, v229, v123, s28
	v_add3_u32 v230, v230, v124, s28
	v_add3_u32 v231, v231, v125, s28
	v_add3_u32 v232, v232, v126, s28
	v_add3_u32 v233, v233, v127, s28
	v_perm_b32 v242, v227, v226, s29
	v_perm_b32 v243, v229, v228, s29
	v_perm_b32 v244, v231, v230, s29
	v_perm_b32 v245, v233, v232, s29
	s_nop 0
	global_store_dwordx4 v108, v[242:245], s[6:7]
	ds_read_b32 v226, v114
	ds_read_b32 v227, v114 offset:512
	ds_read_b32 v228, v114 offset:1024
	ds_read_b32 v229, v114 offset:1536
	ds_read_b32 v230, v114 offset:2048
	ds_read_b32 v231, v114 offset:2560
	ds_read_b32 v232, v114 offset:3072
	ds_read_b32 v233, v114 offset:3584
	s_waitcnt lgkmcnt(0)
	v_bfe_u32 v120, v226, 16, 1
	v_bfe_u32 v121, v227, 16, 1
	v_bfe_u32 v122, v228, 16, 1
	v_bfe_u32 v123, v229, 16, 1
	v_bfe_u32 v124, v230, 16, 1
	v_bfe_u32 v125, v231, 16, 1
	v_bfe_u32 v126, v232, 16, 1
	v_bfe_u32 v127, v233, 16, 1
	v_add3_u32 v226, v226, v120, s28
	v_add3_u32 v227, v227, v121, s28
	v_add3_u32 v228, v228, v122, s28
	v_add3_u32 v229, v229, v123, s28
	v_add3_u32 v230, v230, v124, s28
	v_add3_u32 v231, v231, v125, s28
	v_add3_u32 v232, v232, v126, s28
	v_add3_u32 v233, v233, v127, s28
	v_perm_b32 v242, v227, v226, s29
	v_perm_b32 v243, v229, v228, s29
	v_perm_b32 v244, v231, v230, s29
	v_perm_b32 v245, v233, v232, s29
	s_nop 0
	global_store_dwordx4 v109, v[242:245], s[6:7]
	ds_read_b32 v226, v116
	ds_read_b32 v227, v116 offset:512
	ds_read_b32 v228, v116 offset:1024
	ds_read_b32 v229, v116 offset:1536
	ds_read_b32 v230, v116 offset:2048
	ds_read_b32 v231, v116 offset:2560
	ds_read_b32 v232, v116 offset:3072
	ds_read_b32 v233, v116 offset:3584
	s_waitcnt lgkmcnt(0)
	v_bfe_u32 v120, v226, 16, 1
	v_bfe_u32 v121, v227, 16, 1
	v_bfe_u32 v122, v228, 16, 1
	v_bfe_u32 v123, v229, 16, 1
	v_bfe_u32 v124, v230, 16, 1
	v_bfe_u32 v125, v231, 16, 1
	v_bfe_u32 v126, v232, 16, 1
	v_bfe_u32 v127, v233, 16, 1
	v_add3_u32 v226, v226, v120, s28
	v_add3_u32 v227, v227, v121, s28
	v_add3_u32 v228, v228, v122, s28
	v_add3_u32 v229, v229, v123, s28
	v_add3_u32 v230, v230, v124, s28
	v_add3_u32 v231, v231, v125, s28
	v_add3_u32 v232, v232, v126, s28
	v_add3_u32 v233, v233, v127, s28
	v_perm_b32 v242, v227, v226, s29
	v_perm_b32 v243, v229, v228, s29
	v_perm_b32 v244, v231, v230, s29
	v_perm_b32 v245, v233, v232, s29
	s_nop 0
	global_store_dwordx4 v110, v[242:245], s[6:7]
	ds_read_b32 v226, v118
	ds_read_b32 v227, v118 offset:512
	ds_read_b32 v228, v118 offset:1024
	ds_read_b32 v229, v118 offset:1536
	ds_read_b32 v230, v118 offset:2048
	ds_read_b32 v231, v118 offset:2560
	ds_read_b32 v232, v118 offset:3072
	ds_read_b32 v233, v118 offset:3584
	s_waitcnt lgkmcnt(0)
; #define GAS __attribute__((address_space(1)))
; #define LAS __attribute__((address_space(3)))
; #define LDS_WAIT() asm volatile("s_waitcnt lgkmcnt(0)" ::: "memory")
; __device__ __forceinline__ unsigned pk2(float lo, float hi) { return f2bf(lo) | (f2bf(hi) << 16); }
; template <int MAP, bool KS, bool KPERM = false>
; __device__ __forceinline__ void p0_transpose_item(const float* W, int K, int Nsrc, int nblk, bf16* WT, const float* ksA, const float* ksB, int ksplit, LAS float* scr, int item, int lane) {
;     ...
;     for (int i = 0; i < 32; ++i) { const int kk = 2 * i + (lane >> 5); const int k = k0 + kk;
;         if (KS) v[i] *= (k < ksplit ? ksA[k] : ksB[k - ksplit]);
;         scr[kk * 33 + (lane & 31)] = v[i]; }
;     LDS_WAIT(); asm volatile("" ::: "memory");
;     const int c = lane & 7;
; #pragma unroll
;     for (int j = 0; j < 4; ++j) { const int n = (lane >> 3) + 8 * j; const LAS float* s = scr + (8 * c) * 33 + n;
;         v4u o; o.x = pk2(s[0 * 33], s[1 * 33]); o.y = pk2(s[2 * 33], s[3 * 33]); o.z = pk2(s[4 * 33], s[5 * 33]); o.w = pk2(s[6 * 33], s[7 * 33]);
;         *(GAS v4u*)(WT + (size_t)(n0 + n) * K + k0 + 8 * c) = o; }
	v_bfe_u32 v120, v226, 16, 1
	v_bfe_u32 v121, v227, 16, 1
	v_bfe_u32 v122, v228, 16, 1
	v_bfe_u32 v123, v229, 16, 1
	v_bfe_u32 v124, v230, 16, 1
	v_bfe_u32 v125, v231, 16, 1
	v_bfe_u32 v126, v232, 16, 1
	v_bfe_u32 v127, v233, 16, 1
	v_add3_u32 v226, v226, v120, s28
	v_add3_u32 v227, v227, v121, s28
	v_add3_u32 v228, v228, v122, s28
	v_add3_u32 v229, v229, v123, s28
	v_add3_u32 v230, v230, v124, s28
	v_add3_u32 v231, v231, v125, s28
	v_add3_u32 v232, v232, v126, s28
	v_add3_u32 v233, v233, v127, s28
	v_perm_b32 v242, v227, v226, s29
	v_perm_b32 v243, v229, v228, s29
	v_perm_b32 v244, v231, v230, s29
	v_perm_b32 v245, v233, v232, s29
	s_nop 0
	global_store_dwordx4 v111, v[242:245], s[6:7]
	s_add_i32 s26, s23, 8
	s_add_i32 s27, s23, 24
	s_waitcnt vmcnt(12)
	v_mul_f32_e32 v176, v218, v176
	v_mul_f32_e32 v177, v218, v177
	v_mul_f32_e32 v178, v218, v178
	v_mul_f32_e32 v179, v218, v179
	ds_write_b128 v210, v[176:179]
	v_mul_f32_e32 v180, v219, v180
	v_mul_f32_e32 v181, v219, v181
	v_mul_f32_e32 v182, v219, v182
	v_mul_f32_e32 v183, v219, v183
	ds_write_b128 v210, v[180:183] offset:1024
	v_mul_f32_e32 v184, v220, v184
	v_mul_f32_e32 v185, v220, v185
	v_mul_f32_e32 v186, v220, v186
	v_mul_f32_e32 v187, v220, v187
	ds_write_b128 v210, v[184:187] offset:2048
	v_mul_f32_e32 v188, v221, v188
	v_mul_f32_e32 v189, v221, v189
	v_mul_f32_e32 v190, v221, v190
	v_mul_f32_e32 v191, v221, v191
	ds_write_b128 v210, v[188:191] offset:3072
	v_mul_f32_e32 v192, v222, v192
	v_mul_f32_e32 v193, v222, v193
	v_mul_f32_e32 v194, v222, v194
	v_mul_f32_e32 v195, v222, v195
	ds_write_b128 v210, v[192:195] offset:4096
	v_mul_f32_e32 v196, v223, v196
	v_mul_f32_e32 v197, v223, v197
	v_mul_f32_e32 v198, v223, v198
	v_mul_f32_e32 v199, v223, v199
	ds_write_b128 v210, v[196:199] offset:5120
	v_mul_f32_e32 v200, v224, v200
	v_mul_f32_e32 v201, v224, v201
	v_mul_f32_e32 v202, v224, v202
	v_mul_f32_e32 v203, v224, v203
	ds_write_b128 v210, v[200:203] offset:6144
	v_mul_f32_e32 v204, v225, v204
	v_mul_f32_e32 v205, v225, v205
	v_mul_f32_e32 v206, v225, v206
	v_mul_f32_e32 v207, v225, v207
	ds_write_b128 v210, v[204:207] offset:7168
	s_waitcnt lgkmcnt(0)
	s_barrier
	s_lshl_b32 s20, s27, 7
	s_cmp_lt_u32 s27, 40
	s_cselect_b32 s21, 0, 0x830
	s_cmp_lt_u32 s27, 72
	s_cselect_b32 s21, s21, 0xfffff030
	s_add_i32 s20, s20, s21
	s_lshl_b32 s20, s20, 2
	s_add_u32 s8, s16, s20
	s_addc_u32 s9, s17, 0
	global_load_dwordx4 v[176:179], v208, s[8:9]
	s_add_u32 s8, s8, 0x16280
	s_addc_u32 s9, s9, 0
	global_load_dwordx4 v[180:183], v208, s[8:9]
	s_add_u32 s8, s8, 0x16280
	s_addc_u32 s9, s9, 0
	global_load_dwordx4 v[184:187], v208, s[8:9]
	s_add_u32 s8, s8, 0x16280
	s_addc_u32 s9, s9, 0
	global_load_dwordx4 v[188:191], v208, s[8:9]
	s_add_u32 s8, s8, 0x16280
	s_addc_u32 s9, s9, 0
	global_load_dwordx4 v[192:195], v208, s[8:9]
	s_add_u32 s8, s8, 0x16280
	s_addc_u32 s9, s9, 0
	global_load_dwordx4 v[196:199], v208, s[8:9]
	s_add_u32 s8, s8, 0x16280
	s_addc_u32 s9, s9, 0
	global_load_dwordx4 v[200:203], v208, s[8:9]
	s_add_u32 s8, s8, 0x16280
	s_addc_u32 s9, s9, 0
	global_load_dwordx4 v[204:207], v208, s[8:9]
	s_mul_i32 s20, s26, 0x100000
	s_add_u32 s6, s18, s20
	s_addc_u32 s7, s19, 0
	s_cmp_lt_u32 s26, 16
	s_cselect_b32 s20, 1, 0
	s_sub_i32 s21, s26, 16
	s_bitcmp0_b32 s21, 2
	s_cselect_b32 s21, 1, 0
	s_cmp_lt_u32 s26, 40
	s_cselect_b32 s21, s21, 0
	s_or_b32 s20, s20, s21
	s_cmp_lg_u32 s20, 0
	s_cselect_b64 s[20:21], -1, 0
	v_cndmask_b32_e64 v108, v100, v104, s[20:21]
	v_cndmask_b32_e64 v109, v101, v105, s[20:21]
	v_cndmask_b32_e64 v110, v102, v106, s[20:21]
	v_cndmask_b32_e64 v111, v103, v107, s[20:21]
	ds_read_b32 v226, v113
	ds_read_b32 v227, v113 offset:512
	ds_read_b32 v228, v113 offset:1024
	ds_read_b32 v229, v113 offset:1536
	ds_read_b32 v230, v113 offset:2048
	ds_read_b32 v231, v113 offset:2560
	ds_read_b32 v232, v113 offset:3072
	ds_read_b32 v233, v113 offset:3584
	s_waitcnt lgkmcnt(0)
	v_bfe_u32 v120, v226, 16, 1
	v_bfe_u32 v121, v227, 16, 1
	v_bfe_u32 v122, v228, 16, 1
	v_bfe_u32 v123, v229, 16, 1
	v_bfe_u32 v124, v230, 16, 1
	v_bfe_u32 v125, v231, 16, 1
	v_bfe_u32 v126, v232, 16, 1
	v_bfe_u32 v127, v233, 16, 1
	v_add3_u32 v226, v226, v120, s28
	v_add3_u32 v227, v227, v121, s28
	v_add3_u32 v228, v228, v122, s28
	v_add3_u32 v229, v229, v123, s28
	v_add3_u32 v230, v230, v124, s28
	v_add3_u32 v231, v231, v125, s28
	v_add3_u32 v232, v232, v126, s28
	v_add3_u32 v233, v233, v127, s28
	v_perm_b32 v242, v227, v226, s29
	v_perm_b32 v243, v229, v228, s29
	v_perm_b32 v244, v231, v230, s29
	v_perm_b32 v245, v233, v232, s29
	s_nop 0
	global_store_dwordx4 v108, v[242:245], s[6:7]
	ds_read_b32 v226, v115
	ds_read_b32 v227, v115 offset:512
	ds_read_b32 v228, v115 offset:1024
	ds_read_b32 v229, v115 offset:1536
	ds_read_b32 v230, v115 offset:2048
	ds_read_b32 v231, v115 offset:2560
	ds_read_b32 v232, v115 offset:3072
	ds_read_b32 v233, v115 offset:3584
	s_waitcnt lgkmcnt(0)
	v_bfe_u32 v120, v226, 16, 1
	v_bfe_u32 v121, v227, 16, 1
	v_bfe_u32 v122, v228, 16, 1
	v_bfe_u32 v123, v229, 16, 1
	v_bfe_u32 v124, v230, 16, 1
	v_bfe_u32 v125, v231, 16, 1
	v_bfe_u32 v126, v232, 16, 1
	v_bfe_u32 v127, v233, 16, 1
	v_add3_u32 v226, v226, v120, s28
	v_add3_u32 v227, v227, v121, s28
	v_add3_u32 v228, v228, v122, s28
	v_add3_u32 v229, v229, v123, s28
	v_add3_u32 v230, v230, v124, s28
	v_add3_u32 v231, v231, v125, s28
	v_add3_u32 v232, v232, v126, s28
	v_add3_u32 v233, v233, v127, s28
	v_perm_b32 v242, v227, v226, s29
	v_perm_b32 v243, v229, v228, s29
	v_perm_b32 v244, v231, v230, s29
	v_perm_b32 v245, v233, v232, s29
	s_nop 0
	global_store_dwordx4 v109, v[242:245], s[6:7]
	ds_read_b32 v226, v117
	ds_read_b32 v227, v117 offset:512
	ds_read_b32 v228, v117 offset:1024
	ds_read_b32 v229, v117 offset:1536
	ds_read_b32 v230, v117 offset:2048
	ds_read_b32 v231, v117 offset:2560
	ds_read_b32 v232, v117 offset:3072
	ds_read_b32 v233, v117 offset:3584
	s_waitcnt lgkmcnt(0)
; #define GAS __attribute__((address_space(1)))
; #define LAS __attribute__((address_space(3)))
; #define LDS_WAIT() asm volatile("s_waitcnt lgkmcnt(0)" ::: "memory")
; __device__ __forceinline__ unsigned pk2(float lo, float hi) { return f2bf(lo) | (f2bf(hi) << 16); }
; template <int MAP, bool KS, bool KPERM = false>
; __device__ __forceinline__ void p0_transpose_item(const float* W, int K, int Nsrc, int nblk, bf16* WT, const float* ksA, const float* ksB, int ksplit, LAS float* scr, int item, int lane) {
;     ...
;     for (int i = 0; i < 32; ++i) { const int kk = 2 * i + (lane >> 5); const int k = k0 + kk;
;         if (KS) v[i] *= (k < ksplit ? ksA[k] : ksB[k - ksplit]);
;         scr[kk * 33 + (lane & 31)] = v[i]; }
;     LDS_WAIT(); asm volatile("" ::: "memory");
;     const int c = lane & 7;
; #pragma unroll
;     for (int j = 0; j < 4; ++j) { const int n = (lane >> 3) + 8 * j; const LAS float* s = scr + (8 * c) * 33 + n;
;         v4u o; o.x = pk2(s[0 * 33], s[1 * 33]); o.y = pk2(s[2 * 33], s[3 * 33]); o.z = pk2(s[4 * 33], s[5 * 33]); o.w = pk2(s[6 * 33], s[7 * 33]);
;         *(GAS v4u*)(WT + (size_t)(n0 + n) * K + k0 + 8 * c) = o; }
	v_bfe_u32 v120, v226, 16, 1
	v_bfe_u32 v121, v227, 16, 1
	v_bfe_u32 v122, v228, 16, 1
	v_bfe_u32 v123, v229, 16, 1
	v_bfe_u32 v124, v230, 16, 1
	v_bfe_u32 v125, v231, 16, 1
	v_bfe_u32 v126, v232, 16, 1
	v_bfe_u32 v127, v233, 16, 1
	v_add3_u32 v226, v226, v120, s28
	v_add3_u32 v227, v227, v121, s28
	v_add3_u32 v228, v228, v122, s28
	v_add3_u32 v229, v229, v123, s28
	v_add3_u32 v230, v230, v124, s28
	v_add3_u32 v231, v231, v125, s28
	v_add3_u32 v232, v232, v126, s28
	v_add3_u32 v233, v233, v127, s28
	v_perm_b32 v242, v227, v226, s29
	v_perm_b32 v243, v229, v228, s29
	v_perm_b32 v244, v231, v230, s29
	v_perm_b32 v245, v233, v232, s29
	s_nop 0
	global_store_dwordx4 v110, v[242:245], s[6:7]
	ds_read_b32 v226, v119
	ds_read_b32 v227, v119 offset:512
	ds_read_b32 v228, v119 offset:1024
	ds_read_b32 v229, v119 offset:1536
	ds_read_b32 v230, v119 offset:2048
	ds_read_b32 v231, v119 offset:2560
	ds_read_b32 v232, v119 offset:3072
	ds_read_b32 v233, v119 offset:3584
	s_waitcnt lgkmcnt(0)
	v_bfe_u32 v120, v226, 16, 1
	v_bfe_u32 v121, v227, 16, 1
	v_bfe_u32 v122, v228, 16, 1
	v_bfe_u32 v123, v229, 16, 1
	v_bfe_u32 v124, v230, 16, 1
	v_bfe_u32 v125, v231, 16, 1
	v_bfe_u32 v126, v232, 16, 1
	v_bfe_u32 v127, v233, 16, 1
	v_add3_u32 v226, v226, v120, s28
	v_add3_u32 v227, v227, v121, s28
	v_add3_u32 v228, v228, v122, s28
	v_add3_u32 v229, v229, v123, s28
	v_add3_u32 v230, v230, v124, s28
	v_add3_u32 v231, v231, v125, s28
	v_add3_u32 v232, v232, v126, s28
	v_add3_u32 v233, v233, v127, s28
	v_perm_b32 v242, v227, v226, s29
	v_perm_b32 v243, v229, v228, s29
	v_perm_b32 v244, v231, v230, s29
	v_perm_b32 v245, v233, v232, s29
	s_nop 0
	global_store_dwordx4 v111, v[242:245], s[6:7]
	s_add_i32 s26, s23, 16
	s_add_i32 s27, s23, 32
	s_waitcnt vmcnt(16)
	v_mul_f32_e32 v144, v218, v144
	v_mul_f32_e32 v145, v218, v145
	v_mul_f32_e32 v146, v218, v146
	v_mul_f32_e32 v147, v218, v147
	ds_write_b128 v209, v[144:147]
	v_mul_f32_e32 v148, v219, v148
	v_mul_f32_e32 v149, v219, v149
	v_mul_f32_e32 v150, v219, v150
	v_mul_f32_e32 v151, v219, v151
	ds_write_b128 v209, v[148:151] offset:1024
	v_mul_f32_e32 v152, v220, v152
	v_mul_f32_e32 v153, v220, v153
	v_mul_f32_e32 v154, v220, v154
	v_mul_f32_e32 v155, v220, v155
	ds_write_b128 v209, v[152:155] offset:2048
	v_mul_f32_e32 v156, v221, v156
	v_mul_f32_e32 v157, v221, v157
	v_mul_f32_e32 v158, v221, v158
	v_mul_f32_e32 v159, v221, v159
	ds_write_b128 v209, v[156:159] offset:3072
	v_mul_f32_e32 v160, v222, v160
	v_mul_f32_e32 v161, v222, v161
	v_mul_f32_e32 v162, v222, v162
	v_mul_f32_e32 v163, v222, v163
	ds_write_b128 v209, v[160:163] offset:4096
	v_mul_f32_e32 v164, v223, v164
	v_mul_f32_e32 v165, v223, v165
	v_mul_f32_e32 v166, v223, v166
	v_mul_f32_e32 v167, v223, v167
	ds_write_b128 v209, v[164:167] offset:5120
	v_mul_f32_e32 v168, v224, v168
	v_mul_f32_e32 v169, v224, v169
	v_mul_f32_e32 v170, v224, v170
	v_mul_f32_e32 v171, v224, v171
	ds_write_b128 v209, v[168:171] offset:6144
	v_mul_f32_e32 v172, v225, v172
	v_mul_f32_e32 v173, v225, v173
	v_mul_f32_e32 v174, v225, v174
	v_mul_f32_e32 v175, v225, v175
	ds_write_b128 v209, v[172:175] offset:7168
	s_waitcnt lgkmcnt(0)
	s_barrier
	s_lshl_b32 s20, s27, 7
	s_cmp_lt_u32 s27, 40
	s_cselect_b32 s21, 0, 0x830
	s_cmp_lt_u32 s27, 72
	s_cselect_b32 s21, s21, 0xfffff030
	s_add_i32 s20, s20, s21
	s_lshl_b32 s20, s20, 2
	s_add_u32 s8, s16, s20
	s_addc_u32 s9, s17, 0
	global_load_dwordx4 v[144:147], v208, s[8:9]
	s_add_u32 s8, s8, 0x16280
	s_addc_u32 s9, s9, 0
	global_load_dwordx4 v[148:151], v208, s[8:9]
	s_add_u32 s8, s8, 0x16280
	s_addc_u32 s9, s9, 0
	global_load_dwordx4 v[152:155], v208, s[8:9]
	s_add_u32 s8, s8, 0x16280
	s_addc_u32 s9, s9, 0
	global_load_dwordx4 v[156:159], v208, s[8:9]
	s_add_u32 s8, s8, 0x16280
	s_addc_u32 s9, s9, 0
	global_load_dwordx4 v[160:163], v208, s[8:9]
	s_add_u32 s8, s8, 0x16280
	s_addc_u32 s9, s9, 0
	global_load_dwordx4 v[164:167], v208, s[8:9]
	s_add_u32 s8, s8, 0x16280
	s_addc_u32 s9, s9, 0
	global_load_dwordx4 v[168:171], v208, s[8:9]
	s_add_u32 s8, s8, 0x16280
	s_addc_u32 s9, s9, 0
	global_load_dwordx4 v[172:175], v208, s[8:9]
	s_mul_i32 s20, s26, 0x100000
	s_add_u32 s6, s18, s20
	s_addc_u32 s7, s19, 0
	s_cmp_lt_u32 s26, 16
	s_cselect_b32 s20, 1, 0
	s_sub_i32 s21, s26, 16
	s_bitcmp0_b32 s21, 2
	s_cselect_b32 s21, 1, 0
	s_cmp_lt_u32 s26, 40
	s_cselect_b32 s21, s21, 0
	s_or_b32 s20, s20, s21
	s_cmp_lg_u32 s20, 0
	s_cselect_b64 s[20:21], -1, 0
	v_cndmask_b32_e64 v108, v100, v104, s[20:21]
	v_cndmask_b32_e64 v109, v101, v105, s[20:21]
	v_cndmask_b32_e64 v110, v102, v106, s[20:21]
	v_cndmask_b32_e64 v111, v103, v107, s[20:21]
	ds_read_b32 v226, v112
	ds_read_b32 v227, v112 offset:512
	ds_read_b32 v228, v112 offset:1024
	ds_read_b32 v229, v112 offset:1536
	ds_read_b32 v230, v112 offset:2048
	ds_read_b32 v231, v112 offset:2560
	ds_read_b32 v232, v112 offset:3072
	ds_read_b32 v233, v112 offset:3584
	s_waitcnt lgkmcnt(0)
	v_bfe_u32 v120, v226, 16, 1
	v_bfe_u32 v121, v227, 16, 1
	v_bfe_u32 v122, v228, 16, 1
	v_bfe_u32 v123, v229, 16, 1
	v_bfe_u32 v124, v230, 16, 1
	v_bfe_u32 v125, v231, 16, 1
	v_bfe_u32 v126, v232, 16, 1
	v_bfe_u32 v127, v233, 16, 1
	v_add3_u32 v226, v226, v120, s28
	v_add3_u32 v227, v227, v121, s28
	v_add3_u32 v228, v228, v122, s28
	v_add3_u32 v229, v229, v123, s28
	v_add3_u32 v230, v230, v124, s28
	v_add3_u32 v231, v231, v125, s28
	v_add3_u32 v232, v232, v126, s28
	v_add3_u32 v233, v233, v127, s28
	v_perm_b32 v242, v227, v226, s29
	v_perm_b32 v243, v229, v228, s29
	v_perm_b32 v244, v231, v230, s29
	v_perm_b32 v245, v233, v232, s29
	s_nop 0
	global_store_dwordx4 v108, v[242:245], s[6:7]
	ds_read_b32 v226, v114
	ds_read_b32 v227, v114 offset:512
	ds_read_b32 v228, v114 offset:1024
	ds_read_b32 v229, v114 offset:1536
	ds_read_b32 v230, v114 offset:2048
	ds_read_b32 v231, v114 offset:2560
	ds_read_b32 v232, v114 offset:3072
	ds_read_b32 v233, v114 offset:3584
	s_waitcnt lgkmcnt(0)
; #define GAS __attribute__((address_space(1)))
; #define LAS __attribute__((address_space(3)))
; #define LDS_WAIT() asm volatile("s_waitcnt lgkmcnt(0)" ::: "memory")
; __device__ __forceinline__ unsigned pk2(float lo, float hi) { return f2bf(lo) | (f2bf(hi) << 16); }
; template <int MAP, bool KS, bool KPERM = false>
; __device__ __forceinline__ void p0_transpose_item(const float* W, int K, int Nsrc, int nblk, bf16* WT, const float* ksA, const float* ksB, int ksplit, LAS float* scr, int item, int lane) {
;     ...
;     for (int i = 0; i < 32; ++i) { const int kk = 2 * i + (lane >> 5); const int k = k0 + kk;
;         if (KS) v[i] *= (k < ksplit ? ksA[k] : ksB[k - ksplit]);
;         scr[kk * 33 + (lane & 31)] = v[i]; }
;     LDS_WAIT(); asm volatile("" ::: "memory");
;     const int c = lane & 7;
; #pragma unroll
;     for (int j = 0; j < 4; ++j) { const int n = (lane >> 3) + 8 * j; const LAS float* s = scr + (8 * c) * 33 + n;
;         v4u o; o.x = pk2(s[0 * 33], s[1 * 33]); o.y = pk2(s[2 * 33], s[3 * 33]); o.z = pk2(s[4 * 33], s[5 * 33]); o.w = pk2(s[6 * 33], s[7 * 33]);
;         *(GAS v4u*)(WT + (size_t)(n0 + n) * K + k0 + 8 * c) = o; }
	v_bfe_u32 v120, v226, 16, 1
	v_bfe_u32 v121, v227, 16, 1
	v_bfe_u32 v122, v228, 16, 1
	v_bfe_u32 v123, v229, 16, 1
	v_bfe_u32 v124, v230, 16, 1
	v_bfe_u32 v125, v231, 16, 1
	v_bfe_u32 v126, v232, 16, 1
	v_bfe_u32 v127, v233, 16, 1
	v_add3_u32 v226, v226, v120, s28
	v_add3_u32 v227, v227, v121, s28
	v_add3_u32 v228, v228, v122, s28
	v_add3_u32 v229, v229, v123, s28
	v_add3_u32 v230, v230, v124, s28
	v_add3_u32 v231, v231, v125, s28
	v_add3_u32 v232, v232, v126, s28
	v_add3_u32 v233, v233, v127, s28
	v_perm_b32 v242, v227, v226, s29
	v_perm_b32 v243, v229, v228, s29
	v_perm_b32 v244, v231, v230, s29
	v_perm_b32 v245, v233, v232, s29
	s_nop 0
	global_store_dwordx4 v109, v[242:245], s[6:7]
	ds_read_b32 v226, v116
	ds_read_b32 v227, v116 offset:512
	ds_read_b32 v228, v116 offset:1024
	ds_read_b32 v229, v116 offset:1536
	ds_read_b32 v230, v116 offset:2048
	ds_read_b32 v231, v116 offset:2560
	ds_read_b32 v232, v116 offset:3072
	ds_read_b32 v233, v116 offset:3584
	s_waitcnt lgkmcnt(0)
	v_bfe_u32 v120, v226, 16, 1
	v_bfe_u32 v121, v227, 16, 1
	v_bfe_u32 v122, v228, 16, 1
	v_bfe_u32 v123, v229, 16, 1
	v_bfe_u32 v124, v230, 16, 1
	v_bfe_u32 v125, v231, 16, 1
	v_bfe_u32 v126, v232, 16, 1
	v_bfe_u32 v127, v233, 16, 1
	v_add3_u32 v226, v226, v120, s28
	v_add3_u32 v227, v227, v121, s28
	v_add3_u32 v228, v228, v122, s28
	v_add3_u32 v229, v229, v123, s28
	v_add3_u32 v230, v230, v124, s28
	v_add3_u32 v231, v231, v125, s28
	v_add3_u32 v232, v232, v126, s28
	v_add3_u32 v233, v233, v127, s28
	v_perm_b32 v242, v227, v226, s29
	v_perm_b32 v243, v229, v228, s29
	v_perm_b32 v244, v231, v230, s29
	v_perm_b32 v245, v233, v232, s29
	s_nop 0
	global_store_dwordx4 v110, v[242:245], s[6:7]
	ds_read_b32 v226, v118
	ds_read_b32 v227, v118 offset:512
	ds_read_b32 v228, v118 offset:1024
	ds_read_b32 v229, v118 offset:1536
	ds_read_b32 v230, v118 offset:2048
	ds_read_b32 v231, v118 offset:2560
	ds_read_b32 v232, v118 offset:3072
	ds_read_b32 v233, v118 offset:3584
	s_waitcnt lgkmcnt(0)
	v_bfe_u32 v120, v226, 16, 1
	v_bfe_u32 v121, v227, 16, 1
	v_bfe_u32 v122, v228, 16, 1
	v_bfe_u32 v123, v229, 16, 1
	v_bfe_u32 v124, v230, 16, 1
	v_bfe_u32 v125, v231, 16, 1
	v_bfe_u32 v126, v232, 16, 1
	v_bfe_u32 v127, v233, 16, 1
	v_add3_u32 v226, v226, v120, s28
	v_add3_u32 v227, v227, v121, s28
	v_add3_u32 v228, v228, v122, s28
	v_add3_u32 v229, v229, v123, s28
	v_add3_u32 v230, v230, v124, s28
	v_add3_u32 v231, v231, v125, s28
	v_add3_u32 v232, v232, v126, s28
	v_add3_u32 v233, v233, v127, s28
	v_perm_b32 v242, v227, v226, s29
	v_perm_b32 v243, v229, v228, s29
	v_perm_b32 v244, v231, v230, s29
	v_perm_b32 v245, v233, v232, s29
	s_nop 0
	global_store_dwordx4 v111, v[242:245], s[6:7]
	s_add_i32 s26, s23, 24
	s_add_i32 s27, s23, 40
	s_waitcnt vmcnt(16)
	v_mul_f32_e32 v176, v218, v176
	v_mul_f32_e32 v177, v218, v177
	v_mul_f32_e32 v178, v218, v178
	v_mul_f32_e32 v179, v218, v179
	ds_write_b128 v210, v[176:179]
	v_mul_f32_e32 v180, v219, v180
	v_mul_f32_e32 v181, v219, v181
	v_mul_f32_e32 v182, v219, v182
	v_mul_f32_e32 v183, v219, v183
	ds_write_b128 v210, v[180:183] offset:1024
	v_mul_f32_e32 v184, v220, v184
	v_mul_f32_e32 v185, v220, v185
	v_mul_f32_e32 v186, v220, v186
	v_mul_f32_e32 v187, v220, v187
	ds_write_b128 v210, v[184:187] offset:2048
	v_mul_f32_e32 v188, v221, v188
	v_mul_f32_e32 v189, v221, v189
	v_mul_f32_e32 v190, v221, v190
	v_mul_f32_e32 v191, v221, v191
	ds_write_b128 v210, v[188:191] offset:3072
	v_mul_f32_e32 v192, v222, v192
	v_mul_f32_e32 v193, v222, v193
	v_mul_f32_e32 v194, v222, v194
	v_mul_f32_e32 v195, v222, v195
	ds_write_b128 v210, v[192:195] offset:4096
	v_mul_f32_e32 v196, v223, v196
	v_mul_f32_e32 v197, v223, v197
	v_mul_f32_e32 v198, v223, v198
	v_mul_f32_e32 v199, v223, v199
	ds_write_b128 v210, v[196:199] offset:5120
	v_mul_f32_e32 v200, v224, v200
	v_mul_f32_e32 v201, v224, v201
	v_mul_f32_e32 v202, v224, v202
	v_mul_f32_e32 v203, v224, v203
	ds_write_b128 v210, v[200:203] offset:6144
	v_mul_f32_e32 v204, v225, v204
	v_mul_f32_e32 v205, v225, v205
	v_mul_f32_e32 v206, v225, v206
	v_mul_f32_e32 v207, v225, v207
	ds_write_b128 v210, v[204:207] offset:7168
	s_waitcnt lgkmcnt(0)
	s_barrier
	s_lshl_b32 s20, s27, 7
	s_cmp_lt_u32 s27, 40
	s_cselect_b32 s21, 0, 0x830
	s_cmp_lt_u32 s27, 72
	s_cselect_b32 s21, s21, 0xfffff030
	s_add_i32 s20, s20, s21
	s_lshl_b32 s20, s20, 2
	s_add_u32 s8, s16, s20
	s_addc_u32 s9, s17, 0
	global_load_dwordx4 v[176:179], v208, s[8:9]
	s_add_u32 s8, s8, 0x16280
	s_addc_u32 s9, s9, 0
	global_load_dwordx4 v[180:183], v208, s[8:9]
	s_add_u32 s8, s8, 0x16280
	s_addc_u32 s9, s9, 0
	global_load_dwordx4 v[184:187], v208, s[8:9]
	s_add_u32 s8, s8, 0x16280
	s_addc_u32 s9, s9, 0
	global_load_dwordx4 v[188:191], v208, s[8:9]
	s_add_u32 s8, s8, 0x16280
	s_addc_u32 s9, s9, 0
	global_load_dwordx4 v[192:195], v208, s[8:9]
	s_add_u32 s8, s8, 0x16280
	s_addc_u32 s9, s9, 0
	global_load_dwordx4 v[196:199], v208, s[8:9]
	s_add_u32 s8, s8, 0x16280
	s_addc_u32 s9, s9, 0
	global_load_dwordx4 v[200:203], v208, s[8:9]
	s_add_u32 s8, s8, 0x16280
	s_addc_u32 s9, s9, 0
	global_load_dwordx4 v[204:207], v208, s[8:9]
	s_mul_i32 s20, s26, 0x100000
	s_add_u32 s6, s18, s20
	s_addc_u32 s7, s19, 0
	s_cmp_lt_u32 s26, 16
	s_cselect_b32 s20, 1, 0
	s_sub_i32 s21, s26, 16
	s_bitcmp0_b32 s21, 2
	s_cselect_b32 s21, 1, 0
	s_cmp_lt_u32 s26, 40
	s_cselect_b32 s21, s21, 0
	s_or_b32 s20, s20, s21
	s_cmp_lg_u32 s20, 0
	s_cselect_b64 s[20:21], -1, 0
	v_cndmask_b32_e64 v108, v100, v104, s[20:21]
	v_cndmask_b32_e64 v109, v101, v105, s[20:21]
	v_cndmask_b32_e64 v110, v102, v106, s[20:21]
	v_cndmask_b32_e64 v111, v103, v107, s[20:21]
	ds_read_b32 v226, v113
	ds_read_b32 v227, v113 offset:512
	ds_read_b32 v228, v113 offset:1024
	ds_read_b32 v229, v113 offset:1536
	ds_read_b32 v230, v113 offset:2048
	ds_read_b32 v231, v113 offset:2560
	ds_read_b32 v232, v113 offset:3072
	ds_read_b32 v233, v113 offset:3584
	s_waitcnt lgkmcnt(0)
; #define GAS __attribute__((address_space(1)))
; #define LAS __attribute__((address_space(3)))
; #define LDS_WAIT() asm volatile("s_waitcnt lgkmcnt(0)" ::: "memory")
; __device__ __forceinline__ unsigned pk2(float lo, float hi) { return f2bf(lo) | (f2bf(hi) << 16); }
; template <int MAP, bool KS, bool KPERM = false>
; __device__ __forceinline__ void p0_transpose_item(const float* W, int K, int Nsrc, int nblk, bf16* WT, const float* ksA, const float* ksB, int ksplit, LAS float* scr, int item, int lane) {
;     ...
;     for (int i = 0; i < 32; ++i) { const int kk = 2 * i + (lane >> 5); const int k = k0 + kk;
;         if (KS) v[i] *= (k < ksplit ? ksA[k] : ksB[k - ksplit]);
;         scr[kk * 33 + (lane & 31)] = v[i]; }
;     LDS_WAIT(); asm volatile("" ::: "memory");
;     const int c = lane & 7;
; #pragma unroll
;     for (int j = 0; j < 4; ++j) { const int n = (lane >> 3) + 8 * j; const LAS float* s = scr + (8 * c) * 33 + n;
;         v4u o; o.x = pk2(s[0 * 33], s[1 * 33]); o.y = pk2(s[2 * 33], s[3 * 33]); o.z = pk2(s[4 * 33], s[5 * 33]); o.w = pk2(s[6 * 33], s[7 * 33]);
;         *(GAS v4u*)(WT + (size_t)(n0 + n) * K + k0 + 8 * c) = o; }
	v_bfe_u32 v120, v226, 16, 1
	v_bfe_u32 v121, v227, 16, 1
	v_bfe_u32 v122, v228, 16, 1
	v_bfe_u32 v123, v229, 16, 1
	v_bfe_u32 v124, v230, 16, 1
	v_bfe_u32 v125, v231, 16, 1
	v_bfe_u32 v126, v232, 16, 1
	v_bfe_u32 v127, v233, 16, 1
	v_add3_u32 v226, v226, v120, s28
	v_add3_u32 v227, v227, v121, s28
	v_add3_u32 v228, v228, v122, s28
	v_add3_u32 v229, v229, v123, s28
	v_add3_u32 v230, v230, v124, s28
	v_add3_u32 v231, v231, v125, s28
	v_add3_u32 v232, v232, v126, s28
	v_add3_u32 v233, v233, v127, s28
	v_perm_b32 v242, v227, v226, s29
	v_perm_b32 v243, v229, v228, s29
	v_perm_b32 v244, v231, v230, s29
	v_perm_b32 v245, v233, v232, s29
	s_nop 0
	global_store_dwordx4 v108, v[242:245], s[6:7]
	ds_read_b32 v226, v115
	ds_read_b32 v227, v115 offset:512
	ds_read_b32 v228, v115 offset:1024
	ds_read_b32 v229, v115 offset:1536
	ds_read_b32 v230, v115 offset:2048
	ds_read_b32 v231, v115 offset:2560
	ds_read_b32 v232, v115 offset:3072
	ds_read_b32 v233, v115 offset:3584
	s_waitcnt lgkmcnt(0)
	v_bfe_u32 v120, v226, 16, 1
	v_bfe_u32 v121, v227, 16, 1
	v_bfe_u32 v122, v228, 16, 1
	v_bfe_u32 v123, v229, 16, 1
	v_bfe_u32 v124, v230, 16, 1
	v_bfe_u32 v125, v231, 16, 1
	v_bfe_u32 v126, v232, 16, 1
	v_bfe_u32 v127, v233, 16, 1
	v_add3_u32 v226, v226, v120, s28
	v_add3_u32 v227, v227, v121, s28
	v_add3_u32 v228, v228, v122, s28
	v_add3_u32 v229, v229, v123, s28
	v_add3_u32 v230, v230, v124, s28
	v_add3_u32 v231, v231, v125, s28
	v_add3_u32 v232, v232, v126, s28
	v_add3_u32 v233, v233, v127, s28
	v_perm_b32 v242, v227, v226, s29
	v_perm_b32 v243, v229, v228, s29
	v_perm_b32 v244, v231, v230, s29
	v_perm_b32 v245, v233, v232, s29
	s_nop 0
	global_store_dwordx4 v109, v[242:245], s[6:7]
	ds_read_b32 v226, v117
	ds_read_b32 v227, v117 offset:512
	ds_read_b32 v228, v117 offset:1024
	ds_read_b32 v229, v117 offset:1536
	ds_read_b32 v230, v117 offset:2048
	ds_read_b32 v231, v117 offset:2560
	ds_read_b32 v232, v117 offset:3072
	ds_read_b32 v233, v117 offset:3584
	s_waitcnt lgkmcnt(0)
	v_bfe_u32 v120, v226, 16, 1
	v_bfe_u32 v121, v227, 16, 1
	v_bfe_u32 v122, v228, 16, 1
	v_bfe_u32 v123, v229, 16, 1
	v_bfe_u32 v124, v230, 16, 1
	v_bfe_u32 v125, v231, 16, 1
	v_bfe_u32 v126, v232, 16, 1
	v_bfe_u32 v127, v233, 16, 1
	v_add3_u32 v226, v226, v120, s28
	v_add3_u32 v227, v227, v121, s28
	v_add3_u32 v228, v228, v122, s28
	v_add3_u32 v229, v229, v123, s28
	v_add3_u32 v230, v230, v124, s28
	v_add3_u32 v231, v231, v125, s28
	v_add3_u32 v232, v232, v126, s28
	v_add3_u32 v233, v233, v127, s28
	v_perm_b32 v242, v227, v226, s29
	v_perm_b32 v243, v229, v228, s29
	v_perm_b32 v244, v231, v230, s29
	v_perm_b32 v245, v233, v232, s29
	s_nop 0
	global_store_dwordx4 v110, v[242:245], s[6:7]
	ds_read_b32 v226, v119
	ds_read_b32 v227, v119 offset:512
	ds_read_b32 v228, v119 offset:1024
	ds_read_b32 v229, v119 offset:1536
	ds_read_b32 v230, v119 offset:2048
	ds_read_b32 v231, v119 offset:2560
	ds_read_b32 v232, v119 offset:3072
	ds_read_b32 v233, v119 offset:3584
	s_waitcnt lgkmcnt(0)
	v_bfe_u32 v120, v226, 16, 1
	v_bfe_u32 v121, v227, 16, 1
	v_bfe_u32 v122, v228, 16, 1
	v_bfe_u32 v123, v229, 16, 1
	v_bfe_u32 v124, v230, 16, 1
	v_bfe_u32 v125, v231, 16, 1
	v_bfe_u32 v126, v232, 16, 1
	v_bfe_u32 v127, v233, 16, 1
	v_add3_u32 v226, v226, v120, s28
	v_add3_u32 v227, v227, v121, s28
	v_add3_u32 v228, v228, v122, s28
	v_add3_u32 v229, v229, v123, s28
	v_add3_u32 v230, v230, v124, s28
	v_add3_u32 v231, v231, v125, s28
	v_add3_u32 v232, v232, v126, s28
	v_add3_u32 v233, v233, v127, s28
	v_perm_b32 v242, v227, v226, s29
	v_perm_b32 v243, v229, v228, s29
	v_perm_b32 v244, v231, v230, s29
	v_perm_b32 v245, v233, v232, s29
	s_nop 0
	global_store_dwordx4 v111, v[242:245], s[6:7]
	s_add_i32 s26, s23, 32
	s_add_i32 s27, s23, 48
	s_waitcnt vmcnt(16)
	v_mul_f32_e32 v144, v218, v144
	v_mul_f32_e32 v145, v218, v145
	v_mul_f32_e32 v146, v218, v146
	v_mul_f32_e32 v147, v218, v147
	ds_write_b128 v209, v[144:147]
	v_mul_f32_e32 v148, v219, v148
	v_mul_f32_e32 v149, v219, v149
	v_mul_f32_e32 v150, v219, v150
	v_mul_f32_e32 v151, v219, v151
	ds_write_b128 v209, v[148:151] offset:1024
	v_mul_f32_e32 v152, v220, v152
	v_mul_f32_e32 v153, v220, v153
	v_mul_f32_e32 v154, v220, v154
	v_mul_f32_e32 v155, v220, v155
	ds_write_b128 v209, v[152:155] offset:2048
	v_mul_f32_e32 v156, v221, v156
	v_mul_f32_e32 v157, v221, v157
	v_mul_f32_e32 v158, v221, v158
	v_mul_f32_e32 v159, v221, v159
	ds_write_b128 v209, v[156:159] offset:3072
	v_mul_f32_e32 v160, v222, v160
	v_mul_f32_e32 v161, v222, v161
	v_mul_f32_e32 v162, v222, v162
	v_mul_f32_e32 v163, v222, v163
	ds_write_b128 v209, v[160:163] offset:4096
	v_mul_f32_e32 v164, v223, v164
	v_mul_f32_e32 v165, v223, v165
	v_mul_f32_e32 v166, v223, v166
	v_mul_f32_e32 v167, v223, v167
	ds_write_b128 v209, v[164:167] offset:5120
	v_mul_f32_e32 v168, v224, v168
	v_mul_f32_e32 v169, v224, v169
	v_mul_f32_e32 v170, v224, v170
	v_mul_f32_e32 v171, v224, v171
	ds_write_b128 v209, v[168:171] offset:6144
	v_mul_f32_e32 v172, v225, v172
	v_mul_f32_e32 v173, v225, v173
	v_mul_f32_e32 v174, v225, v174
	v_mul_f32_e32 v175, v225, v175
	ds_write_b128 v209, v[172:175] offset:7168
	s_waitcnt lgkmcnt(0)
	s_barrier
; #define GAS __attribute__((address_space(1)))
; #define LAS __attribute__((address_space(3)))
; #define LDS_WAIT() asm volatile("s_waitcnt lgkmcnt(0)" ::: "memory")
; __device__ __forceinline__ unsigned pk2(float lo, float hi) { return f2bf(lo) | (f2bf(hi) << 16); }
; template <int MAP, bool KS, bool KPERM = false>
; __device__ __forceinline__ void p0_transpose_item(const float* W, int K, int Nsrc, int nblk, bf16* WT, const float* ksA, const float* ksB, int ksplit, LAS float* scr, int item, int lane) {
;     ...
;     for (int i = 0; i < 32; ++i) { const int kk = 2 * i + (lane >> 5); const int k = k0 + kk;
;         if (KS) v[i] *= (k < ksplit ? ksA[k] : ksB[k - ksplit]);
;         scr[kk * 33 + (lane & 31)] = v[i]; }
;     LDS_WAIT(); asm volatile("" ::: "memory");
;     const int c = lane & 7;
; #pragma unroll
;     for (int j = 0; j < 4; ++j) { const int n = (lane >> 3) + 8 * j; const LAS float* s = scr + (8 * c) * 33 + n;
;         v4u o; o.x = pk2(s[0 * 33], s[1 * 33]); o.y = pk2(s[2 * 33], s[3 * 33]); o.z = pk2(s[4 * 33], s[5 * 33]); o.w = pk2(s[6 * 33], s[7 * 33]);
;         *(GAS v4u*)(WT + (size_t)(n0 + n) * K + k0 + 8 * c) = o; }
	s_lshl_b32 s20, s27, 7
	s_cmp_lt_u32 s27, 40
	s_cselect_b32 s21, 0, 0x830
	s_cmp_lt_u32 s27, 72
	s_cselect_b32 s21, s21, 0xfffff030
	s_add_i32 s20, s20, s21
	s_lshl_b32 s20, s20, 2
	s_add_u32 s8, s16, s20
	s_addc_u32 s9, s17, 0
	global_load_dwordx4 v[144:147], v208, s[8:9]
	s_add_u32 s8, s8, 0x16280
	s_addc_u32 s9, s9, 0
	global_load_dwordx4 v[148:151], v208, s[8:9]
	s_add_u32 s8, s8, 0x16280
	s_addc_u32 s9, s9, 0
	global_load_dwordx4 v[152:155], v208, s[8:9]
	s_add_u32 s8, s8, 0x16280
	s_addc_u32 s9, s9, 0
	global_load_dwordx4 v[156:159], v208, s[8:9]
	s_add_u32 s8, s8, 0x16280
	s_addc_u32 s9, s9, 0
	global_load_dwordx4 v[160:163], v208, s[8:9]
	s_add_u32 s8, s8, 0x16280
	s_addc_u32 s9, s9, 0
	global_load_dwordx4 v[164:167], v208, s[8:9]
	s_add_u32 s8, s8, 0x16280
	s_addc_u32 s9, s9, 0
	global_load_dwordx4 v[168:171], v208, s[8:9]
	s_add_u32 s8, s8, 0x16280
	s_addc_u32 s9, s9, 0
	global_load_dwordx4 v[172:175], v208, s[8:9]
	s_mul_i32 s20, s26, 0x100000
	s_add_u32 s6, s18, s20
	s_addc_u32 s7, s19, 0
	s_cmp_lt_u32 s26, 16
	s_cselect_b32 s20, 1, 0
	s_sub_i32 s21, s26, 16
	s_bitcmp0_b32 s21, 2
	s_cselect_b32 s21, 1, 0
	s_cmp_lt_u32 s26, 40
	s_cselect_b32 s21, s21, 0
	s_or_b32 s20, s20, s21
	s_cmp_lg_u32 s20, 0
	s_cselect_b64 s[20:21], -1, 0
	v_cndmask_b32_e64 v108, v100, v104, s[20:21]
	v_cndmask_b32_e64 v109, v101, v105, s[20:21]
	v_cndmask_b32_e64 v110, v102, v106, s[20:21]
	v_cndmask_b32_e64 v111, v103, v107, s[20:21]
	ds_read_b32 v226, v112
	ds_read_b32 v227, v112 offset:512
	ds_read_b32 v228, v112 offset:1024
	ds_read_b32 v229, v112 offset:1536
	ds_read_b32 v230, v112 offset:2048
	ds_read_b32 v231, v112 offset:2560
	ds_read_b32 v232, v112 offset:3072
	ds_read_b32 v233, v112 offset:3584
	s_waitcnt lgkmcnt(0)
	v_bfe_u32 v120, v226, 16, 1
	v_bfe_u32 v121, v227, 16, 1
	v_bfe_u32 v122, v228, 16, 1
	v_bfe_u32 v123, v229, 16, 1
	v_bfe_u32 v124, v230, 16, 1
	v_bfe_u32 v125, v231, 16, 1
	v_bfe_u32 v126, v232, 16, 1
	v_bfe_u32 v127, v233, 16, 1
	v_add3_u32 v226, v226, v120, s28
	v_add3_u32 v227, v227, v121, s28
	v_add3_u32 v228, v228, v122, s28
	v_add3_u32 v229, v229, v123, s28
	v_add3_u32 v230, v230, v124, s28
	v_add3_u32 v231, v231, v125, s28
	v_add3_u32 v232, v232, v126, s28
	v_add3_u32 v233, v233, v127, s28
	v_perm_b32 v242, v227, v226, s29
	v_perm_b32 v243, v229, v228, s29
	v_perm_b32 v244, v231, v230, s29
	v_perm_b32 v245, v233, v232, s29
	s_nop 0
	global_store_dwordx4 v108, v[242:245], s[6:7]
	ds_read_b32 v226, v114
	ds_read_b32 v227, v114 offset:512
	ds_read_b32 v228, v114 offset:1024
	ds_read_b32 v229, v114 offset:1536
	ds_read_b32 v230, v114 offset:2048
	ds_read_b32 v231, v114 offset:2560
	ds_read_b32 v232, v114 offset:3072
	ds_read_b32 v233, v114 offset:3584
	s_waitcnt lgkmcnt(0)
	v_bfe_u32 v120, v226, 16, 1
	v_bfe_u32 v121, v227, 16, 1
	v_bfe_u32 v122, v228, 16, 1
	v_bfe_u32 v123, v229, 16, 1
	v_bfe_u32 v124, v230, 16, 1
	v_bfe_u32 v125, v231, 16, 1
	v_bfe_u32 v126, v232, 16, 1
	v_bfe_u32 v127, v233, 16, 1
	v_add3_u32 v226, v226, v120, s28
	v_add3_u32 v227, v227, v121, s28
	v_add3_u32 v228, v228, v122, s28
	v_add3_u32 v229, v229, v123, s28
	v_add3_u32 v230, v230, v124, s28
	v_add3_u32 v231, v231, v125, s28
	v_add3_u32 v232, v232, v126, s28
	v_add3_u32 v233, v233, v127, s28
	v_perm_b32 v242, v227, v226, s29
	v_perm_b32 v243, v229, v228, s29
	v_perm_b32 v244, v231, v230, s29
	v_perm_b32 v245, v233, v232, s29
	s_nop 0
	global_store_dwordx4 v109, v[242:245], s[6:7]
	ds_read_b32 v226, v116
	ds_read_b32 v227, v116 offset:512
	ds_read_b32 v228, v116 offset:1024
	ds_read_b32 v229, v116 offset:1536
	ds_read_b32 v230, v116 offset:2048
	ds_read_b32 v231, v116 offset:2560
	ds_read_b32 v232, v116 offset:3072
	ds_read_b32 v233, v116 offset:3584
	s_waitcnt lgkmcnt(0)
	v_bfe_u32 v120, v226, 16, 1
	v_bfe_u32 v121, v227, 16, 1
	v_bfe_u32 v122, v228, 16, 1
	v_bfe_u32 v123, v229, 16, 1
	v_bfe_u32 v124, v230, 16, 1
	v_bfe_u32 v125, v231, 16, 1
	v_bfe_u32 v126, v232, 16, 1
	v_bfe_u32 v127, v233, 16, 1
	v_add3_u32 v226, v226, v120, s28
	v_add3_u32 v227, v227, v121, s28
	v_add3_u32 v228, v228, v122, s28
	v_add3_u32 v229, v229, v123, s28
	v_add3_u32 v230, v230, v124, s28
	v_add3_u32 v231, v231, v125, s28
	v_add3_u32 v232, v232, v126, s28
	v_add3_u32 v233, v233, v127, s28
	v_perm_b32 v242, v227, v226, s29
	v_perm_b32 v243, v229, v228, s29
	v_perm_b32 v244, v231, v230, s29
	v_perm_b32 v245, v233, v232, s29
	s_nop 0
	global_store_dwordx4 v110, v[242:245], s[6:7]
	ds_read_b32 v226, v118
	ds_read_b32 v227, v118 offset:512
	ds_read_b32 v228, v118 offset:1024
	ds_read_b32 v229, v118 offset:1536
	ds_read_b32 v230, v118 offset:2048
	ds_read_b32 v231, v118 offset:2560
	ds_read_b32 v232, v118 offset:3072
	ds_read_b32 v233, v118 offset:3584
	s_waitcnt lgkmcnt(0)
	v_bfe_u32 v120, v226, 16, 1
	v_bfe_u32 v121, v227, 16, 1
	v_bfe_u32 v122, v228, 16, 1
	v_bfe_u32 v123, v229, 16, 1
	v_bfe_u32 v124, v230, 16, 1
	v_bfe_u32 v125, v231, 16, 1
	v_bfe_u32 v126, v232, 16, 1
	v_bfe_u32 v127, v233, 16, 1
	v_add3_u32 v226, v226, v120, s28
	v_add3_u32 v227, v227, v121, s28
	v_add3_u32 v228, v228, v122, s28
	v_add3_u32 v229, v229, v123, s28
	v_add3_u32 v230, v230, v124, s28
	v_add3_u32 v231, v231, v125, s28
	v_add3_u32 v232, v232, v126, s28
	v_add3_u32 v233, v233, v127, s28
	v_perm_b32 v242, v227, v226, s29
	v_perm_b32 v243, v229, v228, s29
	v_perm_b32 v244, v231, v230, s29
	v_perm_b32 v245, v233, v232, s29
	s_nop 0
	global_store_dwordx4 v111, v[242:245], s[6:7]
	s_add_i32 s26, s23, 40
	s_add_i32 s27, s23, 56
	s_waitcnt vmcnt(16)
	v_mul_f32_e32 v176, v218, v176
	v_mul_f32_e32 v177, v218, v177
	v_mul_f32_e32 v178, v218, v178
	v_mul_f32_e32 v179, v218, v179
	ds_write_b128 v210, v[176:179]
	v_mul_f32_e32 v180, v219, v180
	v_mul_f32_e32 v181, v219, v181
	v_mul_f32_e32 v182, v219, v182
	v_mul_f32_e32 v183, v219, v183
	ds_write_b128 v210, v[180:183] offset:1024
	v_mul_f32_e32 v184, v220, v184
	v_mul_f32_e32 v185, v220, v185
	v_mul_f32_e32 v186, v220, v186
	v_mul_f32_e32 v187, v220, v187
	ds_write_b128 v210, v[184:187] offset:2048
	v_mul_f32_e32 v188, v221, v188
	v_mul_f32_e32 v189, v221, v189
	v_mul_f32_e32 v190, v221, v190
	v_mul_f32_e32 v191, v221, v191
	ds_write_b128 v210, v[188:191] offset:3072
	v_mul_f32_e32 v192, v222, v192
	v_mul_f32_e32 v193, v222, v193
	v_mul_f32_e32 v194, v222, v194
	v_mul_f32_e32 v195, v222, v195
	ds_write_b128 v210, v[192:195] offset:4096
	v_mul_f32_e32 v196, v223, v196
	v_mul_f32_e32 v197, v223, v197
	v_mul_f32_e32 v198, v223, v198
	v_mul_f32_e32 v199, v223, v199
	ds_write_b128 v210, v[196:199] offset:5120
	v_mul_f32_e32 v200, v224, v200
	v_mul_f32_e32 v201, v224, v201
	v_mul_f32_e32 v202, v224, v202
	v_mul_f32_e32 v203, v224, v203
	ds_write_b128 v210, v[200:203] offset:6144
	v_mul_f32_e32 v204, v225, v204
	v_mul_f32_e32 v205, v225, v205
	v_mul_f32_e32 v206, v225, v206
	v_mul_f32_e32 v207, v225, v207
	ds_write_b128 v210, v[204:207] offset:7168
	s_waitcnt lgkmcnt(0)
	s_barrier
; #define GAS __attribute__((address_space(1)))
; #define LAS __attribute__((address_space(3)))
; #define LDS_WAIT() asm volatile("s_waitcnt lgkmcnt(0)" ::: "memory")
; __device__ __forceinline__ unsigned pk2(float lo, float hi) { return f2bf(lo) | (f2bf(hi) << 16); }
; template <int MAP, bool KS, bool KPERM = false>
; __device__ __forceinline__ void p0_transpose_item(const float* W, int K, int Nsrc, int nblk, bf16* WT, const float* ksA, const float* ksB, int ksplit, LAS float* scr, int item, int lane) {
;     ...
;     for (int i = 0; i < 32; ++i) { const int kk = 2 * i + (lane >> 5); const int k = k0 + kk;
;         if (KS) v[i] *= (k < ksplit ? ksA[k] : ksB[k - ksplit]);
;         scr[kk * 33 + (lane & 31)] = v[i]; }
;     LDS_WAIT(); asm volatile("" ::: "memory");
;     const int c = lane & 7;
; #pragma unroll
;     for (int j = 0; j < 4; ++j) { const int n = (lane >> 3) + 8 * j; const LAS float* s = scr + (8 * c) * 33 + n;
;         v4u o; o.x = pk2(s[0 * 33], s[1 * 33]); o.y = pk2(s[2 * 33], s[3 * 33]); o.z = pk2(s[4 * 33], s[5 * 33]); o.w = pk2(s[6 * 33], s[7 * 33]);
;         *(GAS v4u*)(WT + (size_t)(n0 + n) * K + k0 + 8 * c) = o; }
	s_lshl_b32 s20, s27, 7
	s_cmp_lt_u32 s27, 40
	s_cselect_b32 s21, 0, 0x830
	s_cmp_lt_u32 s27, 72
	s_cselect_b32 s21, s21, 0xfffff030
	s_add_i32 s20, s20, s21
	s_lshl_b32 s20, s20, 2
	s_add_u32 s8, s16, s20
	s_addc_u32 s9, s17, 0
	global_load_dwordx4 v[176:179], v208, s[8:9]
	s_add_u32 s8, s8, 0x16280
	s_addc_u32 s9, s9, 0
	global_load_dwordx4 v[180:183], v208, s[8:9]
	s_add_u32 s8, s8, 0x16280
	s_addc_u32 s9, s9, 0
	global_load_dwordx4 v[184:187], v208, s[8:9]
	s_add_u32 s8, s8, 0x16280
	s_addc_u32 s9, s9, 0
	global_load_dwordx4 v[188:191], v208, s[8:9]
	s_add_u32 s8, s8, 0x16280
	s_addc_u32 s9, s9, 0
	global_load_dwordx4 v[192:195], v208, s[8:9]
	s_add_u32 s8, s8, 0x16280
	s_addc_u32 s9, s9, 0
	global_load_dwordx4 v[196:199], v208, s[8:9]
	s_add_u32 s8, s8, 0x16280
	s_addc_u32 s9, s9, 0
	global_load_dwordx4 v[200:203], v208, s[8:9]
	s_add_u32 s8, s8, 0x16280
	s_addc_u32 s9, s9, 0
	global_load_dwordx4 v[204:207], v208, s[8:9]
	s_mul_i32 s20, s26, 0x100000
	s_add_u32 s6, s18, s20
	s_addc_u32 s7, s19, 0
	s_cmp_lt_u32 s26, 16
	s_cselect_b32 s20, 1, 0
	s_sub_i32 s21, s26, 16
	s_bitcmp0_b32 s21, 2
	s_cselect_b32 s21, 1, 0
	s_cmp_lt_u32 s26, 40
	s_cselect_b32 s21, s21, 0
	s_or_b32 s20, s20, s21
	s_cmp_lg_u32 s20, 0
	s_cselect_b64 s[20:21], -1, 0
	v_cndmask_b32_e64 v108, v100, v104, s[20:21]
	v_cndmask_b32_e64 v109, v101, v105, s[20:21]
	v_cndmask_b32_e64 v110, v102, v106, s[20:21]
	v_cndmask_b32_e64 v111, v103, v107, s[20:21]
	ds_read_b32 v226, v113
	ds_read_b32 v227, v113 offset:512
	ds_read_b32 v228, v113 offset:1024
	ds_read_b32 v229, v113 offset:1536
	ds_read_b32 v230, v113 offset:2048
	ds_read_b32 v231, v113 offset:2560
	ds_read_b32 v232, v113 offset:3072
	ds_read_b32 v233, v113 offset:3584
	s_waitcnt lgkmcnt(0)
	v_bfe_u32 v120, v226, 16, 1
	v_bfe_u32 v121, v227, 16, 1
	v_bfe_u32 v122, v228, 16, 1
	v_bfe_u32 v123, v229, 16, 1
	v_bfe_u32 v124, v230, 16, 1
	v_bfe_u32 v125, v231, 16, 1
	v_bfe_u32 v126, v232, 16, 1
	v_bfe_u32 v127, v233, 16, 1
	v_add3_u32 v226, v226, v120, s28
	v_add3_u32 v227, v227, v121, s28
	v_add3_u32 v228, v228, v122, s28
	v_add3_u32 v229, v229, v123, s28
	v_add3_u32 v230, v230, v124, s28
	v_add3_u32 v231, v231, v125, s28
	v_add3_u32 v232, v232, v126, s28
	v_add3_u32 v233, v233, v127, s28
	v_perm_b32 v242, v227, v226, s29
	v_perm_b32 v243, v229, v228, s29
	v_perm_b32 v244, v231, v230, s29
	v_perm_b32 v245, v233, v232, s29
	s_nop 0
	global_store_dwordx4 v108, v[242:245], s[6:7]
	ds_read_b32 v226, v115
	ds_read_b32 v227, v115 offset:512
	ds_read_b32 v228, v115 offset:1024
	ds_read_b32 v229, v115 offset:1536
	ds_read_b32 v230, v115 offset:2048
	ds_read_b32 v231, v115 offset:2560
	ds_read_b32 v232, v115 offset:3072
	ds_read_b32 v233, v115 offset:3584
	s_waitcnt lgkmcnt(0)
	v_bfe_u32 v120, v226, 16, 1
	v_bfe_u32 v121, v227, 16, 1
	v_bfe_u32 v122, v228, 16, 1
	v_bfe_u32 v123, v229, 16, 1
	v_bfe_u32 v124, v230, 16, 1
	v_bfe_u32 v125, v231, 16, 1
	v_bfe_u32 v126, v232, 16, 1
	v_bfe_u32 v127, v233, 16, 1
	v_add3_u32 v226, v226, v120, s28
	v_add3_u32 v227, v227, v121, s28
	v_add3_u32 v228, v228, v122, s28
	v_add3_u32 v229, v229, v123, s28
	v_add3_u32 v230, v230, v124, s28
	v_add3_u32 v231, v231, v125, s28
	v_add3_u32 v232, v232, v126, s28
	v_add3_u32 v233, v233, v127, s28
	v_perm_b32 v242, v227, v226, s29
	v_perm_b32 v243, v229, v228, s29
	v_perm_b32 v244, v231, v230, s29
	v_perm_b32 v245, v233, v232, s29
	s_nop 0
	global_store_dwordx4 v109, v[242:245], s[6:7]
	ds_read_b32 v226, v117
	ds_read_b32 v227, v117 offset:512
	ds_read_b32 v228, v117 offset:1024
	ds_read_b32 v229, v117 offset:1536
	ds_read_b32 v230, v117 offset:2048
	ds_read_b32 v231, v117 offset:2560
	ds_read_b32 v232, v117 offset:3072
	ds_read_b32 v233, v117 offset:3584
	s_waitcnt lgkmcnt(0)
	v_bfe_u32 v120, v226, 16, 1
	v_bfe_u32 v121, v227, 16, 1
	v_bfe_u32 v122, v228, 16, 1
	v_bfe_u32 v123, v229, 16, 1
	v_bfe_u32 v124, v230, 16, 1
	v_bfe_u32 v125, v231, 16, 1
	v_bfe_u32 v126, v232, 16, 1
	v_bfe_u32 v127, v233, 16, 1
	v_add3_u32 v226, v226, v120, s28
	v_add3_u32 v227, v227, v121, s28
	v_add3_u32 v228, v228, v122, s28
	v_add3_u32 v229, v229, v123, s28
	v_add3_u32 v230, v230, v124, s28
	v_add3_u32 v231, v231, v125, s28
	v_add3_u32 v232, v232, v126, s28
	v_add3_u32 v233, v233, v127, s28
	v_perm_b32 v242, v227, v226, s29
	v_perm_b32 v243, v229, v228, s29
	v_perm_b32 v244, v231, v230, s29
	v_perm_b32 v245, v233, v232, s29
	s_nop 0
	global_store_dwordx4 v110, v[242:245], s[6:7]
	ds_read_b32 v226, v119
	ds_read_b32 v227, v119 offset:512
	ds_read_b32 v228, v119 offset:1024
	ds_read_b32 v229, v119 offset:1536
	ds_read_b32 v230, v119 offset:2048
	ds_read_b32 v231, v119 offset:2560
	ds_read_b32 v232, v119 offset:3072
	ds_read_b32 v233, v119 offset:3584
	s_waitcnt lgkmcnt(0)
	v_bfe_u32 v120, v226, 16, 1
	v_bfe_u32 v121, v227, 16, 1
	v_bfe_u32 v122, v228, 16, 1
	v_bfe_u32 v123, v229, 16, 1
	v_bfe_u32 v124, v230, 16, 1
	v_bfe_u32 v125, v231, 16, 1
	v_bfe_u32 v126, v232, 16, 1
	v_bfe_u32 v127, v233, 16, 1
	v_add3_u32 v226, v226, v120, s28
	v_add3_u32 v227, v227, v121, s28
	v_add3_u32 v228, v228, v122, s28
	v_add3_u32 v229, v229, v123, s28
	v_add3_u32 v230, v230, v124, s28
	v_add3_u32 v231, v231, v125, s28
	v_add3_u32 v232, v232, v126, s28
	v_add3_u32 v233, v233, v127, s28
	v_perm_b32 v242, v227, v226, s29
	v_perm_b32 v243, v229, v228, s29
	v_perm_b32 v244, v231, v230, s29
	v_perm_b32 v245, v233, v232, s29
	s_nop 0
	global_store_dwordx4 v111, v[242:245], s[6:7]
	s_add_i32 s26, s23, 48
	s_add_i32 s27, s23, 64
	s_waitcnt vmcnt(16)
	v_mul_f32_e32 v144, v218, v144
	v_mul_f32_e32 v145, v218, v145
	v_mul_f32_e32 v146, v218, v146
	v_mul_f32_e32 v147, v218, v147
	ds_write_b128 v209, v[144:147]
	v_mul_f32_e32 v148, v219, v148
	v_mul_f32_e32 v149, v219, v149
	v_mul_f32_e32 v150, v219, v150
	v_mul_f32_e32 v151, v219, v151
	ds_write_b128 v209, v[148:151] offset:1024
	v_mul_f32_e32 v152, v220, v152
	v_mul_f32_e32 v153, v220, v153
	v_mul_f32_e32 v154, v220, v154
	v_mul_f32_e32 v155, v220, v155
	ds_write_b128 v209, v[152:155] offset:2048
	v_mul_f32_e32 v156, v221, v156
	v_mul_f32_e32 v157, v221, v157
	v_mul_f32_e32 v158, v221, v158
	v_mul_f32_e32 v159, v221, v159
	ds_write_b128 v209, v[156:159] offset:3072
	v_mul_f32_e32 v160, v222, v160
	v_mul_f32_e32 v161, v222, v161
	v_mul_f32_e32 v162, v222, v162
	v_mul_f32_e32 v163, v222, v163
	ds_write_b128 v209, v[160:163] offset:4096
	v_mul_f32_e32 v164, v223, v164
	v_mul_f32_e32 v165, v223, v165
	v_mul_f32_e32 v166, v223, v166
	v_mul_f32_e32 v167, v223, v167
	ds_write_b128 v209, v[164:167] offset:5120
	v_mul_f32_e32 v168, v224, v168
	v_mul_f32_e32 v169, v224, v169
	v_mul_f32_e32 v170, v224, v170
	v_mul_f32_e32 v171, v224, v171
	ds_write_b128 v209, v[168:171] offset:6144
	v_mul_f32_e32 v172, v225, v172
	v_mul_f32_e32 v173, v225, v173
	v_mul_f32_e32 v174, v225, v174
	v_mul_f32_e32 v175, v225, v175
	ds_write_b128 v209, v[172:175] offset:7168
	s_waitcnt lgkmcnt(0)
	s_barrier
; #define GAS __attribute__((address_space(1)))
; #define LAS __attribute__((address_space(3)))
; #define LDS_WAIT() asm volatile("s_waitcnt lgkmcnt(0)" ::: "memory")
; __device__ __forceinline__ unsigned pk2(float lo, float hi) { return f2bf(lo) | (f2bf(hi) << 16); }
; template <int MAP, bool KS, bool KPERM = false>
; __device__ __forceinline__ void p0_transpose_item(const float* W, int K, int Nsrc, int nblk, bf16* WT, const float* ksA, const float* ksB, int ksplit, LAS float* scr, int item, int lane) {
;     ...
;     for (int i = 0; i < 32; ++i) { const int kk = 2 * i + (lane >> 5); const int k = k0 + kk;
;         if (KS) v[i] *= (k < ksplit ? ksA[k] : ksB[k - ksplit]);
;         scr[kk * 33 + (lane & 31)] = v[i]; }
;     LDS_WAIT(); asm volatile("" ::: "memory");
;     const int c = lane & 7;
; #pragma unroll
;     for (int j = 0; j < 4; ++j) { const int n = (lane >> 3) + 8 * j; const LAS float* s = scr + (8 * c) * 33 + n;
;         v4u o; o.x = pk2(s[0 * 33], s[1 * 33]); o.y = pk2(s[2 * 33], s[3 * 33]); o.z = pk2(s[4 * 33], s[5 * 33]); o.w = pk2(s[6 * 33], s[7 * 33]);
;         *(GAS v4u*)(WT + (size_t)(n0 + n) * K + k0 + 8 * c) = o; }
	s_lshl_b32 s20, s27, 7
	s_cmp_lt_u32 s27, 40
	s_cselect_b32 s21, 0, 0x830
	s_cmp_lt_u32 s27, 72
	s_cselect_b32 s21, s21, 0xfffff030
	s_add_i32 s20, s20, s21
	s_lshl_b32 s20, s20, 2
	s_add_u32 s8, s16, s20
	s_addc_u32 s9, s17, 0
	global_load_dwordx4 v[144:147], v208, s[8:9]
	s_add_u32 s8, s8, 0x16280
	s_addc_u32 s9, s9, 0
	global_load_dwordx4 v[148:151], v208, s[8:9]
	s_add_u32 s8, s8, 0x16280
	s_addc_u32 s9, s9, 0
	global_load_dwordx4 v[152:155], v208, s[8:9]
	s_add_u32 s8, s8, 0x16280
	s_addc_u32 s9, s9, 0
	global_load_dwordx4 v[156:159], v208, s[8:9]
	s_add_u32 s8, s8, 0x16280
	s_addc_u32 s9, s9, 0
	global_load_dwordx4 v[160:163], v208, s[8:9]
	s_add_u32 s8, s8, 0x16280
	s_addc_u32 s9, s9, 0
	global_load_dwordx4 v[164:167], v208, s[8:9]
	s_add_u32 s8, s8, 0x16280
	s_addc_u32 s9, s9, 0
	global_load_dwordx4 v[168:171], v208, s[8:9]
	s_add_u32 s8, s8, 0x16280
	s_addc_u32 s9, s9, 0
	global_load_dwordx4 v[172:175], v208, s[8:9]
	s_mul_i32 s20, s26, 0x100000
	s_add_u32 s6, s18, s20
	s_addc_u32 s7, s19, 0
	s_cmp_lt_u32 s26, 16
	s_cselect_b32 s20, 1, 0
	s_sub_i32 s21, s26, 16
	s_bitcmp0_b32 s21, 2
	s_cselect_b32 s21, 1, 0
	s_cmp_lt_u32 s26, 40
	s_cselect_b32 s21, s21, 0
	s_or_b32 s20, s20, s21
	s_cmp_lg_u32 s20, 0
	s_cselect_b64 s[20:21], -1, 0
	v_cndmask_b32_e64 v108, v100, v104, s[20:21]
	v_cndmask_b32_e64 v109, v101, v105, s[20:21]
	v_cndmask_b32_e64 v110, v102, v106, s[20:21]
	v_cndmask_b32_e64 v111, v103, v107, s[20:21]
	ds_read_b32 v226, v112
	ds_read_b32 v227, v112 offset:512
	ds_read_b32 v228, v112 offset:1024
	ds_read_b32 v229, v112 offset:1536
	ds_read_b32 v230, v112 offset:2048
	ds_read_b32 v231, v112 offset:2560
	ds_read_b32 v232, v112 offset:3072
	ds_read_b32 v233, v112 offset:3584
	s_waitcnt lgkmcnt(0)
	v_bfe_u32 v120, v226, 16, 1
	v_bfe_u32 v121, v227, 16, 1
	v_bfe_u32 v122, v228, 16, 1
	v_bfe_u32 v123, v229, 16, 1
	v_bfe_u32 v124, v230, 16, 1
	v_bfe_u32 v125, v231, 16, 1
	v_bfe_u32 v126, v232, 16, 1
	v_bfe_u32 v127, v233, 16, 1
	v_add3_u32 v226, v226, v120, s28
	v_add3_u32 v227, v227, v121, s28
	v_add3_u32 v228, v228, v122, s28
	v_add3_u32 v229, v229, v123, s28
	v_add3_u32 v230, v230, v124, s28
	v_add3_u32 v231, v231, v125, s28
	v_add3_u32 v232, v232, v126, s28
	v_add3_u32 v233, v233, v127, s28
	v_perm_b32 v242, v227, v226, s29
	v_perm_b32 v243, v229, v228, s29
	v_perm_b32 v244, v231, v230, s29
	v_perm_b32 v245, v233, v232, s29
	s_nop 0
	global_store_dwordx4 v108, v[242:245], s[6:7]
	ds_read_b32 v226, v114
	ds_read_b32 v227, v114 offset:512
	ds_read_b32 v228, v114 offset:1024
	ds_read_b32 v229, v114 offset:1536
	ds_read_b32 v230, v114 offset:2048
	ds_read_b32 v231, v114 offset:2560
	ds_read_b32 v232, v114 offset:3072
	ds_read_b32 v233, v114 offset:3584
	s_waitcnt lgkmcnt(0)
	v_bfe_u32 v120, v226, 16, 1
	v_bfe_u32 v121, v227, 16, 1
	v_bfe_u32 v122, v228, 16, 1
	v_bfe_u32 v123, v229, 16, 1
	v_bfe_u32 v124, v230, 16, 1
	v_bfe_u32 v125, v231, 16, 1
	v_bfe_u32 v126, v232, 16, 1
	v_bfe_u32 v127, v233, 16, 1
	v_add3_u32 v226, v226, v120, s28
	v_add3_u32 v227, v227, v121, s28
	v_add3_u32 v228, v228, v122, s28
	v_add3_u32 v229, v229, v123, s28
	v_add3_u32 v230, v230, v124, s28
	v_add3_u32 v231, v231, v125, s28
	v_add3_u32 v232, v232, v126, s28
	v_add3_u32 v233, v233, v127, s28
	v_perm_b32 v242, v227, v226, s29
	v_perm_b32 v243, v229, v228, s29
	v_perm_b32 v244, v231, v230, s29
	v_perm_b32 v245, v233, v232, s29
	s_nop 0
	global_store_dwordx4 v109, v[242:245], s[6:7]
	ds_read_b32 v226, v116
	ds_read_b32 v227, v116 offset:512
	ds_read_b32 v228, v116 offset:1024
	ds_read_b32 v229, v116 offset:1536
	ds_read_b32 v230, v116 offset:2048
	ds_read_b32 v231, v116 offset:2560
	ds_read_b32 v232, v116 offset:3072
	ds_read_b32 v233, v116 offset:3584
	s_waitcnt lgkmcnt(0)
	v_bfe_u32 v120, v226, 16, 1
	v_bfe_u32 v121, v227, 16, 1
	v_bfe_u32 v122, v228, 16, 1
	v_bfe_u32 v123, v229, 16, 1
	v_bfe_u32 v124, v230, 16, 1
	v_bfe_u32 v125, v231, 16, 1
	v_bfe_u32 v126, v232, 16, 1
	v_bfe_u32 v127, v233, 16, 1
	v_add3_u32 v226, v226, v120, s28
	v_add3_u32 v227, v227, v121, s28
	v_add3_u32 v228, v228, v122, s28
	v_add3_u32 v229, v229, v123, s28
	v_add3_u32 v230, v230, v124, s28
	v_add3_u32 v231, v231, v125, s28
	v_add3_u32 v232, v232, v126, s28
	v_add3_u32 v233, v233, v127, s28
	v_perm_b32 v242, v227, v226, s29
	v_perm_b32 v243, v229, v228, s29
	v_perm_b32 v244, v231, v230, s29
	v_perm_b32 v245, v233, v232, s29
	s_nop 0
	global_store_dwordx4 v110, v[242:245], s[6:7]
	ds_read_b32 v226, v118
	ds_read_b32 v227, v118 offset:512
	ds_read_b32 v228, v118 offset:1024
	ds_read_b32 v229, v118 offset:1536
	ds_read_b32 v230, v118 offset:2048
	ds_read_b32 v231, v118 offset:2560
	ds_read_b32 v232, v118 offset:3072
	ds_read_b32 v233, v118 offset:3584
	s_waitcnt lgkmcnt(0)
	v_bfe_u32 v120, v226, 16, 1
	v_bfe_u32 v121, v227, 16, 1
	v_bfe_u32 v122, v228, 16, 1
	v_bfe_u32 v123, v229, 16, 1
	v_bfe_u32 v124, v230, 16, 1
	v_bfe_u32 v125, v231, 16, 1
	v_bfe_u32 v126, v232, 16, 1
	v_bfe_u32 v127, v233, 16, 1
	v_add3_u32 v226, v226, v120, s28
	v_add3_u32 v227, v227, v121, s28
	v_add3_u32 v228, v228, v122, s28
	v_add3_u32 v229, v229, v123, s28
	v_add3_u32 v230, v230, v124, s28
	v_add3_u32 v231, v231, v125, s28
	v_add3_u32 v232, v232, v126, s28
	v_add3_u32 v233, v233, v127, s28
	v_perm_b32 v242, v227, v226, s29
	v_perm_b32 v243, v229, v228, s29
	v_perm_b32 v244, v231, v230, s29
	v_perm_b32 v245, v233, v232, s29
	s_nop 0
	global_store_dwordx4 v111, v[242:245], s[6:7]
	s_add_i32 s26, s23, 56
	s_add_i32 s27, s23, 72
	s_waitcnt vmcnt(16)
	v_mul_f32_e32 v176, v218, v176
	v_mul_f32_e32 v177, v218, v177
	v_mul_f32_e32 v178, v218, v178
	v_mul_f32_e32 v179, v218, v179
	ds_write_b128 v210, v[176:179]
	v_mul_f32_e32 v180, v219, v180
	v_mul_f32_e32 v181, v219, v181
	v_mul_f32_e32 v182, v219, v182
	v_mul_f32_e32 v183, v219, v183
	ds_write_b128 v210, v[180:183] offset:1024
	v_mul_f32_e32 v184, v220, v184
	v_mul_f32_e32 v185, v220, v185
	v_mul_f32_e32 v186, v220, v186
	v_mul_f32_e32 v187, v220, v187
	ds_write_b128 v210, v[184:187] offset:2048
	v_mul_f32_e32 v188, v221, v188
	v_mul_f32_e32 v189, v221, v189
	v_mul_f32_e32 v190, v221, v190
	v_mul_f32_e32 v191, v221, v191
	ds_write_b128 v210, v[188:191] offset:3072
	v_mul_f32_e32 v192, v222, v192
	v_mul_f32_e32 v193, v222, v193
	v_mul_f32_e32 v194, v222, v194
	v_mul_f32_e32 v195, v222, v195
	ds_write_b128 v210, v[192:195] offset:4096
	v_mul_f32_e32 v196, v223, v196
	v_mul_f32_e32 v197, v223, v197
	v_mul_f32_e32 v198, v223, v198
	v_mul_f32_e32 v199, v223, v199
	ds_write_b128 v210, v[196:199] offset:5120
	v_mul_f32_e32 v200, v224, v200
	v_mul_f32_e32 v201, v224, v201
	v_mul_f32_e32 v202, v224, v202
	v_mul_f32_e32 v203, v224, v203
	ds_write_b128 v210, v[200:203] offset:6144
	v_mul_f32_e32 v204, v225, v204
	v_mul_f32_e32 v205, v225, v205
	v_mul_f32_e32 v206, v225, v206
	v_mul_f32_e32 v207, v225, v207
	ds_write_b128 v210, v[204:207] offset:7168
	s_waitcnt lgkmcnt(0)
	s_barrier
; #define GAS __attribute__((address_space(1)))
; #define LAS __attribute__((address_space(3)))
; #define LDS_WAIT() asm volatile("s_waitcnt lgkmcnt(0)" ::: "memory")
; __device__ __forceinline__ unsigned pk2(float lo, float hi) { return f2bf(lo) | (f2bf(hi) << 16); }
; template <int MAP, bool KS, bool KPERM = false>
; __device__ __forceinline__ void p0_transpose_item(const float* W, int K, int Nsrc, int nblk, bf16* WT, const float* ksA, const float* ksB, int ksplit, LAS float* scr, int item, int lane) {
;     ...
;     for (int i = 0; i < 32; ++i) { const int kk = 2 * i + (lane >> 5); const int k = k0 + kk;
;         if (KS) v[i] *= (k < ksplit ? ksA[k] : ksB[k - ksplit]);
;         scr[kk * 33 + (lane & 31)] = v[i]; }
;     LDS_WAIT(); asm volatile("" ::: "memory");
;     const int c = lane & 7;
; #pragma unroll
;     for (int j = 0; j < 4; ++j) { const int n = (lane >> 3) + 8 * j; const LAS float* s = scr + (8 * c) * 33 + n;
;         v4u o; o.x = pk2(s[0 * 33], s[1 * 33]); o.y = pk2(s[2 * 33], s[3 * 33]); o.z = pk2(s[4 * 33], s[5 * 33]); o.w = pk2(s[6 * 33], s[7 * 33]);
;         *(GAS v4u*)(WT + (size_t)(n0 + n) * K + k0 + 8 * c) = o; }
	s_lshl_b32 s20, s27, 7
	s_cmp_lt_u32 s27, 40
	s_cselect_b32 s21, 0, 0x830
	s_cmp_lt_u32 s27, 72
	s_cselect_b32 s21, s21, 0xfffff030
	s_add_i32 s20, s20, s21
	s_lshl_b32 s20, s20, 2
	s_add_u32 s8, s16, s20
	s_addc_u32 s9, s17, 0
	global_load_dwordx4 v[176:179], v208, s[8:9]
	s_add_u32 s8, s8, 0x16280
	s_addc_u32 s9, s9, 0
	global_load_dwordx4 v[180:183], v208, s[8:9]
	s_add_u32 s8, s8, 0x16280
	s_addc_u32 s9, s9, 0
	global_load_dwordx4 v[184:187], v208, s[8:9]
	s_add_u32 s8, s8, 0x16280
	s_addc_u32 s9, s9, 0
	global_load_dwordx4 v[188:191], v208, s[8:9]
	s_add_u32 s8, s8, 0x16280
	s_addc_u32 s9, s9, 0
	global_load_dwordx4 v[192:195], v208, s[8:9]
	s_add_u32 s8, s8, 0x16280
	s_addc_u32 s9, s9, 0
	global_load_dwordx4 v[196:199], v208, s[8:9]
	s_add_u32 s8, s8, 0x16280
	s_addc_u32 s9, s9, 0
	global_load_dwordx4 v[200:203], v208, s[8:9]
	s_add_u32 s8, s8, 0x16280
	s_addc_u32 s9, s9, 0
	global_load_dwordx4 v[204:207], v208, s[8:9]
	s_mul_i32 s20, s26, 0x100000
	s_add_u32 s6, s18, s20
	s_addc_u32 s7, s19, 0
	s_cmp_lt_u32 s26, 16
	s_cselect_b32 s20, 1, 0
	s_sub_i32 s21, s26, 16
	s_bitcmp0_b32 s21, 2
	s_cselect_b32 s21, 1, 0
	s_cmp_lt_u32 s26, 40
	s_cselect_b32 s21, s21, 0
	s_or_b32 s20, s20, s21
	s_cmp_lg_u32 s20, 0
	s_cselect_b64 s[20:21], -1, 0
	v_cndmask_b32_e64 v108, v100, v104, s[20:21]
	v_cndmask_b32_e64 v109, v101, v105, s[20:21]
	v_cndmask_b32_e64 v110, v102, v106, s[20:21]
	v_cndmask_b32_e64 v111, v103, v107, s[20:21]
	ds_read_b32 v226, v113
	ds_read_b32 v227, v113 offset:512
	ds_read_b32 v228, v113 offset:1024
	ds_read_b32 v229, v113 offset:1536
	ds_read_b32 v230, v113 offset:2048
	ds_read_b32 v231, v113 offset:2560
	ds_read_b32 v232, v113 offset:3072
	ds_read_b32 v233, v113 offset:3584
	s_waitcnt lgkmcnt(0)
	v_bfe_u32 v120, v226, 16, 1
	v_bfe_u32 v121, v227, 16, 1
	v_bfe_u32 v122, v228, 16, 1
	v_bfe_u32 v123, v229, 16, 1
	v_bfe_u32 v124, v230, 16, 1
	v_bfe_u32 v125, v231, 16, 1
	v_bfe_u32 v126, v232, 16, 1
	v_bfe_u32 v127, v233, 16, 1
	v_add3_u32 v226, v226, v120, s28
	v_add3_u32 v227, v227, v121, s28
	v_add3_u32 v228, v228, v122, s28
	v_add3_u32 v229, v229, v123, s28
	v_add3_u32 v230, v230, v124, s28
	v_add3_u32 v231, v231, v125, s28
	v_add3_u32 v232, v232, v126, s28
	v_add3_u32 v233, v233, v127, s28
	v_perm_b32 v242, v227, v226, s29
	v_perm_b32 v243, v229, v228, s29
	v_perm_b32 v244, v231, v230, s29
	v_perm_b32 v245, v233, v232, s29
	s_nop 0
	global_store_dwordx4 v108, v[242:245], s[6:7]
	ds_read_b32 v226, v115
	ds_read_b32 v227, v115 offset:512
	ds_read_b32 v228, v115 offset:1024
	ds_read_b32 v229, v115 offset:1536
	ds_read_b32 v230, v115 offset:2048
	ds_read_b32 v231, v115 offset:2560
	ds_read_b32 v232, v115 offset:3072
	ds_read_b32 v233, v115 offset:3584
	s_waitcnt lgkmcnt(0)
	v_bfe_u32 v120, v226, 16, 1
	v_bfe_u32 v121, v227, 16, 1
	v_bfe_u32 v122, v228, 16, 1
	v_bfe_u32 v123, v229, 16, 1
	v_bfe_u32 v124, v230, 16, 1
	v_bfe_u32 v125, v231, 16, 1
	v_bfe_u32 v126, v232, 16, 1
	v_bfe_u32 v127, v233, 16, 1
	v_add3_u32 v226, v226, v120, s28
	v_add3_u32 v227, v227, v121, s28
	v_add3_u32 v228, v228, v122, s28
	v_add3_u32 v229, v229, v123, s28
	v_add3_u32 v230, v230, v124, s28
	v_add3_u32 v231, v231, v125, s28
	v_add3_u32 v232, v232, v126, s28
	v_add3_u32 v233, v233, v127, s28
	v_perm_b32 v242, v227, v226, s29
	v_perm_b32 v243, v229, v228, s29
	v_perm_b32 v244, v231, v230, s29
	v_perm_b32 v245, v233, v232, s29
	s_nop 0
	global_store_dwordx4 v109, v[242:245], s[6:7]
	ds_read_b32 v226, v117
	ds_read_b32 v227, v117 offset:512
	ds_read_b32 v228, v117 offset:1024
	ds_read_b32 v229, v117 offset:1536
	ds_read_b32 v230, v117 offset:2048
	ds_read_b32 v231, v117 offset:2560
	ds_read_b32 v232, v117 offset:3072
	ds_read_b32 v233, v117 offset:3584
	s_waitcnt lgkmcnt(0)
	v_bfe_u32 v120, v226, 16, 1
	v_bfe_u32 v121, v227, 16, 1
	v_bfe_u32 v122, v228, 16, 1
	v_bfe_u32 v123, v229, 16, 1
	v_bfe_u32 v124, v230, 16, 1
	v_bfe_u32 v125, v231, 16, 1
	v_bfe_u32 v126, v232, 16, 1
	v_bfe_u32 v127, v233, 16, 1
	v_add3_u32 v226, v226, v120, s28
	v_add3_u32 v227, v227, v121, s28
	v_add3_u32 v228, v228, v122, s28
	v_add3_u32 v229, v229, v123, s28
	v_add3_u32 v230, v230, v124, s28
	v_add3_u32 v231, v231, v125, s28
	v_add3_u32 v232, v232, v126, s28
	v_add3_u32 v233, v233, v127, s28
	v_perm_b32 v242, v227, v226, s29
	v_perm_b32 v243, v229, v228, s29
	v_perm_b32 v244, v231, v230, s29
	v_perm_b32 v245, v233, v232, s29
	s_nop 0
	global_store_dwordx4 v110, v[242:245], s[6:7]
	ds_read_b32 v226, v119
	ds_read_b32 v227, v119 offset:512
	ds_read_b32 v228, v119 offset:1024
	ds_read_b32 v229, v119 offset:1536
	ds_read_b32 v230, v119 offset:2048
	ds_read_b32 v231, v119 offset:2560
	ds_read_b32 v232, v119 offset:3072
	ds_read_b32 v233, v119 offset:3584
	s_waitcnt lgkmcnt(0)
	v_bfe_u32 v120, v226, 16, 1
	v_bfe_u32 v121, v227, 16, 1
	v_bfe_u32 v122, v228, 16, 1
	v_bfe_u32 v123, v229, 16, 1
	v_bfe_u32 v124, v230, 16, 1
	v_bfe_u32 v125, v231, 16, 1
	v_bfe_u32 v126, v232, 16, 1
	v_bfe_u32 v127, v233, 16, 1
	v_add3_u32 v226, v226, v120, s28
	v_add3_u32 v227, v227, v121, s28
	v_add3_u32 v228, v228, v122, s28
	v_add3_u32 v229, v229, v123, s28
	v_add3_u32 v230, v230, v124, s28
	v_add3_u32 v231, v231, v125, s28
	v_add3_u32 v232, v232, v126, s28
	v_add3_u32 v233, v233, v127, s28
	v_perm_b32 v242, v227, v226, s29
	v_perm_b32 v243, v229, v228, s29
	v_perm_b32 v244, v231, v230, s29
	v_perm_b32 v245, v233, v232, s29
	s_nop 0
	global_store_dwordx4 v111, v[242:245], s[6:7]
	s_add_i32 s26, s23, 64
	s_add_i32 s27, s23, 80
	s_waitcnt vmcnt(16)
	v_mul_f32_e32 v144, v218, v144
	v_mul_f32_e32 v145, v218, v145
	v_mul_f32_e32 v146, v218, v146
	v_mul_f32_e32 v147, v218, v147
	ds_write_b128 v209, v[144:147]
	v_mul_f32_e32 v148, v219, v148
	v_mul_f32_e32 v149, v219, v149
	v_mul_f32_e32 v150, v219, v150
	v_mul_f32_e32 v151, v219, v151
	ds_write_b128 v209, v[148:151] offset:1024
	v_mul_f32_e32 v152, v220, v152
	v_mul_f32_e32 v153, v220, v153
	v_mul_f32_e32 v154, v220, v154
	v_mul_f32_e32 v155, v220, v155
	ds_write_b128 v209, v[152:155] offset:2048
	v_mul_f32_e32 v156, v221, v156
	v_mul_f32_e32 v157, v221, v157
	v_mul_f32_e32 v158, v221, v158
	v_mul_f32_e32 v159, v221, v159
	ds_write_b128 v209, v[156:159] offset:3072
	v_mul_f32_e32 v160, v222, v160
	v_mul_f32_e32 v161, v222, v161
	v_mul_f32_e32 v162, v222, v162
	v_mul_f32_e32 v163, v222, v163
	ds_write_b128 v209, v[160:163] offset:4096
	v_mul_f32_e32 v164, v223, v164
	v_mul_f32_e32 v165, v223, v165
	v_mul_f32_e32 v166, v223, v166
	v_mul_f32_e32 v167, v223, v167
	ds_write_b128 v209, v[164:167] offset:5120
	v_mul_f32_e32 v168, v224, v168
	v_mul_f32_e32 v169, v224, v169
	v_mul_f32_e32 v170, v224, v170
	v_mul_f32_e32 v171, v224, v171
	ds_write_b128 v209, v[168:171] offset:6144
	v_mul_f32_e32 v172, v225, v172
	v_mul_f32_e32 v173, v225, v173
	v_mul_f32_e32 v174, v225, v174
	v_mul_f32_e32 v175, v225, v175
	ds_write_b128 v209, v[172:175] offset:7168
	s_waitcnt lgkmcnt(0)
	s_barrier
; #define GAS __attribute__((address_space(1)))
; #define LAS __attribute__((address_space(3)))
; #define LDS_WAIT() asm volatile("s_waitcnt lgkmcnt(0)" ::: "memory")
; __device__ __forceinline__ unsigned pk2(float lo, float hi) { return f2bf(lo) | (f2bf(hi) << 16); }
; template <int MAP, bool KS, bool KPERM = false>
; __device__ __forceinline__ void p0_transpose_item(const float* W, int K, int Nsrc, int nblk, bf16* WT, const float* ksA, const float* ksB, int ksplit, LAS float* scr, int item, int lane) {
;     ...
;     for (int i = 0; i < 32; ++i) { const int kk = 2 * i + (lane >> 5); const int k = k0 + kk;
;         if (KS) v[i] *= (k < ksplit ? ksA[k] : ksB[k - ksplit]);
;         scr[kk * 33 + (lane & 31)] = v[i]; }
;     LDS_WAIT(); asm volatile("" ::: "memory");
;     const int c = lane & 7;
; #pragma unroll
;     for (int j = 0; j < 4; ++j) { const int n = (lane >> 3) + 8 * j; const LAS float* s = scr + (8 * c) * 33 + n;
;         v4u o; o.x = pk2(s[0 * 33], s[1 * 33]); o.y = pk2(s[2 * 33], s[3 * 33]); o.z = pk2(s[4 * 33], s[5 * 33]); o.w = pk2(s[6 * 33], s[7 * 33]);
;         *(GAS v4u*)(WT + (size_t)(n0 + n) * K + k0 + 8 * c) = o; }
	s_lshl_b32 s20, s27, 7
	s_cmp_lt_u32 s27, 40
	s_cselect_b32 s21, 0, 0x830
	s_cmp_lt_u32 s27, 72
	s_cselect_b32 s21, s21, 0xfffff030
	s_add_i32 s20, s20, s21
	s_lshl_b32 s20, s20, 2
	s_add_u32 s8, s16, s20
	s_addc_u32 s9, s17, 0
	global_load_dwordx4 v[144:147], v208, s[8:9]
	s_add_u32 s8, s8, 0x16280
	s_addc_u32 s9, s9, 0
	global_load_dwordx4 v[148:151], v208, s[8:9]
	s_add_u32 s8, s8, 0x16280
	s_addc_u32 s9, s9, 0
	global_load_dwordx4 v[152:155], v208, s[8:9]
	s_add_u32 s8, s8, 0x16280
	s_addc_u32 s9, s9, 0
	global_load_dwordx4 v[156:159], v208, s[8:9]
	s_add_u32 s8, s8, 0x16280
	s_addc_u32 s9, s9, 0
	global_load_dwordx4 v[160:163], v208, s[8:9]
	s_add_u32 s8, s8, 0x16280
	s_addc_u32 s9, s9, 0
	global_load_dwordx4 v[164:167], v208, s[8:9]
	s_add_u32 s8, s8, 0x16280
	s_addc_u32 s9, s9, 0
	global_load_dwordx4 v[168:171], v208, s[8:9]
	s_add_u32 s8, s8, 0x16280
	s_addc_u32 s9, s9, 0
	global_load_dwordx4 v[172:175], v208, s[8:9]
	s_mul_i32 s20, s26, 0x100000
	s_add_u32 s6, s18, s20
	s_addc_u32 s7, s19, 0
	s_cmp_lt_u32 s26, 16
	s_cselect_b32 s20, 1, 0
	s_sub_i32 s21, s26, 16
	s_bitcmp0_b32 s21, 2
	s_cselect_b32 s21, 1, 0
	s_cmp_lt_u32 s26, 40
	s_cselect_b32 s21, s21, 0
	s_or_b32 s20, s20, s21
	s_cmp_lg_u32 s20, 0
	s_cselect_b64 s[20:21], -1, 0
	v_cndmask_b32_e64 v108, v100, v104, s[20:21]
	v_cndmask_b32_e64 v109, v101, v105, s[20:21]
	v_cndmask_b32_e64 v110, v102, v106, s[20:21]
	v_cndmask_b32_e64 v111, v103, v107, s[20:21]
	ds_read_b32 v226, v112
	ds_read_b32 v227, v112 offset:512
	ds_read_b32 v228, v112 offset:1024
	ds_read_b32 v229, v112 offset:1536
	ds_read_b32 v230, v112 offset:2048
	ds_read_b32 v231, v112 offset:2560
	ds_read_b32 v232, v112 offset:3072
	ds_read_b32 v233, v112 offset:3584
	s_waitcnt lgkmcnt(0)
	v_bfe_u32 v120, v226, 16, 1
	v_bfe_u32 v121, v227, 16, 1
	v_bfe_u32 v122, v228, 16, 1
	v_bfe_u32 v123, v229, 16, 1
	v_bfe_u32 v124, v230, 16, 1
	v_bfe_u32 v125, v231, 16, 1
	v_bfe_u32 v126, v232, 16, 1
	v_bfe_u32 v127, v233, 16, 1
	v_add3_u32 v226, v226, v120, s28
	v_add3_u32 v227, v227, v121, s28
	v_add3_u32 v228, v228, v122, s28
	v_add3_u32 v229, v229, v123, s28
	v_add3_u32 v230, v230, v124, s28
	v_add3_u32 v231, v231, v125, s28
	v_add3_u32 v232, v232, v126, s28
	v_add3_u32 v233, v233, v127, s28
	v_perm_b32 v242, v227, v226, s29
	v_perm_b32 v243, v229, v228, s29
	v_perm_b32 v244, v231, v230, s29
	v_perm_b32 v245, v233, v232, s29
	s_nop 0
	global_store_dwordx4 v108, v[242:245], s[6:7]
	ds_read_b32 v226, v114
	ds_read_b32 v227, v114 offset:512
	ds_read_b32 v228, v114 offset:1024
	ds_read_b32 v229, v114 offset:1536
	ds_read_b32 v230, v114 offset:2048
	ds_read_b32 v231, v114 offset:2560
	ds_read_b32 v232, v114 offset:3072
	ds_read_b32 v233, v114 offset:3584
	s_waitcnt lgkmcnt(0)
	v_bfe_u32 v120, v226, 16, 1
	v_bfe_u32 v121, v227, 16, 1
	v_bfe_u32 v122, v228, 16, 1
	v_bfe_u32 v123, v229, 16, 1
	v_bfe_u32 v124, v230, 16, 1
	v_bfe_u32 v125, v231, 16, 1
	v_bfe_u32 v126, v232, 16, 1
	v_bfe_u32 v127, v233, 16, 1
	v_add3_u32 v226, v226, v120, s28
	v_add3_u32 v227, v227, v121, s28
	v_add3_u32 v228, v228, v122, s28
	v_add3_u32 v229, v229, v123, s28
	v_add3_u32 v230, v230, v124, s28
	v_add3_u32 v231, v231, v125, s28
	v_add3_u32 v232, v232, v126, s28
	v_add3_u32 v233, v233, v127, s28
	v_perm_b32 v242, v227, v226, s29
	v_perm_b32 v243, v229, v228, s29
	v_perm_b32 v244, v231, v230, s29
	v_perm_b32 v245, v233, v232, s29
	s_nop 0
	global_store_dwordx4 v109, v[242:245], s[6:7]
	ds_read_b32 v226, v116
	ds_read_b32 v227, v116 offset:512
	ds_read_b32 v228, v116 offset:1024
	ds_read_b32 v229, v116 offset:1536
	ds_read_b32 v230, v116 offset:2048
	ds_read_b32 v231, v116 offset:2560
	ds_read_b32 v232, v116 offset:3072
	ds_read_b32 v233, v116 offset:3584
	s_waitcnt lgkmcnt(0)
	v_bfe_u32 v120, v226, 16, 1
	v_bfe_u32 v121, v227, 16, 1
	v_bfe_u32 v122, v228, 16, 1
	v_bfe_u32 v123, v229, 16, 1
	v_bfe_u32 v124, v230, 16, 1
	v_bfe_u32 v125, v231, 16, 1
	v_bfe_u32 v126, v232, 16, 1
	v_bfe_u32 v127, v233, 16, 1
	v_add3_u32 v226, v226, v120, s28
	v_add3_u32 v227, v227, v121, s28
	v_add3_u32 v228, v228, v122, s28
	v_add3_u32 v229, v229, v123, s28
	v_add3_u32 v230, v230, v124, s28
	v_add3_u32 v231, v231, v125, s28
	v_add3_u32 v232, v232, v126, s28
	v_add3_u32 v233, v233, v127, s28
	v_perm_b32 v242, v227, v226, s29
	v_perm_b32 v243, v229, v228, s29
	v_perm_b32 v244, v231, v230, s29
	v_perm_b32 v245, v233, v232, s29
	s_nop 0
	global_store_dwordx4 v110, v[242:245], s[6:7]
	ds_read_b32 v226, v118
	ds_read_b32 v227, v118 offset:512
	ds_read_b32 v228, v118 offset:1024
	ds_read_b32 v229, v118 offset:1536
	ds_read_b32 v230, v118 offset:2048
	ds_read_b32 v231, v118 offset:2560
	ds_read_b32 v232, v118 offset:3072
	ds_read_b32 v233, v118 offset:3584
	s_waitcnt lgkmcnt(0)
	v_bfe_u32 v120, v226, 16, 1
	v_bfe_u32 v121, v227, 16, 1
	v_bfe_u32 v122, v228, 16, 1
	v_bfe_u32 v123, v229, 16, 1
	v_bfe_u32 v124, v230, 16, 1
	v_bfe_u32 v125, v231, 16, 1
	v_bfe_u32 v126, v232, 16, 1
	v_bfe_u32 v127, v233, 16, 1
	v_add3_u32 v226, v226, v120, s28
	v_add3_u32 v227, v227, v121, s28
	v_add3_u32 v228, v228, v122, s28
	v_add3_u32 v229, v229, v123, s28
	v_add3_u32 v230, v230, v124, s28
	v_add3_u32 v231, v231, v125, s28
	v_add3_u32 v232, v232, v126, s28
	v_add3_u32 v233, v233, v127, s28
	v_perm_b32 v242, v227, v226, s29
	v_perm_b32 v243, v229, v228, s29
	v_perm_b32 v244, v231, v230, s29
	v_perm_b32 v245, v233, v232, s29
	s_nop 0
	global_store_dwordx4 v111, v[242:245], s[6:7]
	s_add_i32 s26, s23, 72
	s_add_i32 s27, s23, 88
	s_waitcnt vmcnt(16)
	v_mul_f32_e32 v176, v218, v176
	v_mul_f32_e32 v177, v218, v177
	v_mul_f32_e32 v178, v218, v178
	v_mul_f32_e32 v179, v218, v179
	ds_write_b128 v210, v[176:179]
	v_mul_f32_e32 v180, v219, v180
	v_mul_f32_e32 v181, v219, v181
	v_mul_f32_e32 v182, v219, v182
	v_mul_f32_e32 v183, v219, v183
	ds_write_b128 v210, v[180:183] offset:1024
	v_mul_f32_e32 v184, v220, v184
	v_mul_f32_e32 v185, v220, v185
	v_mul_f32_e32 v186, v220, v186
	v_mul_f32_e32 v187, v220, v187
	ds_write_b128 v210, v[184:187] offset:2048
	v_mul_f32_e32 v188, v221, v188
	v_mul_f32_e32 v189, v221, v189
	v_mul_f32_e32 v190, v221, v190
	v_mul_f32_e32 v191, v221, v191
	ds_write_b128 v210, v[188:191] offset:3072
	v_mul_f32_e32 v192, v222, v192
	v_mul_f32_e32 v193, v222, v193
	v_mul_f32_e32 v194, v222, v194
	v_mul_f32_e32 v195, v222, v195
	ds_write_b128 v210, v[192:195] offset:4096
	v_mul_f32_e32 v196, v223, v196
	v_mul_f32_e32 v197, v223, v197
	v_mul_f32_e32 v198, v223, v198
	v_mul_f32_e32 v199, v223, v199
	ds_write_b128 v210, v[196:199] offset:5120
	v_mul_f32_e32 v200, v224, v200
	v_mul_f32_e32 v201, v224, v201
	v_mul_f32_e32 v202, v224, v202
	v_mul_f32_e32 v203, v224, v203
	ds_write_b128 v210, v[200:203] offset:6144
	v_mul_f32_e32 v204, v225, v204
	v_mul_f32_e32 v205, v225, v205
	v_mul_f32_e32 v206, v225, v206
	v_mul_f32_e32 v207, v225, v207
	ds_write_b128 v210, v[204:207] offset:7168
	s_waitcnt lgkmcnt(0)
	s_barrier
; #define GAS __attribute__((address_space(1)))
; #define LAS __attribute__((address_space(3)))
; #define LDS_WAIT() asm volatile("s_waitcnt lgkmcnt(0)" ::: "memory")
; __device__ __forceinline__ unsigned pk2(float lo, float hi) { return f2bf(lo) | (f2bf(hi) << 16); }
; template <int MAP, bool KS, bool KPERM = false>
; __device__ __forceinline__ void p0_transpose_item(const float* W, int K, int Nsrc, int nblk, bf16* WT, const float* ksA, const float* ksB, int ksplit, LAS float* scr, int item, int lane) {
;     ...
;     for (int i = 0; i < 32; ++i) { const int kk = 2 * i + (lane >> 5); const int k = k0 + kk;
;         if (KS) v[i] *= (k < ksplit ? ksA[k] : ksB[k - ksplit]);
;         scr[kk * 33 + (lane & 31)] = v[i]; }
;     LDS_WAIT(); asm volatile("" ::: "memory");
;     const int c = lane & 7;
; #pragma unroll
;     for (int j = 0; j < 4; ++j) { const int n = (lane >> 3) + 8 * j; const LAS float* s = scr + (8 * c) * 33 + n;
;         v4u o; o.x = pk2(s[0 * 33], s[1 * 33]); o.y = pk2(s[2 * 33], s[3 * 33]); o.z = pk2(s[4 * 33], s[5 * 33]); o.w = pk2(s[6 * 33], s[7 * 33]);
;         *(GAS v4u*)(WT + (size_t)(n0 + n) * K + k0 + 8 * c) = o; }
	s_mul_i32 s20, s26, 0x100000
	s_add_u32 s6, s18, s20
	s_addc_u32 s7, s19, 0
	s_cmp_lt_u32 s26, 16
	s_cselect_b32 s20, 1, 0
	s_sub_i32 s21, s26, 16
	s_bitcmp0_b32 s21, 2
	s_cselect_b32 s21, 1, 0
	s_cmp_lt_u32 s26, 40
	s_cselect_b32 s21, s21, 0
	s_or_b32 s20, s20, s21
	s_cmp_lg_u32 s20, 0
	s_cselect_b64 s[20:21], -1, 0
	v_cndmask_b32_e64 v108, v100, v104, s[20:21]
	v_cndmask_b32_e64 v109, v101, v105, s[20:21]
	v_cndmask_b32_e64 v110, v102, v106, s[20:21]
	v_cndmask_b32_e64 v111, v103, v107, s[20:21]
	ds_read_b32 v226, v113
	ds_read_b32 v227, v113 offset:512
	ds_read_b32 v228, v113 offset:1024
	ds_read_b32 v229, v113 offset:1536
	ds_read_b32 v230, v113 offset:2048
	ds_read_b32 v231, v113 offset:2560
	ds_read_b32 v232, v113 offset:3072
	ds_read_b32 v233, v113 offset:3584
	s_waitcnt lgkmcnt(0)
	v_bfe_u32 v120, v226, 16, 1
	v_bfe_u32 v121, v227, 16, 1
	v_bfe_u32 v122, v228, 16, 1
	v_bfe_u32 v123, v229, 16, 1
	v_bfe_u32 v124, v230, 16, 1
	v_bfe_u32 v125, v231, 16, 1
	v_bfe_u32 v126, v232, 16, 1
	v_bfe_u32 v127, v233, 16, 1
	v_add3_u32 v226, v226, v120, s28
	v_add3_u32 v227, v227, v121, s28
	v_add3_u32 v228, v228, v122, s28
	v_add3_u32 v229, v229, v123, s28
	v_add3_u32 v230, v230, v124, s28
	v_add3_u32 v231, v231, v125, s28
	v_add3_u32 v232, v232, v126, s28
	v_add3_u32 v233, v233, v127, s28
	v_perm_b32 v242, v227, v226, s29
	v_perm_b32 v243, v229, v228, s29
	v_perm_b32 v244, v231, v230, s29
	v_perm_b32 v245, v233, v232, s29
	s_nop 0
	global_store_dwordx4 v108, v[242:245], s[6:7]
	ds_read_b32 v226, v115
	ds_read_b32 v227, v115 offset:512
	ds_read_b32 v228, v115 offset:1024
	ds_read_b32 v229, v115 offset:1536
	ds_read_b32 v230, v115 offset:2048
	ds_read_b32 v231, v115 offset:2560
	ds_read_b32 v232, v115 offset:3072
	ds_read_b32 v233, v115 offset:3584
	s_waitcnt lgkmcnt(0)
	v_bfe_u32 v120, v226, 16, 1
	v_bfe_u32 v121, v227, 16, 1
	v_bfe_u32 v122, v228, 16, 1
	v_bfe_u32 v123, v229, 16, 1
	v_bfe_u32 v124, v230, 16, 1
	v_bfe_u32 v125, v231, 16, 1
	v_bfe_u32 v126, v232, 16, 1
	v_bfe_u32 v127, v233, 16, 1
	v_add3_u32 v226, v226, v120, s28
	v_add3_u32 v227, v227, v121, s28
	v_add3_u32 v228, v228, v122, s28
	v_add3_u32 v229, v229, v123, s28
	v_add3_u32 v230, v230, v124, s28
	v_add3_u32 v231, v231, v125, s28
	v_add3_u32 v232, v232, v126, s28
	v_add3_u32 v233, v233, v127, s28
	v_perm_b32 v242, v227, v226, s29
	v_perm_b32 v243, v229, v228, s29
	v_perm_b32 v244, v231, v230, s29
	v_perm_b32 v245, v233, v232, s29
	s_nop 0
	global_store_dwordx4 v109, v[242:245], s[6:7]
	ds_read_b32 v226, v117
	ds_read_b32 v227, v117 offset:512
	ds_read_b32 v228, v117 offset:1024
	ds_read_b32 v229, v117 offset:1536
	ds_read_b32 v230, v117 offset:2048
	ds_read_b32 v231, v117 offset:2560
	ds_read_b32 v232, v117 offset:3072
	ds_read_b32 v233, v117 offset:3584
	s_waitcnt lgkmcnt(0)
	v_bfe_u32 v120, v226, 16, 1
	v_bfe_u32 v121, v227, 16, 1
	v_bfe_u32 v122, v228, 16, 1
	v_bfe_u32 v123, v229, 16, 1
	v_bfe_u32 v124, v230, 16, 1
	v_bfe_u32 v125, v231, 16, 1
	v_bfe_u32 v126, v232, 16, 1
	v_bfe_u32 v127, v233, 16, 1
	v_add3_u32 v226, v226, v120, s28
	v_add3_u32 v227, v227, v121, s28
	v_add3_u32 v228, v228, v122, s28
	v_add3_u32 v229, v229, v123, s28
	v_add3_u32 v230, v230, v124, s28
	v_add3_u32 v231, v231, v125, s28
	v_add3_u32 v232, v232, v126, s28
	v_add3_u32 v233, v233, v127, s28
	v_perm_b32 v242, v227, v226, s29
	v_perm_b32 v243, v229, v228, s29
	v_perm_b32 v244, v231, v230, s29
	v_perm_b32 v245, v233, v232, s29
	s_nop 0
	global_store_dwordx4 v110, v[242:245], s[6:7]
	ds_read_b32 v226, v119
	ds_read_b32 v227, v119 offset:512
	ds_read_b32 v228, v119 offset:1024
	ds_read_b32 v229, v119 offset:1536
	ds_read_b32 v230, v119 offset:2048
	ds_read_b32 v231, v119 offset:2560
	ds_read_b32 v232, v119 offset:3072
	ds_read_b32 v233, v119 offset:3584
	s_waitcnt lgkmcnt(0)
	v_bfe_u32 v120, v226, 16, 1
	v_bfe_u32 v121, v227, 16, 1
	v_bfe_u32 v122, v228, 16, 1
	v_bfe_u32 v123, v229, 16, 1
	v_bfe_u32 v124, v230, 16, 1
	v_bfe_u32 v125, v231, 16, 1
	v_bfe_u32 v126, v232, 16, 1
	v_bfe_u32 v127, v233, 16, 1
	v_add3_u32 v226, v226, v120, s28
	v_add3_u32 v227, v227, v121, s28
	v_add3_u32 v228, v228, v122, s28
	v_add3_u32 v229, v229, v123, s28
	v_add3_u32 v230, v230, v124, s28
	v_add3_u32 v231, v231, v125, s28
	v_add3_u32 v232, v232, v126, s28
	v_add3_u32 v233, v233, v127, s28
	v_perm_b32 v242, v227, v226, s29
	v_perm_b32 v243, v229, v228, s29
	v_perm_b32 v244, v231, v230, s29
	v_perm_b32 v245, v233, v232, s29
	s_nop 0
	global_store_dwordx4 v111, v[242:245], s[6:7]
	s_add_i32 s26, s23, 80
	s_add_i32 s27, s23, 96
	s_waitcnt vmcnt(8)
	v_mul_f32_e32 v144, v218, v144
	v_mul_f32_e32 v145, v218, v145
	v_mul_f32_e32 v146, v218, v146
	v_mul_f32_e32 v147, v218, v147
	ds_write_b128 v209, v[144:147]
	v_mul_f32_e32 v148, v219, v148
	v_mul_f32_e32 v149, v219, v149
	v_mul_f32_e32 v150, v219, v150
	v_mul_f32_e32 v151, v219, v151
	ds_write_b128 v209, v[148:151] offset:1024
	v_mul_f32_e32 v152, v220, v152
	v_mul_f32_e32 v153, v220, v153
	v_mul_f32_e32 v154, v220, v154
	v_mul_f32_e32 v155, v220, v155
	ds_write_b128 v209, v[152:155] offset:2048
	v_mul_f32_e32 v156, v221, v156
	v_mul_f32_e32 v157, v221, v157
	v_mul_f32_e32 v158, v221, v158
	v_mul_f32_e32 v159, v221, v159
	ds_write_b128 v209, v[156:159] offset:3072
	v_mul_f32_e32 v160, v222, v160
	v_mul_f32_e32 v161, v222, v161
	v_mul_f32_e32 v162, v222, v162
	v_mul_f32_e32 v163, v222, v163
	ds_write_b128 v209, v[160:163] offset:4096
	v_mul_f32_e32 v164, v223, v164
	v_mul_f32_e32 v165, v223, v165
	v_mul_f32_e32 v166, v223, v166
	v_mul_f32_e32 v167, v223, v167
	ds_write_b128 v209, v[164:167] offset:5120
	v_mul_f32_e32 v168, v224, v168
	v_mul_f32_e32 v169, v224, v169
	v_mul_f32_e32 v170, v224, v170
	v_mul_f32_e32 v171, v224, v171
	ds_write_b128 v209, v[168:171] offset:6144
	v_mul_f32_e32 v172, v225, v172
	v_mul_f32_e32 v173, v225, v173
	v_mul_f32_e32 v174, v225, v174
	v_mul_f32_e32 v175, v225, v175
	ds_write_b128 v209, v[172:175] offset:7168
	s_waitcnt lgkmcnt(0)
	s_barrier
; #define GAS __attribute__((address_space(1)))
; #define LAS __attribute__((address_space(3)))
; #define LDS_WAIT() asm volatile("s_waitcnt lgkmcnt(0)" ::: "memory")
; __device__ __forceinline__ unsigned pk2(float lo, float hi) { return f2bf(lo) | (f2bf(hi) << 16); }
; template <int MAP, bool KS, bool KPERM = false>
; __device__ __forceinline__ void p0_transpose_item(const float* W, int K, int Nsrc, int nblk, bf16* WT, const float* ksA, const float* ksB, int ksplit, LAS float* scr, int item, int lane) {
;     ...
;     for (int i = 0; i < 32; ++i) { const int kk = 2 * i + (lane >> 5); const int k = k0 + kk;
;         if (KS) v[i] *= (k < ksplit ? ksA[k] : ksB[k - ksplit]);
;         scr[kk * 33 + (lane & 31)] = v[i]; }
;     LDS_WAIT(); asm volatile("" ::: "memory");
;     const int c = lane & 7;
; #pragma unroll
;     for (int j = 0; j < 4; ++j) { const int n = (lane >> 3) + 8 * j; const LAS float* s = scr + (8 * c) * 33 + n;
;         v4u o; o.x = pk2(s[0 * 33], s[1 * 33]); o.y = pk2(s[2 * 33], s[3 * 33]); o.z = pk2(s[4 * 33], s[5 * 33]); o.w = pk2(s[6 * 33], s[7 * 33]);
;         *(GAS v4u*)(WT + (size_t)(n0 + n) * K + k0 + 8 * c) = o; }
	s_mul_i32 s20, s26, 0x100000
	s_add_u32 s6, s18, s20
	s_addc_u32 s7, s19, 0
	s_cmp_lt_u32 s26, 16
	s_cselect_b32 s20, 1, 0
	s_sub_i32 s21, s26, 16
	s_bitcmp0_b32 s21, 2
	s_cselect_b32 s21, 1, 0
	s_cmp_lt_u32 s26, 40
	s_cselect_b32 s21, s21, 0
	s_or_b32 s20, s20, s21
	s_cmp_lg_u32 s20, 0
	s_cselect_b64 s[20:21], -1, 0
	v_cndmask_b32_e64 v108, v100, v104, s[20:21]
	v_cndmask_b32_e64 v109, v101, v105, s[20:21]
	v_cndmask_b32_e64 v110, v102, v106, s[20:21]
	v_cndmask_b32_e64 v111, v103, v107, s[20:21]
	ds_read_b32 v226, v112
	ds_read_b32 v227, v112 offset:512
	ds_read_b32 v228, v112 offset:1024
	ds_read_b32 v229, v112 offset:1536
	ds_read_b32 v230, v112 offset:2048
	ds_read_b32 v231, v112 offset:2560
	ds_read_b32 v232, v112 offset:3072
	ds_read_b32 v233, v112 offset:3584
	s_waitcnt lgkmcnt(0)
	v_bfe_u32 v120, v226, 16, 1
	v_bfe_u32 v121, v227, 16, 1
	v_bfe_u32 v122, v228, 16, 1
	v_bfe_u32 v123, v229, 16, 1
	v_bfe_u32 v124, v230, 16, 1
	v_bfe_u32 v125, v231, 16, 1
	v_bfe_u32 v126, v232, 16, 1
	v_bfe_u32 v127, v233, 16, 1
	v_add3_u32 v226, v226, v120, s28
	v_add3_u32 v227, v227, v121, s28
	v_add3_u32 v228, v228, v122, s28
	v_add3_u32 v229, v229, v123, s28
	v_add3_u32 v230, v230, v124, s28
	v_add3_u32 v231, v231, v125, s28
	v_add3_u32 v232, v232, v126, s28
	v_add3_u32 v233, v233, v127, s28
	v_perm_b32 v242, v227, v226, s29
	v_perm_b32 v243, v229, v228, s29
	v_perm_b32 v244, v231, v230, s29
	v_perm_b32 v245, v233, v232, s29
	s_nop 0
	global_store_dwordx4 v108, v[242:245], s[6:7]
	ds_read_b32 v226, v114
	ds_read_b32 v227, v114 offset:512
	ds_read_b32 v228, v114 offset:1024
	ds_read_b32 v229, v114 offset:1536
	ds_read_b32 v230, v114 offset:2048
	ds_read_b32 v231, v114 offset:2560
	ds_read_b32 v232, v114 offset:3072
	ds_read_b32 v233, v114 offset:3584
	s_waitcnt lgkmcnt(0)
	v_bfe_u32 v120, v226, 16, 1
	v_bfe_u32 v121, v227, 16, 1
	v_bfe_u32 v122, v228, 16, 1
	v_bfe_u32 v123, v229, 16, 1
	v_bfe_u32 v124, v230, 16, 1
	v_bfe_u32 v125, v231, 16, 1
	v_bfe_u32 v126, v232, 16, 1
	v_bfe_u32 v127, v233, 16, 1
	v_add3_u32 v226, v226, v120, s28
	v_add3_u32 v227, v227, v121, s28
	v_add3_u32 v228, v228, v122, s28
	v_add3_u32 v229, v229, v123, s28
	v_add3_u32 v230, v230, v124, s28
	v_add3_u32 v231, v231, v125, s28
	v_add3_u32 v232, v232, v126, s28
	v_add3_u32 v233, v233, v127, s28
	v_perm_b32 v242, v227, v226, s29
	v_perm_b32 v243, v229, v228, s29
	v_perm_b32 v244, v231, v230, s29
	v_perm_b32 v245, v233, v232, s29
	s_nop 0
	global_store_dwordx4 v109, v[242:245], s[6:7]
	ds_read_b32 v226, v116
	ds_read_b32 v227, v116 offset:512
	ds_read_b32 v228, v116 offset:1024
	ds_read_b32 v229, v116 offset:1536
	ds_read_b32 v230, v116 offset:2048
	ds_read_b32 v231, v116 offset:2560
	ds_read_b32 v232, v116 offset:3072
	ds_read_b32 v233, v116 offset:3584
	s_waitcnt lgkmcnt(0)
	v_bfe_u32 v120, v226, 16, 1
	v_bfe_u32 v121, v227, 16, 1
	v_bfe_u32 v122, v228, 16, 1
	v_bfe_u32 v123, v229, 16, 1
	v_bfe_u32 v124, v230, 16, 1
	v_bfe_u32 v125, v231, 16, 1
	v_bfe_u32 v126, v232, 16, 1
	v_bfe_u32 v127, v233, 16, 1
	v_add3_u32 v226, v226, v120, s28
	v_add3_u32 v227, v227, v121, s28
	v_add3_u32 v228, v228, v122, s28
	v_add3_u32 v229, v229, v123, s28
	v_add3_u32 v230, v230, v124, s28
	v_add3_u32 v231, v231, v125, s28
	v_add3_u32 v232, v232, v126, s28
	v_add3_u32 v233, v233, v127, s28
	v_perm_b32 v242, v227, v226, s29
	v_perm_b32 v243, v229, v228, s29
	v_perm_b32 v244, v231, v230, s29
	v_perm_b32 v245, v233, v232, s29
	s_nop 0
	global_store_dwordx4 v110, v[242:245], s[6:7]
	ds_read_b32 v226, v118
	ds_read_b32 v227, v118 offset:512
	ds_read_b32 v228, v118 offset:1024
	ds_read_b32 v229, v118 offset:1536
	ds_read_b32 v230, v118 offset:2048
	ds_read_b32 v231, v118 offset:2560
	ds_read_b32 v232, v118 offset:3072
	ds_read_b32 v233, v118 offset:3584
	s_waitcnt lgkmcnt(0)
	v_bfe_u32 v120, v226, 16, 1
	v_bfe_u32 v121, v227, 16, 1
	v_bfe_u32 v122, v228, 16, 1
	v_bfe_u32 v123, v229, 16, 1
	v_bfe_u32 v124, v230, 16, 1
	v_bfe_u32 v125, v231, 16, 1
	v_bfe_u32 v126, v232, 16, 1
	v_bfe_u32 v127, v233, 16, 1
	v_add3_u32 v226, v226, v120, s28
	v_add3_u32 v227, v227, v121, s28
	v_add3_u32 v228, v228, v122, s28
	v_add3_u32 v229, v229, v123, s28
	v_add3_u32 v230, v230, v124, s28
	v_add3_u32 v231, v231, v125, s28
	v_add3_u32 v232, v232, v126, s28
	v_add3_u32 v233, v233, v127, s28
	v_perm_b32 v242, v227, v226, s29
	v_perm_b32 v243, v229, v228, s29
	v_perm_b32 v244, v231, v230, s29
	v_perm_b32 v245, v233, v232, s29
	s_nop 0
	global_store_dwordx4 v111, v[242:245], s[6:7]
	s_waitcnt lgkmcnt(0)
	s_barrier
; __device__ __forceinline__ int src_col_in(int c) {
;     if (c < 5120) { const int blk = c >> 7, p = c & 127; const bool rope = blk < 16 || ((((blk - 16) >> 2) & 1) == 0); const int d = rope ? (p >> 1) + 64 * (p & 1) : p; return blk * 128 + d; }
;     if (c < OFF_Z) return c + 2096;
;     if (c < OFF_G) return c - 4048;
;     if (c < OFF_DT) return 5120 + (c - OFF_G);
;     if (c < NSRC) return c;
;     return -1;
; }
;     const int pr = item >> 1, kb = 2 * (pr / nblk) + (item & 1), nb = pr % nblk, k0 = 64 * kb, n0 = 32 * nb;
;     const int nr = n0 + (lane & 31); const int sc = MAP == 1 ? src_col_in(nr) : nr;
;     float v[32];
; #pragma unroll
;     for (int i = 0; i < 32; ++i) v[i] = sc >= 0 ? W[(size_t)(k0 + 2 * i + (lane >> 5)) * Nsrc + sc] : 0.f;
; #pragma unroll
;     for (int i = 0; i < 32; ++i) { const int k = k0 + 2 * i + (lane >> 5); float x = v[i] * wscale; if (KS) x *= (k < ksplit ? ksA[k] : ksB[k - ksplit]); scr[(2 * i + (lane >> 5)) * 33 + (lane & 31)] = x; }
	v_lshrrev_b32_e32 v246, 5, v249
	v_lshl_add_u32 v246, v250, 4, v246
	v_and_b32_e32 v247, 31, v249
	v_lshlrev_b32_e32 v247, 4, v247
	s_mov_b32 s20, 0xb140
	v_mad_u32_u24 v208, v246, s20, v247
	v_lshrrev_b32_e32 v246, 3, v249
	v_lshl_add_u32 v246, v250, 4, v246
	v_and_b32_e32 v247, 7, v249
	v_lshlrev_b32_e32 v247, 4, v247
	v_lshl_add_u32 v100, v246, 12, v247
	v_and_b32_e32 v248, 63, v246
	v_lshlrev_b32_e32 v248, 1, v248
	v_lshrrev_b32_e32 v246, 6, v246
	v_or_b32_e32 v248, v248, v246
	v_lshl_add_u32 v104, v248, 12, v247
	v_lshrrev_b32_e32 v246, 3, v249
	v_lshl_add_u32 v246, v250, 4, v246
	v_add_u32_e32 v246, 8, v246
	v_and_b32_e32 v247, 7, v249
	v_lshlrev_b32_e32 v247, 4, v247
	v_lshl_add_u32 v101, v246, 12, v247
	v_and_b32_e32 v248, 63, v246
	v_lshlrev_b32_e32 v248, 1, v248
	v_lshrrev_b32_e32 v246, 6, v246
	v_or_b32_e32 v248, v248, v246
	v_lshl_add_u32 v105, v248, 12, v247
	s_lshr_b32 s22, s15, 3
	s_and_b32 s23, s15, 7
	v_readlane_b32 s16, v253, 7
	v_readlane_b32 s17, v253, 8
	v_readlane_b32 s18, v253, 41
	v_readlane_b32 s19, v253, 42
	s_add_u32 s16, s16, 0xb140000
	s_addc_u32 s17, s17, 0
	s_mul_i32 s20, s22, 0x58a000
	s_add_u32 s16, s16, s20
	s_addc_u32 s17, s17, 0
	s_add_u32 s18, s18, 0x5c00000
	s_addc_u32 s19, s19, 0
	s_lshl_b32 s20, s22, 7
	s_add_u32 s18, s18, s20
	s_addc_u32 s19, s19, 0
	v_readlane_b32 s10, v253, 5
	v_readlane_b32 s11, v253, 6
	s_lshl_b32 s20, s22, 9
	s_add_i32 s20, s20, 0x4000
	s_add_u32 s10, s10, s20
	s_addc_u32 s11, s11, 0
	s_mov_b32 s44, 0xc3e00000
	v_mov_b32_e32 v246, 0x43e00000
	s_mov_b32 s28, 0x7fff
	s_mov_b32 s29, 0x07060302
	global_load_dword v218, v217, s[10:11] offset:0
	global_load_dword v219, v217, s[10:11] offset:8
	global_load_dword v220, v217, s[10:11] offset:16
	global_load_dword v221, v217, s[10:11] offset:24
	global_load_dword v222, v217, s[10:11] offset:32
	global_load_dword v223, v217, s[10:11] offset:40
	global_load_dword v224, v217, s[10:11] offset:48
	global_load_dword v225, v217, s[10:11] offset:56
	s_waitcnt vmcnt(0)
	v_mul_f32_e32 v218, 0x42800000, v218
	v_mul_f32_e32 v219, 0x42800000, v219
	v_mul_f32_e32 v220, 0x42800000, v220
	v_mul_f32_e32 v221, 0x42800000, v221
	v_mul_f32_e32 v222, 0x42800000, v222
	v_mul_f32_e32 v223, 0x42800000, v223
	v_mul_f32_e32 v224, 0x42800000, v224
	v_mul_f32_e32 v225, 0x42800000, v225
	s_mov_b32 s24, s23
	s_add_i32 s25, s23, 8
	s_lshl_b32 s20, s24, 7
	s_cmp_lt_u32 s24, 40
	s_cselect_b32 s21, 0, 0x830
	s_cmp_lt_u32 s24, 72
	s_cselect_b32 s21, s21, 0xfffff030
	s_add_i32 s20, s20, s21
	s_lshl_b32 s20, s20, 2
	s_add_u32 s8, s16, s20
	s_addc_u32 s9, s17, 0
	global_load_dwordx4 v[144:147], v208, s[8:9]
	s_add_u32 s8, s8, 0x16280
	s_addc_u32 s9, s9, 0
	global_load_dwordx4 v[148:151], v208, s[8:9]
	s_add_u32 s8, s8, 0x16280
	s_addc_u32 s9, s9, 0
	global_load_dwordx4 v[152:155], v208, s[8:9]
	s_add_u32 s8, s8, 0x16280
	s_addc_u32 s9, s9, 0
	global_load_dwordx4 v[156:159], v208, s[8:9]
	s_add_u32 s8, s8, 0x16280
	s_addc_u32 s9, s9, 0
	global_load_dwordx4 v[160:163], v208, s[8:9]
	s_add_u32 s8, s8, 0x16280
	s_addc_u32 s9, s9, 0
	global_load_dwordx4 v[164:167], v208, s[8:9]
	s_add_u32 s8, s8, 0x16280
	s_addc_u32 s9, s9, 0
	global_load_dwordx4 v[168:171], v208, s[8:9]
	s_add_u32 s8, s8, 0x16280
	s_addc_u32 s9, s9, 0
	global_load_dwordx4 v[172:175], v208, s[8:9]
	s_lshl_b32 s20, s25, 7
	s_cmp_lt_u32 s25, 40
	s_cselect_b32 s21, 0, 0x830
	s_cmp_lt_u32 s25, 72
	s_cselect_b32 s21, s21, 0xfffff030
	s_add_i32 s20, s20, s21
	s_lshl_b32 s20, s20, 2
	s_add_u32 s8, s16, s20
	s_addc_u32 s9, s17, 0
	global_load_dwordx4 v[176:179], v208, s[8:9]
	s_add_u32 s8, s8, 0x16280
	s_addc_u32 s9, s9, 0
	global_load_dwordx4 v[180:183], v208, s[8:9]
	s_add_u32 s8, s8, 0x16280
	s_addc_u32 s9, s9, 0
	global_load_dwordx4 v[184:187], v208, s[8:9]
	s_add_u32 s8, s8, 0x16280
	s_addc_u32 s9, s9, 0
	global_load_dwordx4 v[188:191], v208, s[8:9]
	s_add_u32 s8, s8, 0x16280
	s_addc_u32 s9, s9, 0
	global_load_dwordx4 v[192:195], v208, s[8:9]
	s_add_u32 s8, s8, 0x16280
	s_addc_u32 s9, s9, 0
	global_load_dwordx4 v[196:199], v208, s[8:9]
	s_add_u32 s8, s8, 0x16280
	s_addc_u32 s9, s9, 0
	global_load_dwordx4 v[200:203], v208, s[8:9]
	s_add_u32 s8, s8, 0x16280
	s_addc_u32 s9, s9, 0
	global_load_dwordx4 v[204:207], v208, s[8:9]
	s_add_i32 s26, s23, 0
	s_add_i32 s27, s23, 16
	s_waitcnt vmcnt(8)
	v_mul_f32_e32 v144, v218, v144
	v_mul_f32_e32 v145, v218, v145
	v_mul_f32_e32 v146, v218, v146
	v_mul_f32_e32 v147, v218, v147
	ds_write_b128 v209, v[144:147]
	v_mul_f32_e32 v148, v219, v148
	v_mul_f32_e32 v149, v219, v149
	v_mul_f32_e32 v150, v219, v150
	v_mul_f32_e32 v151, v219, v151
	ds_write_b128 v209, v[148:151] offset:1024
	v_mul_f32_e32 v152, v220, v152
	v_mul_f32_e32 v153, v220, v153
	v_mul_f32_e32 v154, v220, v154
	v_mul_f32_e32 v155, v220, v155
	ds_write_b128 v209, v[152:155] offset:2048
	v_mul_f32_e32 v156, v221, v156
	v_mul_f32_e32 v157, v221, v157
	v_mul_f32_e32 v158, v221, v158
	v_mul_f32_e32 v159, v221, v159
	ds_write_b128 v209, v[156:159] offset:3072
	v_mul_f32_e32 v160, v222, v160
	v_mul_f32_e32 v161, v222, v161
	v_mul_f32_e32 v162, v222, v162
	v_mul_f32_e32 v163, v222, v163
	ds_write_b128 v209, v[160:163] offset:4096
	v_mul_f32_e32 v164, v223, v164
	v_mul_f32_e32 v165, v223, v165
	v_mul_f32_e32 v166, v223, v166
	v_mul_f32_e32 v167, v223, v167
	ds_write_b128 v209, v[164:167] offset:5120
	v_mul_f32_e32 v168, v224, v168
	v_mul_f32_e32 v169, v224, v169
	v_mul_f32_e32 v170, v224, v170
	v_mul_f32_e32 v171, v224, v171
	ds_write_b128 v209, v[168:171] offset:6144
	v_mul_f32_e32 v172, v225, v172
	v_mul_f32_e32 v173, v225, v173
	v_mul_f32_e32 v174, v225, v174
	v_mul_f32_e32 v175, v225, v175
	ds_write_b128 v209, v[172:175] offset:7168
	s_waitcnt lgkmcnt(0)
	s_barrier
; #define GAS __attribute__((address_space(1)))
; #define LAS __attribute__((address_space(3)))
; #define LDS_WAIT() asm volatile("s_waitcnt lgkmcnt(0)" ::: "memory")
; __device__ __forceinline__ unsigned pk4_fp8(float a, float b, float c, float d) {
;     a = fminf(fmaxf(a, -448.f), 448.f); b = fminf(fmaxf(b, -448.f), 448.f); c = fminf(fmaxf(c, -448.f), 448.f); d = fminf(fmaxf(d, -448.f), 448.f);
;     int w = __builtin_amdgcn_cvt_pk_fp8_f32(a, b, 0, false); w = __builtin_amdgcn_cvt_pk_fp8_f32(c, d, w, true); return (unsigned)w; }
;     ...
;     for (int i = 0; i < 32; ++i) { const int k = k0 + 2 * i + (lane >> 5); float x = v[i] * wscale; if (KS) x *= (k < ksplit ? ksA[k] : ksB[k - ksplit]); scr[(2 * i + (lane >> 5)) * 33 + (lane & 31)] = x; }
;     LDS_WAIT(); asm volatile("" ::: "memory");
;     const int c = lane & 7;
; #pragma unroll
;     for (int j = 0; j < 4; ++j) { const int n = (lane >> 3) + 8 * j; const LAS float* s = scr + (8 * c) * 33 + n;
;         const unsigned long long o = (unsigned long long)pg8::pk4_fp8(s[0 * 33], s[1 * 33], s[2 * 33], s[3 * 33]) | ((unsigned long long)pg8::pk4_fp8(s[4 * 33], s[5 * 33], s[6 * 33], s[7 * 33]) << 32);
;         *(GAS unsigned long long*)(WT + (size_t)(n0 + n) * K + k0 + 8 * c) = o; }
	s_lshl_b32 s20, s27, 7
	s_cmp_lt_u32 s27, 40
	s_cselect_b32 s21, 0, 0x830
	s_cmp_lt_u32 s27, 72
	s_cselect_b32 s21, s21, 0xfffff030
	s_add_i32 s20, s20, s21
	s_lshl_b32 s20, s20, 2
	s_add_u32 s8, s16, s20
	s_addc_u32 s9, s17, 0
	global_load_dwordx4 v[144:147], v208, s[8:9]
	s_add_u32 s8, s8, 0x16280
	s_addc_u32 s9, s9, 0
	global_load_dwordx4 v[148:151], v208, s[8:9]
	s_add_u32 s8, s8, 0x16280
	s_addc_u32 s9, s9, 0
	global_load_dwordx4 v[152:155], v208, s[8:9]
	s_add_u32 s8, s8, 0x16280
	s_addc_u32 s9, s9, 0
	global_load_dwordx4 v[156:159], v208, s[8:9]
	s_add_u32 s8, s8, 0x16280
	s_addc_u32 s9, s9, 0
	global_load_dwordx4 v[160:163], v208, s[8:9]
	s_add_u32 s8, s8, 0x16280
	s_addc_u32 s9, s9, 0
	global_load_dwordx4 v[164:167], v208, s[8:9]
	s_add_u32 s8, s8, 0x16280
	s_addc_u32 s9, s9, 0
	global_load_dwordx4 v[168:171], v208, s[8:9]
	s_add_u32 s8, s8, 0x16280
	s_addc_u32 s9, s9, 0
	global_load_dwordx4 v[172:175], v208, s[8:9]
	s_mul_i32 s20, s26, 0x80000
	s_add_u32 s6, s18, s20
	s_addc_u32 s7, s19, 0
	s_cmp_lt_u32 s26, 16
	s_cselect_b32 s20, 1, 0
	s_sub_i32 s21, s26, 16
	s_bitcmp0_b32 s21, 2
	s_cselect_b32 s21, 1, 0
	s_cmp_lt_u32 s26, 40
	s_cselect_b32 s21, s21, 0
	s_or_b32 s20, s20, s21
	s_cmp_lg_u32 s20, 0
	s_cselect_b64 s[20:21], -1, 0
	v_cndmask_b32_e64 v108, v100, v104, s[20:21]
	v_cndmask_b32_e64 v109, v101, v105, s[20:21]
	ds_read_b32 v226, v211
	ds_read_b32 v227, v211 offset:512
	ds_read_b32 v228, v211 offset:1024
	ds_read_b32 v229, v211 offset:1536
	ds_read_b32 v230, v211 offset:2048
	ds_read_b32 v231, v211 offset:2560
	ds_read_b32 v232, v211 offset:3072
	ds_read_b32 v233, v211 offset:3584
	ds_read_b32 v234, v211 offset:4096
	ds_read_b32 v235, v211 offset:4608
	ds_read_b32 v236, v211 offset:5120
	ds_read_b32 v237, v211 offset:5632
	ds_read_b32 v238, v211 offset:6144
	ds_read_b32 v239, v211 offset:6656
	ds_read_b32 v240, v211 offset:7168
	ds_read_b32 v241, v211 offset:7680
	s_waitcnt lgkmcnt(0)
	v_max_f32_e32 v226, v226, v226
	v_max_f32_e32 v227, v227, v227
	v_max_f32_e32 v228, v228, v228
	v_max_f32_e32 v229, v229, v229
	v_max_f32_e32 v230, v230, v230
	v_max_f32_e32 v231, v231, v231
	v_max_f32_e32 v232, v232, v232
	v_max_f32_e32 v233, v233, v233
	v_max_f32_e32 v234, v234, v234
	v_max_f32_e32 v235, v235, v235
	v_max_f32_e32 v236, v236, v236
	v_max_f32_e32 v237, v237, v237
	v_max_f32_e32 v238, v238, v238
	v_max_f32_e32 v239, v239, v239
	v_max_f32_e32 v240, v240, v240
	v_max_f32_e32 v241, v241, v241
	v_med3_f32 v226, v226, s44, v246
	v_med3_f32 v227, v227, s44, v246
	v_med3_f32 v228, v228, s44, v246
	v_med3_f32 v229, v229, s44, v246
	v_med3_f32 v230, v230, s44, v246
	v_med3_f32 v231, v231, s44, v246
	v_med3_f32 v232, v232, s44, v246
	v_med3_f32 v233, v233, s44, v246
	v_med3_f32 v234, v234, s44, v246
	v_med3_f32 v235, v235, s44, v246
	v_med3_f32 v236, v236, s44, v246
	v_med3_f32 v237, v237, s44, v246
	v_med3_f32 v238, v238, s44, v246
	v_med3_f32 v239, v239, s44, v246
	v_med3_f32 v240, v240, s44, v246
	v_med3_f32 v241, v241, s44, v246
	v_mov_b32_e32 v242, 0
	v_mov_b32_e32 v243, 0
	v_mov_b32_e32 v244, 0
	v_mov_b32_e32 v245, 0
	v_cvt_pk_fp8_f32 v242, v226, v227
	v_cvt_pk_fp8_f32 v243, v230, v231
	v_cvt_pk_fp8_f32 v244, v234, v235
	v_cvt_pk_fp8_f32 v245, v238, v239
	v_cvt_pk_fp8_f32 v242, v228, v229 op_sel:[0,0,1]
	v_cvt_pk_fp8_f32 v243, v232, v233 op_sel:[0,0,1]
	v_cvt_pk_fp8_f32 v244, v236, v237 op_sel:[0,0,1]
	v_cvt_pk_fp8_f32 v245, v240, v241 op_sel:[0,0,1]
	s_nop 0
	global_store_dwordx4 v108, v[242:245], s[6:7]
	ds_read_b32 v226, v213
	ds_read_b32 v227, v213 offset:512
	ds_read_b32 v228, v213 offset:1024
	ds_read_b32 v229, v213 offset:1536
	ds_read_b32 v230, v213 offset:2048
	ds_read_b32 v231, v213 offset:2560
	ds_read_b32 v232, v213 offset:3072
	ds_read_b32 v233, v213 offset:3584
	ds_read_b32 v234, v213 offset:4096
	ds_read_b32 v235, v213 offset:4608
	ds_read_b32 v236, v213 offset:5120
	ds_read_b32 v237, v213 offset:5632
	ds_read_b32 v238, v213 offset:6144
	ds_read_b32 v239, v213 offset:6656
	ds_read_b32 v240, v213 offset:7168
	ds_read_b32 v241, v213 offset:7680
	s_waitcnt lgkmcnt(0)
	v_max_f32_e32 v226, v226, v226
	v_max_f32_e32 v227, v227, v227
	v_max_f32_e32 v228, v228, v228
	v_max_f32_e32 v229, v229, v229
	v_max_f32_e32 v230, v230, v230
	v_max_f32_e32 v231, v231, v231
	v_max_f32_e32 v232, v232, v232
	v_max_f32_e32 v233, v233, v233
	v_max_f32_e32 v234, v234, v234
	v_max_f32_e32 v235, v235, v235
	v_max_f32_e32 v236, v236, v236
	v_max_f32_e32 v237, v237, v237
	v_max_f32_e32 v238, v238, v238
	v_max_f32_e32 v239, v239, v239
	v_max_f32_e32 v240, v240, v240
	v_max_f32_e32 v241, v241, v241
	v_med3_f32 v226, v226, s44, v246
	v_med3_f32 v227, v227, s44, v246
	v_med3_f32 v228, v228, s44, v246
	v_med3_f32 v229, v229, s44, v246
	v_med3_f32 v230, v230, s44, v246
	v_med3_f32 v231, v231, s44, v246
	v_med3_f32 v232, v232, s44, v246
	v_med3_f32 v233, v233, s44, v246
	v_med3_f32 v234, v234, s44, v246
	v_med3_f32 v235, v235, s44, v246
	v_med3_f32 v236, v236, s44, v246
	v_med3_f32 v237, v237, s44, v246
	v_med3_f32 v238, v238, s44, v246
	v_med3_f32 v239, v239, s44, v246
	v_med3_f32 v240, v240, s44, v246
	v_med3_f32 v241, v241, s44, v246
	v_mov_b32_e32 v242, 0
	v_mov_b32_e32 v243, 0
	v_mov_b32_e32 v244, 0
	v_mov_b32_e32 v245, 0
	v_cvt_pk_fp8_f32 v242, v226, v227
	v_cvt_pk_fp8_f32 v243, v230, v231
	v_cvt_pk_fp8_f32 v244, v234, v235
	v_cvt_pk_fp8_f32 v245, v238, v239
	v_cvt_pk_fp8_f32 v242, v228, v229 op_sel:[0,0,1]
	v_cvt_pk_fp8_f32 v243, v232, v233 op_sel:[0,0,1]
	v_cvt_pk_fp8_f32 v244, v236, v237 op_sel:[0,0,1]
	v_cvt_pk_fp8_f32 v245, v240, v241 op_sel:[0,0,1]
	s_nop 0
	global_store_dwordx4 v109, v[242:245], s[6:7]
	s_add_i32 s26, s23, 8
	s_add_i32 s27, s23, 24
	s_waitcnt vmcnt(10)
; #define GAS __attribute__((address_space(1)))
; #define LAS __attribute__((address_space(3)))
; #define LDS_WAIT() asm volatile("s_waitcnt lgkmcnt(0)" ::: "memory")
; __device__ __forceinline__ unsigned pk4_fp8(float a, float b, float c, float d) {
;     a = fminf(fmaxf(a, -448.f), 448.f); b = fminf(fmaxf(b, -448.f), 448.f); c = fminf(fmaxf(c, -448.f), 448.f); d = fminf(fmaxf(d, -448.f), 448.f);
;     int w = __builtin_amdgcn_cvt_pk_fp8_f32(a, b, 0, false); w = __builtin_amdgcn_cvt_pk_fp8_f32(c, d, w, true); return (unsigned)w; }
;     ...
;     for (int i = 0; i < 32; ++i) { const int k = k0 + 2 * i + (lane >> 5); float x = v[i] * wscale; if (KS) x *= (k < ksplit ? ksA[k] : ksB[k - ksplit]); scr[(2 * i + (lane >> 5)) * 33 + (lane & 31)] = x; }
;     LDS_WAIT(); asm volatile("" ::: "memory");
;     const int c = lane & 7;
; #pragma unroll
;     for (int j = 0; j < 4; ++j) { const int n = (lane >> 3) + 8 * j; const LAS float* s = scr + (8 * c) * 33 + n;
;         const unsigned long long o = (unsigned long long)pg8::pk4_fp8(s[0 * 33], s[1 * 33], s[2 * 33], s[3 * 33]) | ((unsigned long long)pg8::pk4_fp8(s[4 * 33], s[5 * 33], s[6 * 33], s[7 * 33]) << 32);
;         *(GAS unsigned long long*)(WT + (size_t)(n0 + n) * K + k0 + 8 * c) = o; }
	v_mul_f32_e32 v176, v218, v176
	v_mul_f32_e32 v177, v218, v177
	v_mul_f32_e32 v178, v218, v178
	v_mul_f32_e32 v179, v218, v179
	ds_write_b128 v210, v[176:179]
	v_mul_f32_e32 v180, v219, v180
	v_mul_f32_e32 v181, v219, v181
	v_mul_f32_e32 v182, v219, v182
	v_mul_f32_e32 v183, v219, v183
	ds_write_b128 v210, v[180:183] offset:1024
	v_mul_f32_e32 v184, v220, v184
	v_mul_f32_e32 v185, v220, v185
	v_mul_f32_e32 v186, v220, v186
	v_mul_f32_e32 v187, v220, v187
	ds_write_b128 v210, v[184:187] offset:2048
	v_mul_f32_e32 v188, v221, v188
	v_mul_f32_e32 v189, v221, v189
	v_mul_f32_e32 v190, v221, v190
	v_mul_f32_e32 v191, v221, v191
	ds_write_b128 v210, v[188:191] offset:3072
	v_mul_f32_e32 v192, v222, v192
	v_mul_f32_e32 v193, v222, v193
	v_mul_f32_e32 v194, v222, v194
	v_mul_f32_e32 v195, v222, v195
	ds_write_b128 v210, v[192:195] offset:4096
	v_mul_f32_e32 v196, v223, v196
	v_mul_f32_e32 v197, v223, v197
	v_mul_f32_e32 v198, v223, v198
	v_mul_f32_e32 v199, v223, v199
	ds_write_b128 v210, v[196:199] offset:5120
	v_mul_f32_e32 v200, v224, v200
	v_mul_f32_e32 v201, v224, v201
	v_mul_f32_e32 v202, v224, v202
	v_mul_f32_e32 v203, v224, v203
	ds_write_b128 v210, v[200:203] offset:6144
	v_mul_f32_e32 v204, v225, v204
	v_mul_f32_e32 v205, v225, v205
	v_mul_f32_e32 v206, v225, v206
	v_mul_f32_e32 v207, v225, v207
	ds_write_b128 v210, v[204:207] offset:7168
	s_waitcnt lgkmcnt(0)
	s_barrier
	s_lshl_b32 s20, s27, 7
	s_cmp_lt_u32 s27, 40
	s_cselect_b32 s21, 0, 0x830
	s_cmp_lt_u32 s27, 72
	s_cselect_b32 s21, s21, 0xfffff030
	s_add_i32 s20, s20, s21
	s_lshl_b32 s20, s20, 2
	s_add_u32 s8, s16, s20
	s_addc_u32 s9, s17, 0
	global_load_dwordx4 v[176:179], v208, s[8:9]
	s_add_u32 s8, s8, 0x16280
	s_addc_u32 s9, s9, 0
	global_load_dwordx4 v[180:183], v208, s[8:9]
	s_add_u32 s8, s8, 0x16280
	s_addc_u32 s9, s9, 0
	global_load_dwordx4 v[184:187], v208, s[8:9]
	s_add_u32 s8, s8, 0x16280
	s_addc_u32 s9, s9, 0
	global_load_dwordx4 v[188:191], v208, s[8:9]
	s_add_u32 s8, s8, 0x16280
	s_addc_u32 s9, s9, 0
	global_load_dwordx4 v[192:195], v208, s[8:9]
	s_add_u32 s8, s8, 0x16280
	s_addc_u32 s9, s9, 0
	global_load_dwordx4 v[196:199], v208, s[8:9]
	s_add_u32 s8, s8, 0x16280
	s_addc_u32 s9, s9, 0
	global_load_dwordx4 v[200:203], v208, s[8:9]
	s_add_u32 s8, s8, 0x16280
	s_addc_u32 s9, s9, 0
	global_load_dwordx4 v[204:207], v208, s[8:9]
	s_mul_i32 s20, s26, 0x80000
	s_add_u32 s6, s18, s20
	s_addc_u32 s7, s19, 0
	s_cmp_lt_u32 s26, 16
	s_cselect_b32 s20, 1, 0
	s_sub_i32 s21, s26, 16
	s_bitcmp0_b32 s21, 2
	s_cselect_b32 s21, 1, 0
	s_cmp_lt_u32 s26, 40
	s_cselect_b32 s21, s21, 0
	s_or_b32 s20, s20, s21
	s_cmp_lg_u32 s20, 0
	s_cselect_b64 s[20:21], -1, 0
	v_cndmask_b32_e64 v108, v100, v104, s[20:21]
	v_cndmask_b32_e64 v109, v101, v105, s[20:21]
	ds_read_b32 v226, v212
	ds_read_b32 v227, v212 offset:512
	ds_read_b32 v228, v212 offset:1024
	ds_read_b32 v229, v212 offset:1536
	ds_read_b32 v230, v212 offset:2048
	ds_read_b32 v231, v212 offset:2560
	ds_read_b32 v232, v212 offset:3072
	ds_read_b32 v233, v212 offset:3584
	ds_read_b32 v234, v212 offset:4096
	ds_read_b32 v235, v212 offset:4608
	ds_read_b32 v236, v212 offset:5120
	ds_read_b32 v237, v212 offset:5632
	ds_read_b32 v238, v212 offset:6144
	ds_read_b32 v239, v212 offset:6656
	ds_read_b32 v240, v212 offset:7168
	ds_read_b32 v241, v212 offset:7680
	s_waitcnt lgkmcnt(0)
	v_max_f32_e32 v226, v226, v226
	v_max_f32_e32 v227, v227, v227
	v_max_f32_e32 v228, v228, v228
	v_max_f32_e32 v229, v229, v229
	v_max_f32_e32 v230, v230, v230
	v_max_f32_e32 v231, v231, v231
	v_max_f32_e32 v232, v232, v232
	v_max_f32_e32 v233, v233, v233
	v_max_f32_e32 v234, v234, v234
	v_max_f32_e32 v235, v235, v235
	v_max_f32_e32 v236, v236, v236
	v_max_f32_e32 v237, v237, v237
	v_max_f32_e32 v238, v238, v238
	v_max_f32_e32 v239, v239, v239
	v_max_f32_e32 v240, v240, v240
	v_max_f32_e32 v241, v241, v241
	v_med3_f32 v226, v226, s44, v246
	v_med3_f32 v227, v227, s44, v246
	v_med3_f32 v228, v228, s44, v246
	v_med3_f32 v229, v229, s44, v246
	v_med3_f32 v230, v230, s44, v246
	v_med3_f32 v231, v231, s44, v246
	v_med3_f32 v232, v232, s44, v246
	v_med3_f32 v233, v233, s44, v246
	v_med3_f32 v234, v234, s44, v246
	v_med3_f32 v235, v235, s44, v246
	v_med3_f32 v236, v236, s44, v246
	v_med3_f32 v237, v237, s44, v246
	v_med3_f32 v238, v238, s44, v246
	v_med3_f32 v239, v239, s44, v246
	v_med3_f32 v240, v240, s44, v246
	v_med3_f32 v241, v241, s44, v246
	v_mov_b32_e32 v242, 0
	v_mov_b32_e32 v243, 0
	v_mov_b32_e32 v244, 0
	v_mov_b32_e32 v245, 0
	v_cvt_pk_fp8_f32 v242, v226, v227
	v_cvt_pk_fp8_f32 v243, v230, v231
	v_cvt_pk_fp8_f32 v244, v234, v235
	v_cvt_pk_fp8_f32 v245, v238, v239
	v_cvt_pk_fp8_f32 v242, v228, v229 op_sel:[0,0,1]
	v_cvt_pk_fp8_f32 v243, v232, v233 op_sel:[0,0,1]
	v_cvt_pk_fp8_f32 v244, v236, v237 op_sel:[0,0,1]
	v_cvt_pk_fp8_f32 v245, v240, v241 op_sel:[0,0,1]
	s_nop 0
	global_store_dwordx4 v108, v[242:245], s[6:7]
	ds_read_b32 v226, v214
	ds_read_b32 v227, v214 offset:512
	ds_read_b32 v228, v214 offset:1024
	ds_read_b32 v229, v214 offset:1536
	ds_read_b32 v230, v214 offset:2048
	ds_read_b32 v231, v214 offset:2560
	ds_read_b32 v232, v214 offset:3072
	ds_read_b32 v233, v214 offset:3584
	ds_read_b32 v234, v214 offset:4096
	ds_read_b32 v235, v214 offset:4608
	ds_read_b32 v236, v214 offset:5120
	ds_read_b32 v237, v214 offset:5632
	ds_read_b32 v238, v214 offset:6144
	ds_read_b32 v239, v214 offset:6656
	ds_read_b32 v240, v214 offset:7168
	ds_read_b32 v241, v214 offset:7680
	s_waitcnt lgkmcnt(0)
; #define GAS __attribute__((address_space(1)))
; #define LAS __attribute__((address_space(3)))
; #define LDS_WAIT() asm volatile("s_waitcnt lgkmcnt(0)" ::: "memory")
; __device__ __forceinline__ unsigned pk4_fp8(float a, float b, float c, float d) {
;     a = fminf(fmaxf(a, -448.f), 448.f); b = fminf(fmaxf(b, -448.f), 448.f); c = fminf(fmaxf(c, -448.f), 448.f); d = fminf(fmaxf(d, -448.f), 448.f);
;     int w = __builtin_amdgcn_cvt_pk_fp8_f32(a, b, 0, false); w = __builtin_amdgcn_cvt_pk_fp8_f32(c, d, w, true); return (unsigned)w; }
;     ...
;     for (int i = 0; i < 32; ++i) { const int k = k0 + 2 * i + (lane >> 5); float x = v[i] * wscale; if (KS) x *= (k < ksplit ? ksA[k] : ksB[k - ksplit]); scr[(2 * i + (lane >> 5)) * 33 + (lane & 31)] = x; }
;     LDS_WAIT(); asm volatile("" ::: "memory");
;     const int c = lane & 7;
; #pragma unroll
;     for (int j = 0; j < 4; ++j) { const int n = (lane >> 3) + 8 * j; const LAS float* s = scr + (8 * c) * 33 + n;
;         const unsigned long long o = (unsigned long long)pg8::pk4_fp8(s[0 * 33], s[1 * 33], s[2 * 33], s[3 * 33]) | ((unsigned long long)pg8::pk4_fp8(s[4 * 33], s[5 * 33], s[6 * 33], s[7 * 33]) << 32);
;         *(GAS unsigned long long*)(WT + (size_t)(n0 + n) * K + k0 + 8 * c) = o; }
	v_max_f32_e32 v226, v226, v226
	v_max_f32_e32 v227, v227, v227
	v_max_f32_e32 v228, v228, v228
	v_max_f32_e32 v229, v229, v229
	v_max_f32_e32 v230, v230, v230
	v_max_f32_e32 v231, v231, v231
	v_max_f32_e32 v232, v232, v232
	v_max_f32_e32 v233, v233, v233
	v_max_f32_e32 v234, v234, v234
	v_max_f32_e32 v235, v235, v235
	v_max_f32_e32 v236, v236, v236
	v_max_f32_e32 v237, v237, v237
	v_max_f32_e32 v238, v238, v238
	v_max_f32_e32 v239, v239, v239
	v_max_f32_e32 v240, v240, v240
	v_max_f32_e32 v241, v241, v241
	v_med3_f32 v226, v226, s44, v246
	v_med3_f32 v227, v227, s44, v246
	v_med3_f32 v228, v228, s44, v246
	v_med3_f32 v229, v229, s44, v246
	v_med3_f32 v230, v230, s44, v246
	v_med3_f32 v231, v231, s44, v246
	v_med3_f32 v232, v232, s44, v246
	v_med3_f32 v233, v233, s44, v246
	v_med3_f32 v234, v234, s44, v246
	v_med3_f32 v235, v235, s44, v246
	v_med3_f32 v236, v236, s44, v246
	v_med3_f32 v237, v237, s44, v246
	v_med3_f32 v238, v238, s44, v246
	v_med3_f32 v239, v239, s44, v246
	v_med3_f32 v240, v240, s44, v246
	v_med3_f32 v241, v241, s44, v246
	v_mov_b32_e32 v242, 0
	v_mov_b32_e32 v243, 0
	v_mov_b32_e32 v244, 0
	v_mov_b32_e32 v245, 0
	v_cvt_pk_fp8_f32 v242, v226, v227
	v_cvt_pk_fp8_f32 v243, v230, v231
	v_cvt_pk_fp8_f32 v244, v234, v235
	v_cvt_pk_fp8_f32 v245, v238, v239
	v_cvt_pk_fp8_f32 v242, v228, v229 op_sel:[0,0,1]
	v_cvt_pk_fp8_f32 v243, v232, v233 op_sel:[0,0,1]
	v_cvt_pk_fp8_f32 v244, v236, v237 op_sel:[0,0,1]
	v_cvt_pk_fp8_f32 v245, v240, v241 op_sel:[0,0,1]
	s_nop 0
	global_store_dwordx4 v109, v[242:245], s[6:7]
	s_add_i32 s26, s23, 16
	s_add_i32 s27, s23, 32
	s_waitcnt vmcnt(12)
	v_mul_f32_e32 v144, v218, v144
	v_mul_f32_e32 v145, v218, v145
	v_mul_f32_e32 v146, v218, v146
	v_mul_f32_e32 v147, v218, v147
	ds_write_b128 v209, v[144:147]
	v_mul_f32_e32 v148, v219, v148
	v_mul_f32_e32 v149, v219, v149
	v_mul_f32_e32 v150, v219, v150
	v_mul_f32_e32 v151, v219, v151
	ds_write_b128 v209, v[148:151] offset:1024
	v_mul_f32_e32 v152, v220, v152
	v_mul_f32_e32 v153, v220, v153
	v_mul_f32_e32 v154, v220, v154
	v_mul_f32_e32 v155, v220, v155
	ds_write_b128 v209, v[152:155] offset:2048
	v_mul_f32_e32 v156, v221, v156
	v_mul_f32_e32 v157, v221, v157
	v_mul_f32_e32 v158, v221, v158
	v_mul_f32_e32 v159, v221, v159
	ds_write_b128 v209, v[156:159] offset:3072
	v_mul_f32_e32 v160, v222, v160
	v_mul_f32_e32 v161, v222, v161
	v_mul_f32_e32 v162, v222, v162
	v_mul_f32_e32 v163, v222, v163
	ds_write_b128 v209, v[160:163] offset:4096
	v_mul_f32_e32 v164, v223, v164
	v_mul_f32_e32 v165, v223, v165
	v_mul_f32_e32 v166, v223, v166
	v_mul_f32_e32 v167, v223, v167
	ds_write_b128 v209, v[164:167] offset:5120
	v_mul_f32_e32 v168, v224, v168
	v_mul_f32_e32 v169, v224, v169
	v_mul_f32_e32 v170, v224, v170
	v_mul_f32_e32 v171, v224, v171
	ds_write_b128 v209, v[168:171] offset:6144
	v_mul_f32_e32 v172, v225, v172
	v_mul_f32_e32 v173, v225, v173
	v_mul_f32_e32 v174, v225, v174
	v_mul_f32_e32 v175, v225, v175
	ds_write_b128 v209, v[172:175] offset:7168
	s_waitcnt lgkmcnt(0)
	s_barrier
	s_lshl_b32 s20, s27, 7
	s_cmp_lt_u32 s27, 40
	s_cselect_b32 s21, 0, 0x830
	s_cmp_lt_u32 s27, 72
	s_cselect_b32 s21, s21, 0xfffff030
	s_add_i32 s20, s20, s21
	s_lshl_b32 s20, s20, 2
	s_add_u32 s8, s16, s20
	s_addc_u32 s9, s17, 0
	global_load_dwordx4 v[144:147], v208, s[8:9]
	s_add_u32 s8, s8, 0x16280
	s_addc_u32 s9, s9, 0
	global_load_dwordx4 v[148:151], v208, s[8:9]
	s_add_u32 s8, s8, 0x16280
	s_addc_u32 s9, s9, 0
	global_load_dwordx4 v[152:155], v208, s[8:9]
	s_add_u32 s8, s8, 0x16280
	s_addc_u32 s9, s9, 0
	global_load_dwordx4 v[156:159], v208, s[8:9]
	s_add_u32 s8, s8, 0x16280
	s_addc_u32 s9, s9, 0
	global_load_dwordx4 v[160:163], v208, s[8:9]
	s_add_u32 s8, s8, 0x16280
	s_addc_u32 s9, s9, 0
	global_load_dwordx4 v[164:167], v208, s[8:9]
	s_add_u32 s8, s8, 0x16280
	s_addc_u32 s9, s9, 0
	global_load_dwordx4 v[168:171], v208, s[8:9]
	s_add_u32 s8, s8, 0x16280
	s_addc_u32 s9, s9, 0
	global_load_dwordx4 v[172:175], v208, s[8:9]
	s_mul_i32 s20, s26, 0x80000
	s_add_u32 s6, s18, s20
	s_addc_u32 s7, s19, 0
	s_cmp_lt_u32 s26, 16
	s_cselect_b32 s20, 1, 0
	s_sub_i32 s21, s26, 16
	s_bitcmp0_b32 s21, 2
	s_cselect_b32 s21, 1, 0
	s_cmp_lt_u32 s26, 40
	s_cselect_b32 s21, s21, 0
	s_or_b32 s20, s20, s21
	s_cmp_lg_u32 s20, 0
	s_cselect_b64 s[20:21], -1, 0
	v_cndmask_b32_e64 v108, v100, v104, s[20:21]
	v_cndmask_b32_e64 v109, v101, v105, s[20:21]
	ds_read_b32 v226, v211
	ds_read_b32 v227, v211 offset:512
	ds_read_b32 v228, v211 offset:1024
	ds_read_b32 v229, v211 offset:1536
	ds_read_b32 v230, v211 offset:2048
	ds_read_b32 v231, v211 offset:2560
	ds_read_b32 v232, v211 offset:3072
	ds_read_b32 v233, v211 offset:3584
	ds_read_b32 v234, v211 offset:4096
	ds_read_b32 v235, v211 offset:4608
	ds_read_b32 v236, v211 offset:5120
	ds_read_b32 v237, v211 offset:5632
	ds_read_b32 v238, v211 offset:6144
	ds_read_b32 v239, v211 offset:6656
	ds_read_b32 v240, v211 offset:7168
	ds_read_b32 v241, v211 offset:7680
	s_waitcnt lgkmcnt(0)
; #define GAS __attribute__((address_space(1)))
; #define LAS __attribute__((address_space(3)))
; #define LDS_WAIT() asm volatile("s_waitcnt lgkmcnt(0)" ::: "memory")
; __device__ __forceinline__ unsigned pk4_fp8(float a, float b, float c, float d) {
;     a = fminf(fmaxf(a, -448.f), 448.f); b = fminf(fmaxf(b, -448.f), 448.f); c = fminf(fmaxf(c, -448.f), 448.f); d = fminf(fmaxf(d, -448.f), 448.f);
;     int w = __builtin_amdgcn_cvt_pk_fp8_f32(a, b, 0, false); w = __builtin_amdgcn_cvt_pk_fp8_f32(c, d, w, true); return (unsigned)w; }
;     ...
;     for (int i = 0; i < 32; ++i) { const int k = k0 + 2 * i + (lane >> 5); float x = v[i] * wscale; if (KS) x *= (k < ksplit ? ksA[k] : ksB[k - ksplit]); scr[(2 * i + (lane >> 5)) * 33 + (lane & 31)] = x; }
;     LDS_WAIT(); asm volatile("" ::: "memory");
;     const int c = lane & 7;
; #pragma unroll
;     for (int j = 0; j < 4; ++j) { const int n = (lane >> 3) + 8 * j; const LAS float* s = scr + (8 * c) * 33 + n;
;         const unsigned long long o = (unsigned long long)pg8::pk4_fp8(s[0 * 33], s[1 * 33], s[2 * 33], s[3 * 33]) | ((unsigned long long)pg8::pk4_fp8(s[4 * 33], s[5 * 33], s[6 * 33], s[7 * 33]) << 32);
;         *(GAS unsigned long long*)(WT + (size_t)(n0 + n) * K + k0 + 8 * c) = o; }
	v_max_f32_e32 v226, v226, v226
	v_max_f32_e32 v227, v227, v227
	v_max_f32_e32 v228, v228, v228
	v_max_f32_e32 v229, v229, v229
	v_max_f32_e32 v230, v230, v230
	v_max_f32_e32 v231, v231, v231
	v_max_f32_e32 v232, v232, v232
	v_max_f32_e32 v233, v233, v233
	v_max_f32_e32 v234, v234, v234
	v_max_f32_e32 v235, v235, v235
	v_max_f32_e32 v236, v236, v236
	v_max_f32_e32 v237, v237, v237
	v_max_f32_e32 v238, v238, v238
	v_max_f32_e32 v239, v239, v239
	v_max_f32_e32 v240, v240, v240
	v_max_f32_e32 v241, v241, v241
	v_med3_f32 v226, v226, s44, v246
	v_med3_f32 v227, v227, s44, v246
	v_med3_f32 v228, v228, s44, v246
	v_med3_f32 v229, v229, s44, v246
	v_med3_f32 v230, v230, s44, v246
	v_med3_f32 v231, v231, s44, v246
	v_med3_f32 v232, v232, s44, v246
	v_med3_f32 v233, v233, s44, v246
	v_med3_f32 v234, v234, s44, v246
	v_med3_f32 v235, v235, s44, v246
	v_med3_f32 v236, v236, s44, v246
	v_med3_f32 v237, v237, s44, v246
	v_med3_f32 v238, v238, s44, v246
	v_med3_f32 v239, v239, s44, v246
	v_med3_f32 v240, v240, s44, v246
	v_med3_f32 v241, v241, s44, v246
	v_mov_b32_e32 v242, 0
	v_mov_b32_e32 v243, 0
	v_mov_b32_e32 v244, 0
	v_mov_b32_e32 v245, 0
	v_cvt_pk_fp8_f32 v242, v226, v227
	v_cvt_pk_fp8_f32 v243, v230, v231
	v_cvt_pk_fp8_f32 v244, v234, v235
	v_cvt_pk_fp8_f32 v245, v238, v239
	v_cvt_pk_fp8_f32 v242, v228, v229 op_sel:[0,0,1]
	v_cvt_pk_fp8_f32 v243, v232, v233 op_sel:[0,0,1]
	v_cvt_pk_fp8_f32 v244, v236, v237 op_sel:[0,0,1]
	v_cvt_pk_fp8_f32 v245, v240, v241 op_sel:[0,0,1]
	s_nop 0
	global_store_dwordx4 v108, v[242:245], s[6:7]
	ds_read_b32 v226, v213
	ds_read_b32 v227, v213 offset:512
	ds_read_b32 v228, v213 offset:1024
	ds_read_b32 v229, v213 offset:1536
	ds_read_b32 v230, v213 offset:2048
	ds_read_b32 v231, v213 offset:2560
	ds_read_b32 v232, v213 offset:3072
	ds_read_b32 v233, v213 offset:3584
	ds_read_b32 v234, v213 offset:4096
	ds_read_b32 v235, v213 offset:4608
	ds_read_b32 v236, v213 offset:5120
	ds_read_b32 v237, v213 offset:5632
	ds_read_b32 v238, v213 offset:6144
	ds_read_b32 v239, v213 offset:6656
	ds_read_b32 v240, v213 offset:7168
	ds_read_b32 v241, v213 offset:7680
	s_waitcnt lgkmcnt(0)
	v_max_f32_e32 v226, v226, v226
	v_max_f32_e32 v227, v227, v227
	v_max_f32_e32 v228, v228, v228
	v_max_f32_e32 v229, v229, v229
	v_max_f32_e32 v230, v230, v230
	v_max_f32_e32 v231, v231, v231
	v_max_f32_e32 v232, v232, v232
	v_max_f32_e32 v233, v233, v233
	v_max_f32_e32 v234, v234, v234
	v_max_f32_e32 v235, v235, v235
	v_max_f32_e32 v236, v236, v236
	v_max_f32_e32 v237, v237, v237
	v_max_f32_e32 v238, v238, v238
	v_max_f32_e32 v239, v239, v239
	v_max_f32_e32 v240, v240, v240
	v_max_f32_e32 v241, v241, v241
	v_med3_f32 v226, v226, s44, v246
	v_med3_f32 v227, v227, s44, v246
	v_med3_f32 v228, v228, s44, v246
	v_med3_f32 v229, v229, s44, v246
	v_med3_f32 v230, v230, s44, v246
	v_med3_f32 v231, v231, s44, v246
	v_med3_f32 v232, v232, s44, v246
	v_med3_f32 v233, v233, s44, v246
	v_med3_f32 v234, v234, s44, v246
	v_med3_f32 v235, v235, s44, v246
	v_med3_f32 v236, v236, s44, v246
	v_med3_f32 v237, v237, s44, v246
	v_med3_f32 v238, v238, s44, v246
	v_med3_f32 v239, v239, s44, v246
	v_med3_f32 v240, v240, s44, v246
	v_med3_f32 v241, v241, s44, v246
	v_mov_b32_e32 v242, 0
	v_mov_b32_e32 v243, 0
	v_mov_b32_e32 v244, 0
	v_mov_b32_e32 v245, 0
	v_cvt_pk_fp8_f32 v242, v226, v227
	v_cvt_pk_fp8_f32 v243, v230, v231
	v_cvt_pk_fp8_f32 v244, v234, v235
	v_cvt_pk_fp8_f32 v245, v238, v239
	v_cvt_pk_fp8_f32 v242, v228, v229 op_sel:[0,0,1]
	v_cvt_pk_fp8_f32 v243, v232, v233 op_sel:[0,0,1]
	v_cvt_pk_fp8_f32 v244, v236, v237 op_sel:[0,0,1]
	v_cvt_pk_fp8_f32 v245, v240, v241 op_sel:[0,0,1]
	s_nop 0
	global_store_dwordx4 v109, v[242:245], s[6:7]
	s_add_i32 s26, s23, 24
	s_add_i32 s27, s23, 40
	s_waitcnt vmcnt(12)
	v_mul_f32_e32 v176, v218, v176
	v_mul_f32_e32 v177, v218, v177
	v_mul_f32_e32 v178, v218, v178
	v_mul_f32_e32 v179, v218, v179
	ds_write_b128 v210, v[176:179]
	v_mul_f32_e32 v180, v219, v180
	v_mul_f32_e32 v181, v219, v181
	v_mul_f32_e32 v182, v219, v182
	v_mul_f32_e32 v183, v219, v183
	ds_write_b128 v210, v[180:183] offset:1024
	v_mul_f32_e32 v184, v220, v184
	v_mul_f32_e32 v185, v220, v185
	v_mul_f32_e32 v186, v220, v186
	v_mul_f32_e32 v187, v220, v187
	ds_write_b128 v210, v[184:187] offset:2048
	v_mul_f32_e32 v188, v221, v188
	v_mul_f32_e32 v189, v221, v189
	v_mul_f32_e32 v190, v221, v190
	v_mul_f32_e32 v191, v221, v191
	ds_write_b128 v210, v[188:191] offset:3072
	v_mul_f32_e32 v192, v222, v192
	v_mul_f32_e32 v193, v222, v193
	v_mul_f32_e32 v194, v222, v194
	v_mul_f32_e32 v195, v222, v195
	ds_write_b128 v210, v[192:195] offset:4096
	v_mul_f32_e32 v196, v223, v196
	v_mul_f32_e32 v197, v223, v197
	v_mul_f32_e32 v198, v223, v198
	v_mul_f32_e32 v199, v223, v199
	ds_write_b128 v210, v[196:199] offset:5120
	v_mul_f32_e32 v200, v224, v200
	v_mul_f32_e32 v201, v224, v201
	v_mul_f32_e32 v202, v224, v202
	v_mul_f32_e32 v203, v224, v203
	ds_write_b128 v210, v[200:203] offset:6144
	v_mul_f32_e32 v204, v225, v204
	v_mul_f32_e32 v205, v225, v205
	v_mul_f32_e32 v206, v225, v206
	v_mul_f32_e32 v207, v225, v207
	ds_write_b128 v210, v[204:207] offset:7168
	s_waitcnt lgkmcnt(0)
	s_barrier
; #define GAS __attribute__((address_space(1)))
; #define LAS __attribute__((address_space(3)))
; #define LDS_WAIT() asm volatile("s_waitcnt lgkmcnt(0)" ::: "memory")
; __device__ __forceinline__ unsigned pk4_fp8(float a, float b, float c, float d) {
;     a = fminf(fmaxf(a, -448.f), 448.f); b = fminf(fmaxf(b, -448.f), 448.f); c = fminf(fmaxf(c, -448.f), 448.f); d = fminf(fmaxf(d, -448.f), 448.f);
;     int w = __builtin_amdgcn_cvt_pk_fp8_f32(a, b, 0, false); w = __builtin_amdgcn_cvt_pk_fp8_f32(c, d, w, true); return (unsigned)w; }
;     ...
;     for (int i = 0; i < 32; ++i) { const int k = k0 + 2 * i + (lane >> 5); float x = v[i] * wscale; if (KS) x *= (k < ksplit ? ksA[k] : ksB[k - ksplit]); scr[(2 * i + (lane >> 5)) * 33 + (lane & 31)] = x; }
;     LDS_WAIT(); asm volatile("" ::: "memory");
;     const int c = lane & 7;
; #pragma unroll
;     for (int j = 0; j < 4; ++j) { const int n = (lane >> 3) + 8 * j; const LAS float* s = scr + (8 * c) * 33 + n;
;         const unsigned long long o = (unsigned long long)pg8::pk4_fp8(s[0 * 33], s[1 * 33], s[2 * 33], s[3 * 33]) | ((unsigned long long)pg8::pk4_fp8(s[4 * 33], s[5 * 33], s[6 * 33], s[7 * 33]) << 32);
;         *(GAS unsigned long long*)(WT + (size_t)(n0 + n) * K + k0 + 8 * c) = o; }
	s_lshl_b32 s20, s27, 7
	s_cmp_lt_u32 s27, 40
	s_cselect_b32 s21, 0, 0x830
	s_cmp_lt_u32 s27, 72
	s_cselect_b32 s21, s21, 0xfffff030
	s_add_i32 s20, s20, s21
	s_lshl_b32 s20, s20, 2
	s_add_u32 s8, s16, s20
	s_addc_u32 s9, s17, 0
	global_load_dwordx4 v[176:179], v208, s[8:9]
	s_add_u32 s8, s8, 0x16280
	s_addc_u32 s9, s9, 0
	global_load_dwordx4 v[180:183], v208, s[8:9]
	s_add_u32 s8, s8, 0x16280
	s_addc_u32 s9, s9, 0
	global_load_dwordx4 v[184:187], v208, s[8:9]
	s_add_u32 s8, s8, 0x16280
	s_addc_u32 s9, s9, 0
	global_load_dwordx4 v[188:191], v208, s[8:9]
	s_add_u32 s8, s8, 0x16280
	s_addc_u32 s9, s9, 0
	global_load_dwordx4 v[192:195], v208, s[8:9]
	s_add_u32 s8, s8, 0x16280
	s_addc_u32 s9, s9, 0
	global_load_dwordx4 v[196:199], v208, s[8:9]
	s_add_u32 s8, s8, 0x16280
	s_addc_u32 s9, s9, 0
	global_load_dwordx4 v[200:203], v208, s[8:9]
	s_add_u32 s8, s8, 0x16280
	s_addc_u32 s9, s9, 0
	global_load_dwordx4 v[204:207], v208, s[8:9]
	s_mul_i32 s20, s26, 0x80000
	s_add_u32 s6, s18, s20
	s_addc_u32 s7, s19, 0
	s_cmp_lt_u32 s26, 16
	s_cselect_b32 s20, 1, 0
	s_sub_i32 s21, s26, 16
	s_bitcmp0_b32 s21, 2
	s_cselect_b32 s21, 1, 0
	s_cmp_lt_u32 s26, 40
	s_cselect_b32 s21, s21, 0
	s_or_b32 s20, s20, s21
	s_cmp_lg_u32 s20, 0
	s_cselect_b64 s[20:21], -1, 0
	v_cndmask_b32_e64 v108, v100, v104, s[20:21]
	v_cndmask_b32_e64 v109, v101, v105, s[20:21]
	ds_read_b32 v226, v212
	ds_read_b32 v227, v212 offset:512
	ds_read_b32 v228, v212 offset:1024
	ds_read_b32 v229, v212 offset:1536
	ds_read_b32 v230, v212 offset:2048
	ds_read_b32 v231, v212 offset:2560
	ds_read_b32 v232, v212 offset:3072
	ds_read_b32 v233, v212 offset:3584
	ds_read_b32 v234, v212 offset:4096
	ds_read_b32 v235, v212 offset:4608
	ds_read_b32 v236, v212 offset:5120
	ds_read_b32 v237, v212 offset:5632
	ds_read_b32 v238, v212 offset:6144
	ds_read_b32 v239, v212 offset:6656
	ds_read_b32 v240, v212 offset:7168
	ds_read_b32 v241, v212 offset:7680
	s_waitcnt lgkmcnt(0)
	v_max_f32_e32 v226, v226, v226
	v_max_f32_e32 v227, v227, v227
	v_max_f32_e32 v228, v228, v228
	v_max_f32_e32 v229, v229, v229
	v_max_f32_e32 v230, v230, v230
	v_max_f32_e32 v231, v231, v231
	v_max_f32_e32 v232, v232, v232
	v_max_f32_e32 v233, v233, v233
	v_max_f32_e32 v234, v234, v234
	v_max_f32_e32 v235, v235, v235
	v_max_f32_e32 v236, v236, v236
	v_max_f32_e32 v237, v237, v237
	v_max_f32_e32 v238, v238, v238
	v_max_f32_e32 v239, v239, v239
	v_max_f32_e32 v240, v240, v240
	v_max_f32_e32 v241, v241, v241
	v_med3_f32 v226, v226, s44, v246
	v_med3_f32 v227, v227, s44, v246
	v_med3_f32 v228, v228, s44, v246
	v_med3_f32 v229, v229, s44, v246
	v_med3_f32 v230, v230, s44, v246
	v_med3_f32 v231, v231, s44, v246
	v_med3_f32 v232, v232, s44, v246
	v_med3_f32 v233, v233, s44, v246
	v_med3_f32 v234, v234, s44, v246
	v_med3_f32 v235, v235, s44, v246
	v_med3_f32 v236, v236, s44, v246
	v_med3_f32 v237, v237, s44, v246
	v_med3_f32 v238, v238, s44, v246
	v_med3_f32 v239, v239, s44, v246
	v_med3_f32 v240, v240, s44, v246
	v_med3_f32 v241, v241, s44, v246
	v_mov_b32_e32 v242, 0
	v_mov_b32_e32 v243, 0
	v_mov_b32_e32 v244, 0
	v_mov_b32_e32 v245, 0
	v_cvt_pk_fp8_f32 v242, v226, v227
	v_cvt_pk_fp8_f32 v243, v230, v231
	v_cvt_pk_fp8_f32 v244, v234, v235
	v_cvt_pk_fp8_f32 v245, v238, v239
	v_cvt_pk_fp8_f32 v242, v228, v229 op_sel:[0,0,1]
	v_cvt_pk_fp8_f32 v243, v232, v233 op_sel:[0,0,1]
	v_cvt_pk_fp8_f32 v244, v236, v237 op_sel:[0,0,1]
	v_cvt_pk_fp8_f32 v245, v240, v241 op_sel:[0,0,1]
	s_nop 0
	global_store_dwordx4 v108, v[242:245], s[6:7]
	ds_read_b32 v226, v214
	ds_read_b32 v227, v214 offset:512
	ds_read_b32 v228, v214 offset:1024
	ds_read_b32 v229, v214 offset:1536
	ds_read_b32 v230, v214 offset:2048
	ds_read_b32 v231, v214 offset:2560
	ds_read_b32 v232, v214 offset:3072
	ds_read_b32 v233, v214 offset:3584
	ds_read_b32 v234, v214 offset:4096
	ds_read_b32 v235, v214 offset:4608
	ds_read_b32 v236, v214 offset:5120
	ds_read_b32 v237, v214 offset:5632
	ds_read_b32 v238, v214 offset:6144
	ds_read_b32 v239, v214 offset:6656
	ds_read_b32 v240, v214 offset:7168
	ds_read_b32 v241, v214 offset:7680
	s_waitcnt lgkmcnt(0)
	v_max_f32_e32 v226, v226, v226
	v_max_f32_e32 v227, v227, v227
	v_max_f32_e32 v228, v228, v228
	v_max_f32_e32 v229, v229, v229
	v_max_f32_e32 v230, v230, v230
	v_max_f32_e32 v231, v231, v231
	v_max_f32_e32 v232, v232, v232
	v_max_f32_e32 v233, v233, v233
	v_max_f32_e32 v234, v234, v234
	v_max_f32_e32 v235, v235, v235
	v_max_f32_e32 v236, v236, v236
	v_max_f32_e32 v237, v237, v237
	v_max_f32_e32 v238, v238, v238
	v_max_f32_e32 v239, v239, v239
	v_max_f32_e32 v240, v240, v240
	v_max_f32_e32 v241, v241, v241
	v_med3_f32 v226, v226, s44, v246
	v_med3_f32 v227, v227, s44, v246
	v_med3_f32 v228, v228, s44, v246
	v_med3_f32 v229, v229, s44, v246
	v_med3_f32 v230, v230, s44, v246
	v_med3_f32 v231, v231, s44, v246
	v_med3_f32 v232, v232, s44, v246
	v_med3_f32 v233, v233, s44, v246
	v_med3_f32 v234, v234, s44, v246
	v_med3_f32 v235, v235, s44, v246
	v_med3_f32 v236, v236, s44, v246
	v_med3_f32 v237, v237, s44, v246
	v_med3_f32 v238, v238, s44, v246
	v_med3_f32 v239, v239, s44, v246
	v_med3_f32 v240, v240, s44, v246
	v_med3_f32 v241, v241, s44, v246
	v_mov_b32_e32 v242, 0
	v_mov_b32_e32 v243, 0
	v_mov_b32_e32 v244, 0
	v_mov_b32_e32 v245, 0
	v_cvt_pk_fp8_f32 v242, v226, v227
	v_cvt_pk_fp8_f32 v243, v230, v231
	v_cvt_pk_fp8_f32 v244, v234, v235
	v_cvt_pk_fp8_f32 v245, v238, v239
	v_cvt_pk_fp8_f32 v242, v228, v229 op_sel:[0,0,1]
	v_cvt_pk_fp8_f32 v243, v232, v233 op_sel:[0,0,1]
	v_cvt_pk_fp8_f32 v244, v236, v237 op_sel:[0,0,1]
	v_cvt_pk_fp8_f32 v245, v240, v241 op_sel:[0,0,1]
	s_nop 0
	global_store_dwordx4 v109, v[242:245], s[6:7]
	s_add_i32 s26, s23, 32
	s_add_i32 s27, s23, 48
	s_waitcnt vmcnt(12)
; #define GAS __attribute__((address_space(1)))
; #define LAS __attribute__((address_space(3)))
; #define LDS_WAIT() asm volatile("s_waitcnt lgkmcnt(0)" ::: "memory")
; __device__ __forceinline__ int src_col_in(int c) {
;     if (c < 5120) { const int blk = c >> 7, p = c & 127; const bool rope = blk < 16 || ((((blk - 16) >> 2) & 1) == 0); const int d = rope ? (p >> 1) + 64 * (p & 1) : p; return blk * 128 + d; }
;     if (c < OFF_Z) return c + 2096;
;     if (c < OFF_G) return c - 4048;
;     if (c < OFF_DT) return 5120 + (c - OFF_G);
;     if (c < NSRC) return c;
;     return -1;
; }
;     const int pr = item >> 1, kb = 2 * (pr / nblk) + (item & 1), nb = pr % nblk, k0 = 64 * kb, n0 = 32 * nb;
;     const int nr = n0 + (lane & 31); const int sc = MAP == 1 ? src_col_in(nr) : nr;
;     float v[32];
; #pragma unroll
;     for (int i = 0; i < 32; ++i) v[i] = sc >= 0 ? W[(size_t)(k0 + 2 * i + (lane >> 5)) * Nsrc + sc] : 0.f;
; #pragma unroll
;     for (int i = 0; i < 32; ++i) { const int k = k0 + 2 * i + (lane >> 5); float x = v[i] * wscale; if (KS) x *= (k < ksplit ? ksA[k] : ksB[k - ksplit]); scr[(2 * i + (lane >> 5)) * 33 + (lane & 31)] = x; }
;     LDS_WAIT(); asm volatile("" ::: "memory");
;     const int c = lane & 7;
; #pragma unroll
;     for (int j = 0; j < 4; ++j) { const int n = (lane >> 3) + 8 * j; const LAS float* s = scr + (8 * c) * 33 + n;
;         const unsigned long long o = (unsigned long long)pg8::pk4_fp8(s[0 * 33], s[1 * 33], s[2 * 33], s[3 * 33]) | ((unsigned long long)pg8::pk4_fp8(s[4 * 33], s[5 * 33], s[6 * 33], s[7 * 33]) << 32);
;         *(GAS unsigned long long*)(WT + (size_t)(n0 + n) * K + k0 + 8 * c) = o; }
;     LDS_WAIT(); asm volatile("" ::: "memory");
; }
	v_mul_f32_e32 v144, v218, v144
	v_mul_f32_e32 v145, v218, v145
	v_mul_f32_e32 v146, v218, v146
	v_mul_f32_e32 v147, v218, v147
	ds_write_b128 v209, v[144:147]
	v_mul_f32_e32 v148, v219, v148
	v_mul_f32_e32 v149, v219, v149
	v_mul_f32_e32 v150, v219, v150
	v_mul_f32_e32 v151, v219, v151
	ds_write_b128 v209, v[148:151] offset:1024
	v_mul_f32_e32 v152, v220, v152
	v_mul_f32_e32 v153, v220, v153
	v_mul_f32_e32 v154, v220, v154
	v_mul_f32_e32 v155, v220, v155
	ds_write_b128 v209, v[152:155] offset:2048
	v_mul_f32_e32 v156, v221, v156
	v_mul_f32_e32 v157, v221, v157
	v_mul_f32_e32 v158, v221, v158
	v_mul_f32_e32 v159, v221, v159
	ds_write_b128 v209, v[156:159] offset:3072
	v_mul_f32_e32 v160, v222, v160
	v_mul_f32_e32 v161, v222, v161
	v_mul_f32_e32 v162, v222, v162
	v_mul_f32_e32 v163, v222, v163
	ds_write_b128 v209, v[160:163] offset:4096
	v_mul_f32_e32 v164, v223, v164
	v_mul_f32_e32 v165, v223, v165
	v_mul_f32_e32 v166, v223, v166
	v_mul_f32_e32 v167, v223, v167
	ds_write_b128 v209, v[164:167] offset:5120
	v_mul_f32_e32 v168, v224, v168
	v_mul_f32_e32 v169, v224, v169
	v_mul_f32_e32 v170, v224, v170
	v_mul_f32_e32 v171, v224, v171
	ds_write_b128 v209, v[168:171] offset:6144
	v_mul_f32_e32 v172, v225, v172
	v_mul_f32_e32 v173, v225, v173
	v_mul_f32_e32 v174, v225, v174
	v_mul_f32_e32 v175, v225, v175
	ds_write_b128 v209, v[172:175] offset:7168
	s_waitcnt lgkmcnt(0)
	s_barrier
	s_lshl_b32 s20, s27, 7
	s_cmp_lt_u32 s27, 40
	s_cselect_b32 s21, 0, 0x830
	s_cmp_lt_u32 s27, 72
	s_cselect_b32 s21, s21, 0xfffff030
	s_add_i32 s20, s20, s21
	s_lshl_b32 s20, s20, 2
	s_add_u32 s8, s16, s20
	s_addc_u32 s9, s17, 0
	global_load_dwordx4 v[144:147], v208, s[8:9]
	s_add_u32 s8, s8, 0x16280
	s_addc_u32 s9, s9, 0
	global_load_dwordx4 v[148:151], v208, s[8:9]
	s_add_u32 s8, s8, 0x16280
	s_addc_u32 s9, s9, 0
	global_load_dwordx4 v[152:155], v208, s[8:9]
	s_add_u32 s8, s8, 0x16280
	s_addc_u32 s9, s9, 0
	global_load_dwordx4 v[156:159], v208, s[8:9]
	s_add_u32 s8, s8, 0x16280
	s_addc_u32 s9, s9, 0
	global_load_dwordx4 v[160:163], v208, s[8:9]
	s_add_u32 s8, s8, 0x16280
	s_addc_u32 s9, s9, 0
	global_load_dwordx4 v[164:167], v208, s[8:9]
	s_add_u32 s8, s8, 0x16280
	s_addc_u32 s9, s9, 0
	global_load_dwordx4 v[168:171], v208, s[8:9]
	s_add_u32 s8, s8, 0x16280
	s_addc_u32 s9, s9, 0
	global_load_dwordx4 v[172:175], v208, s[8:9]
	s_mul_i32 s20, s26, 0x80000
	s_add_u32 s6, s18, s20
	s_addc_u32 s7, s19, 0
	s_cmp_lt_u32 s26, 16
	s_cselect_b32 s20, 1, 0
	s_sub_i32 s21, s26, 16
	s_bitcmp0_b32 s21, 2
	s_cselect_b32 s21, 1, 0
	s_cmp_lt_u32 s26, 40
	s_cselect_b32 s21, s21, 0
	s_or_b32 s20, s20, s21
	s_cmp_lg_u32 s20, 0
	s_cselect_b64 s[20:21], -1, 0
	v_cndmask_b32_e64 v108, v100, v104, s[20:21]
	v_cndmask_b32_e64 v109, v101, v105, s[20:21]
	ds_read_b32 v226, v211
	ds_read_b32 v227, v211 offset:512
	ds_read_b32 v228, v211 offset:1024
	ds_read_b32 v229, v211 offset:1536
	ds_read_b32 v230, v211 offset:2048
	ds_read_b32 v231, v211 offset:2560
	ds_read_b32 v232, v211 offset:3072
	ds_read_b32 v233, v211 offset:3584
	ds_read_b32 v234, v211 offset:4096
	ds_read_b32 v235, v211 offset:4608
	ds_read_b32 v236, v211 offset:5120
	ds_read_b32 v237, v211 offset:5632
	ds_read_b32 v238, v211 offset:6144
	ds_read_b32 v239, v211 offset:6656
	ds_read_b32 v240, v211 offset:7168
	ds_read_b32 v241, v211 offset:7680
	s_waitcnt lgkmcnt(0)
	v_max_f32_e32 v226, v226, v226
	v_max_f32_e32 v227, v227, v227
	v_max_f32_e32 v228, v228, v228
	v_max_f32_e32 v229, v229, v229
	v_max_f32_e32 v230, v230, v230
	v_max_f32_e32 v231, v231, v231
	v_max_f32_e32 v232, v232, v232
	v_max_f32_e32 v233, v233, v233
	v_max_f32_e32 v234, v234, v234
	v_max_f32_e32 v235, v235, v235
	v_max_f32_e32 v236, v236, v236
	v_max_f32_e32 v237, v237, v237
	v_max_f32_e32 v238, v238, v238
	v_max_f32_e32 v239, v239, v239
	v_max_f32_e32 v240, v240, v240
	v_max_f32_e32 v241, v241, v241
	v_med3_f32 v226, v226, s44, v246
	v_med3_f32 v227, v227, s44, v246
	v_med3_f32 v228, v228, s44, v246
	v_med3_f32 v229, v229, s44, v246
	v_med3_f32 v230, v230, s44, v246
	v_med3_f32 v231, v231, s44, v246
	v_med3_f32 v232, v232, s44, v246
	v_med3_f32 v233, v233, s44, v246
	v_med3_f32 v234, v234, s44, v246
	v_med3_f32 v235, v235, s44, v246
	v_med3_f32 v236, v236, s44, v246
	v_med3_f32 v237, v237, s44, v246
	v_med3_f32 v238, v238, s44, v246
	v_med3_f32 v239, v239, s44, v246
	v_med3_f32 v240, v240, s44, v246
	v_med3_f32 v241, v241, s44, v246
	v_mov_b32_e32 v242, 0
	v_mov_b32_e32 v243, 0
	v_mov_b32_e32 v244, 0
	v_mov_b32_e32 v245, 0
	v_cvt_pk_fp8_f32 v242, v226, v227
	v_cvt_pk_fp8_f32 v243, v230, v231
	v_cvt_pk_fp8_f32 v244, v234, v235
	v_cvt_pk_fp8_f32 v245, v238, v239
	v_cvt_pk_fp8_f32 v242, v228, v229 op_sel:[0,0,1]
	v_cvt_pk_fp8_f32 v243, v232, v233 op_sel:[0,0,1]
	v_cvt_pk_fp8_f32 v244, v236, v237 op_sel:[0,0,1]
	v_cvt_pk_fp8_f32 v245, v240, v241 op_sel:[0,0,1]
	s_nop 0
	global_store_dwordx4 v108, v[242:245], s[6:7]
	ds_read_b32 v226, v213
	ds_read_b32 v227, v213 offset:512
	ds_read_b32 v228, v213 offset:1024
	ds_read_b32 v229, v213 offset:1536
	ds_read_b32 v230, v213 offset:2048
	ds_read_b32 v231, v213 offset:2560
	ds_read_b32 v232, v213 offset:3072
	ds_read_b32 v233, v213 offset:3584
	ds_read_b32 v234, v213 offset:4096
	ds_read_b32 v235, v213 offset:4608
	ds_read_b32 v236, v213 offset:5120
	ds_read_b32 v237, v213 offset:5632
	ds_read_b32 v238, v213 offset:6144
	ds_read_b32 v239, v213 offset:6656
	ds_read_b32 v240, v213 offset:7168
	ds_read_b32 v241, v213 offset:7680
	s_waitcnt lgkmcnt(0)
; #define GAS __attribute__((address_space(1)))
; #define LAS __attribute__((address_space(3)))
; #define LDS_WAIT() asm volatile("s_waitcnt lgkmcnt(0)" ::: "memory")
; __device__ __forceinline__ unsigned pk4_fp8(float a, float b, float c, float d) {
;     a = fminf(fmaxf(a, -448.f), 448.f); b = fminf(fmaxf(b, -448.f), 448.f); c = fminf(fmaxf(c, -448.f), 448.f); d = fminf(fmaxf(d, -448.f), 448.f);
;     int w = __builtin_amdgcn_cvt_pk_fp8_f32(a, b, 0, false); w = __builtin_amdgcn_cvt_pk_fp8_f32(c, d, w, true); return (unsigned)w; }
;     const int pr = item >> 1, kb = 2 * (pr / nblk) + (item & 1), nb = pr % nblk, k0 = 64 * kb, n0 = 32 * nb;
;     const int nr = n0 + (lane & 31); const int sc = MAP == 1 ? src_col_in(nr) : nr;
;     float v[32];
; #pragma unroll
;     for (int i = 0; i < 32; ++i) v[i] = sc >= 0 ? W[(size_t)(k0 + 2 * i + (lane >> 5)) * Nsrc + sc] : 0.f;
; #pragma unroll
;     for (int i = 0; i < 32; ++i) { const int k = k0 + 2 * i + (lane >> 5); float x = v[i] * wscale; if (KS) x *= (k < ksplit ? ksA[k] : ksB[k - ksplit]); scr[(2 * i + (lane >> 5)) * 33 + (lane & 31)] = x; }
;     LDS_WAIT(); asm volatile("" ::: "memory");
;     const int c = lane & 7;
; #pragma unroll
;     for (int j = 0; j < 4; ++j) { const int n = (lane >> 3) + 8 * j; const LAS float* s = scr + (8 * c) * 33 + n;
;         const unsigned long long o = (unsigned long long)pg8::pk4_fp8(s[0 * 33], s[1 * 33], s[2 * 33], s[3 * 33]) | ((unsigned long long)pg8::pk4_fp8(s[4 * 33], s[5 * 33], s[6 * 33], s[7 * 33]) << 32);
;         *(GAS unsigned long long*)(WT + (size_t)(n0 + n) * K + k0 + 8 * c) = o; }
;     LDS_WAIT(); asm volatile("" ::: "memory");
; }
	v_max_f32_e32 v226, v226, v226
	v_max_f32_e32 v227, v227, v227
	v_max_f32_e32 v228, v228, v228
	v_max_f32_e32 v229, v229, v229
	v_max_f32_e32 v230, v230, v230
	v_max_f32_e32 v231, v231, v231
	v_max_f32_e32 v232, v232, v232
	v_max_f32_e32 v233, v233, v233
	v_max_f32_e32 v234, v234, v234
	v_max_f32_e32 v235, v235, v235
	v_max_f32_e32 v236, v236, v236
	v_max_f32_e32 v237, v237, v237
	v_max_f32_e32 v238, v238, v238
	v_max_f32_e32 v239, v239, v239
	v_max_f32_e32 v240, v240, v240
	v_max_f32_e32 v241, v241, v241
	v_med3_f32 v226, v226, s44, v246
	v_med3_f32 v227, v227, s44, v246
	v_med3_f32 v228, v228, s44, v246
	v_med3_f32 v229, v229, s44, v246
	v_med3_f32 v230, v230, s44, v246
	v_med3_f32 v231, v231, s44, v246
	v_med3_f32 v232, v232, s44, v246
	v_med3_f32 v233, v233, s44, v246
	v_med3_f32 v234, v234, s44, v246
	v_med3_f32 v235, v235, s44, v246
	v_med3_f32 v236, v236, s44, v246
	v_med3_f32 v237, v237, s44, v246
	v_med3_f32 v238, v238, s44, v246
	v_med3_f32 v239, v239, s44, v246
	v_med3_f32 v240, v240, s44, v246
	v_med3_f32 v241, v241, s44, v246
	v_mov_b32_e32 v242, 0
	v_mov_b32_e32 v243, 0
	v_mov_b32_e32 v244, 0
	v_mov_b32_e32 v245, 0
	v_cvt_pk_fp8_f32 v242, v226, v227
	v_cvt_pk_fp8_f32 v243, v230, v231
	v_cvt_pk_fp8_f32 v244, v234, v235
	v_cvt_pk_fp8_f32 v245, v238, v239
	v_cvt_pk_fp8_f32 v242, v228, v229 op_sel:[0,0,1]
	v_cvt_pk_fp8_f32 v243, v232, v233 op_sel:[0,0,1]
	v_cvt_pk_fp8_f32 v244, v236, v237 op_sel:[0,0,1]
	v_cvt_pk_fp8_f32 v245, v240, v241 op_sel:[0,0,1]
	s_nop 0
	global_store_dwordx4 v109, v[242:245], s[6:7]
	s_add_i32 s26, s23, 40
	s_add_i32 s27, s23, 56
	s_waitcnt vmcnt(12)
	v_mul_f32_e32 v176, v218, v176
	v_mul_f32_e32 v177, v218, v177
	v_mul_f32_e32 v178, v218, v178
	v_mul_f32_e32 v179, v218, v179
	ds_write_b128 v210, v[176:179]
	v_mul_f32_e32 v180, v219, v180
	v_mul_f32_e32 v181, v219, v181
	v_mul_f32_e32 v182, v219, v182
	v_mul_f32_e32 v183, v219, v183
	ds_write_b128 v210, v[180:183] offset:1024
	v_mul_f32_e32 v184, v220, v184
	v_mul_f32_e32 v185, v220, v185
	v_mul_f32_e32 v186, v220, v186
	v_mul_f32_e32 v187, v220, v187
	ds_write_b128 v210, v[184:187] offset:2048
	v_mul_f32_e32 v188, v221, v188
	v_mul_f32_e32 v189, v221, v189
	v_mul_f32_e32 v190, v221, v190
	v_mul_f32_e32 v191, v221, v191
	ds_write_b128 v210, v[188:191] offset:3072
	v_mul_f32_e32 v192, v222, v192
	v_mul_f32_e32 v193, v222, v193
	v_mul_f32_e32 v194, v222, v194
	v_mul_f32_e32 v195, v222, v195
	ds_write_b128 v210, v[192:195] offset:4096
	v_mul_f32_e32 v196, v223, v196
	v_mul_f32_e32 v197, v223, v197
	v_mul_f32_e32 v198, v223, v198
	v_mul_f32_e32 v199, v223, v199
	ds_write_b128 v210, v[196:199] offset:5120
	v_mul_f32_e32 v200, v224, v200
	v_mul_f32_e32 v201, v224, v201
	v_mul_f32_e32 v202, v224, v202
	v_mul_f32_e32 v203, v224, v203
	ds_write_b128 v210, v[200:203] offset:6144
	v_mul_f32_e32 v204, v225, v204
	v_mul_f32_e32 v205, v225, v205
	v_mul_f32_e32 v206, v225, v206
	v_mul_f32_e32 v207, v225, v207
	ds_write_b128 v210, v[204:207] offset:7168
	s_waitcnt lgkmcnt(0)
	s_barrier
	s_lshl_b32 s20, s27, 7
	s_cmp_lt_u32 s27, 40
	s_cselect_b32 s21, 0, 0x830
	s_cmp_lt_u32 s27, 72
	s_cselect_b32 s21, s21, 0xfffff030
	s_add_i32 s20, s20, s21
	s_lshl_b32 s20, s20, 2
	s_add_u32 s8, s16, s20
	s_addc_u32 s9, s17, 0
	global_load_dwordx4 v[176:179], v208, s[8:9]
	s_add_u32 s8, s8, 0x16280
	s_addc_u32 s9, s9, 0
	global_load_dwordx4 v[180:183], v208, s[8:9]
	s_add_u32 s8, s8, 0x16280
	s_addc_u32 s9, s9, 0
	global_load_dwordx4 v[184:187], v208, s[8:9]
	s_add_u32 s8, s8, 0x16280
	s_addc_u32 s9, s9, 0
	global_load_dwordx4 v[188:191], v208, s[8:9]
	s_add_u32 s8, s8, 0x16280
	s_addc_u32 s9, s9, 0
	global_load_dwordx4 v[192:195], v208, s[8:9]
	s_add_u32 s8, s8, 0x16280
	s_addc_u32 s9, s9, 0
	global_load_dwordx4 v[196:199], v208, s[8:9]
	s_add_u32 s8, s8, 0x16280
	s_addc_u32 s9, s9, 0
	global_load_dwordx4 v[200:203], v208, s[8:9]
	s_add_u32 s8, s8, 0x16280
	s_addc_u32 s9, s9, 0
	global_load_dwordx4 v[204:207], v208, s[8:9]
	s_mul_i32 s20, s26, 0x80000
	s_add_u32 s6, s18, s20
	s_addc_u32 s7, s19, 0
	s_cmp_lt_u32 s26, 16
	s_cselect_b32 s20, 1, 0
	s_sub_i32 s21, s26, 16
	s_bitcmp0_b32 s21, 2
	s_cselect_b32 s21, 1, 0
	s_cmp_lt_u32 s26, 40
	s_cselect_b32 s21, s21, 0
	s_or_b32 s20, s20, s21
	s_cmp_lg_u32 s20, 0
	s_cselect_b64 s[20:21], -1, 0
	v_cndmask_b32_e64 v108, v100, v104, s[20:21]
	v_cndmask_b32_e64 v109, v101, v105, s[20:21]
	ds_read_b32 v226, v212
	ds_read_b32 v227, v212 offset:512
	ds_read_b32 v228, v212 offset:1024
	ds_read_b32 v229, v212 offset:1536
	ds_read_b32 v230, v212 offset:2048
	ds_read_b32 v231, v212 offset:2560
	ds_read_b32 v232, v212 offset:3072
	ds_read_b32 v233, v212 offset:3584
	ds_read_b32 v234, v212 offset:4096
	ds_read_b32 v235, v212 offset:4608
	ds_read_b32 v236, v212 offset:5120
	ds_read_b32 v237, v212 offset:5632
	ds_read_b32 v238, v212 offset:6144
	ds_read_b32 v239, v212 offset:6656
	ds_read_b32 v240, v212 offset:7168
	ds_read_b32 v241, v212 offset:7680
	s_waitcnt lgkmcnt(0)
; #define GAS __attribute__((address_space(1)))
; #define LAS __attribute__((address_space(3)))
; #define LDS_WAIT() asm volatile("s_waitcnt lgkmcnt(0)" ::: "memory")
; __device__ __forceinline__ unsigned pk4_fp8(float a, float b, float c, float d) {
;     a = fminf(fmaxf(a, -448.f), 448.f); b = fminf(fmaxf(b, -448.f), 448.f); c = fminf(fmaxf(c, -448.f), 448.f); d = fminf(fmaxf(d, -448.f), 448.f);
;     int w = __builtin_amdgcn_cvt_pk_fp8_f32(a, b, 0, false); w = __builtin_amdgcn_cvt_pk_fp8_f32(c, d, w, true); return (unsigned)w; }
;     const int pr = item >> 1, kb = 2 * (pr / nblk) + (item & 1), nb = pr % nblk, k0 = 64 * kb, n0 = 32 * nb;
;     const int nr = n0 + (lane & 31); const int sc = MAP == 1 ? src_col_in(nr) : nr;
;     float v[32];
; #pragma unroll
;     for (int i = 0; i < 32; ++i) v[i] = sc >= 0 ? W[(size_t)(k0 + 2 * i + (lane >> 5)) * Nsrc + sc] : 0.f;
; #pragma unroll
;     for (int i = 0; i < 32; ++i) { const int k = k0 + 2 * i + (lane >> 5); float x = v[i] * wscale; if (KS) x *= (k < ksplit ? ksA[k] : ksB[k - ksplit]); scr[(2 * i + (lane >> 5)) * 33 + (lane & 31)] = x; }
;     LDS_WAIT(); asm volatile("" ::: "memory");
;     const int c = lane & 7;
; #pragma unroll
;     for (int j = 0; j < 4; ++j) { const int n = (lane >> 3) + 8 * j; const LAS float* s = scr + (8 * c) * 33 + n;
;         const unsigned long long o = (unsigned long long)pg8::pk4_fp8(s[0 * 33], s[1 * 33], s[2 * 33], s[3 * 33]) | ((unsigned long long)pg8::pk4_fp8(s[4 * 33], s[5 * 33], s[6 * 33], s[7 * 33]) << 32);
;         *(GAS unsigned long long*)(WT + (size_t)(n0 + n) * K + k0 + 8 * c) = o; }
;     LDS_WAIT(); asm volatile("" ::: "memory");
; }
	v_max_f32_e32 v226, v226, v226
	v_max_f32_e32 v227, v227, v227
	v_max_f32_e32 v228, v228, v228
	v_max_f32_e32 v229, v229, v229
	v_max_f32_e32 v230, v230, v230
	v_max_f32_e32 v231, v231, v231
	v_max_f32_e32 v232, v232, v232
	v_max_f32_e32 v233, v233, v233
	v_max_f32_e32 v234, v234, v234
	v_max_f32_e32 v235, v235, v235
	v_max_f32_e32 v236, v236, v236
	v_max_f32_e32 v237, v237, v237
	v_max_f32_e32 v238, v238, v238
	v_max_f32_e32 v239, v239, v239
	v_max_f32_e32 v240, v240, v240
	v_max_f32_e32 v241, v241, v241
	v_med3_f32 v226, v226, s44, v246
	v_med3_f32 v227, v227, s44, v246
	v_med3_f32 v228, v228, s44, v246
	v_med3_f32 v229, v229, s44, v246
	v_med3_f32 v230, v230, s44, v246
	v_med3_f32 v231, v231, s44, v246
	v_med3_f32 v232, v232, s44, v246
	v_med3_f32 v233, v233, s44, v246
	v_med3_f32 v234, v234, s44, v246
	v_med3_f32 v235, v235, s44, v246
	v_med3_f32 v236, v236, s44, v246
	v_med3_f32 v237, v237, s44, v246
	v_med3_f32 v238, v238, s44, v246
	v_med3_f32 v239, v239, s44, v246
	v_med3_f32 v240, v240, s44, v246
	v_med3_f32 v241, v241, s44, v246
	v_mov_b32_e32 v242, 0
	v_mov_b32_e32 v243, 0
	v_mov_b32_e32 v244, 0
	v_mov_b32_e32 v245, 0
	v_cvt_pk_fp8_f32 v242, v226, v227
	v_cvt_pk_fp8_f32 v243, v230, v231
	v_cvt_pk_fp8_f32 v244, v234, v235
	v_cvt_pk_fp8_f32 v245, v238, v239
	v_cvt_pk_fp8_f32 v242, v228, v229 op_sel:[0,0,1]
	v_cvt_pk_fp8_f32 v243, v232, v233 op_sel:[0,0,1]
	v_cvt_pk_fp8_f32 v244, v236, v237 op_sel:[0,0,1]
	v_cvt_pk_fp8_f32 v245, v240, v241 op_sel:[0,0,1]
	s_nop 0
	global_store_dwordx4 v108, v[242:245], s[6:7]
	ds_read_b32 v226, v214
	ds_read_b32 v227, v214 offset:512
	ds_read_b32 v228, v214 offset:1024
	ds_read_b32 v229, v214 offset:1536
	ds_read_b32 v230, v214 offset:2048
	ds_read_b32 v231, v214 offset:2560
	ds_read_b32 v232, v214 offset:3072
	ds_read_b32 v233, v214 offset:3584
	ds_read_b32 v234, v214 offset:4096
	ds_read_b32 v235, v214 offset:4608
	ds_read_b32 v236, v214 offset:5120
	ds_read_b32 v237, v214 offset:5632
	ds_read_b32 v238, v214 offset:6144
	ds_read_b32 v239, v214 offset:6656
	ds_read_b32 v240, v214 offset:7168
	ds_read_b32 v241, v214 offset:7680
	s_waitcnt lgkmcnt(0)
	v_max_f32_e32 v226, v226, v226
	v_max_f32_e32 v227, v227, v227
	v_max_f32_e32 v228, v228, v228
	v_max_f32_e32 v229, v229, v229
	v_max_f32_e32 v230, v230, v230
	v_max_f32_e32 v231, v231, v231
	v_max_f32_e32 v232, v232, v232
	v_max_f32_e32 v233, v233, v233
	v_max_f32_e32 v234, v234, v234
	v_max_f32_e32 v235, v235, v235
	v_max_f32_e32 v236, v236, v236
	v_max_f32_e32 v237, v237, v237
	v_max_f32_e32 v238, v238, v238
	v_max_f32_e32 v239, v239, v239
	v_max_f32_e32 v240, v240, v240
	v_max_f32_e32 v241, v241, v241
	v_med3_f32 v226, v226, s44, v246
	v_med3_f32 v227, v227, s44, v246
	v_med3_f32 v228, v228, s44, v246
	v_med3_f32 v229, v229, s44, v246
	v_med3_f32 v230, v230, s44, v246
	v_med3_f32 v231, v231, s44, v246
	v_med3_f32 v232, v232, s44, v246
	v_med3_f32 v233, v233, s44, v246
	v_med3_f32 v234, v234, s44, v246
	v_med3_f32 v235, v235, s44, v246
	v_med3_f32 v236, v236, s44, v246
	v_med3_f32 v237, v237, s44, v246
	v_med3_f32 v238, v238, s44, v246
	v_med3_f32 v239, v239, s44, v246
	v_med3_f32 v240, v240, s44, v246
	v_med3_f32 v241, v241, s44, v246
	v_mov_b32_e32 v242, 0
	v_mov_b32_e32 v243, 0
	v_mov_b32_e32 v244, 0
	v_mov_b32_e32 v245, 0
	v_cvt_pk_fp8_f32 v242, v226, v227
	v_cvt_pk_fp8_f32 v243, v230, v231
	v_cvt_pk_fp8_f32 v244, v234, v235
	v_cvt_pk_fp8_f32 v245, v238, v239
	v_cvt_pk_fp8_f32 v242, v228, v229 op_sel:[0,0,1]
	v_cvt_pk_fp8_f32 v243, v232, v233 op_sel:[0,0,1]
	v_cvt_pk_fp8_f32 v244, v236, v237 op_sel:[0,0,1]
	v_cvt_pk_fp8_f32 v245, v240, v241 op_sel:[0,0,1]
	s_nop 0
	global_store_dwordx4 v109, v[242:245], s[6:7]
	s_add_i32 s26, s23, 48
	s_add_i32 s27, s23, 64
	s_waitcnt vmcnt(12)
	v_mul_f32_e32 v144, v218, v144
	v_mul_f32_e32 v145, v218, v145
	v_mul_f32_e32 v146, v218, v146
	v_mul_f32_e32 v147, v218, v147
	ds_write_b128 v209, v[144:147]
	v_mul_f32_e32 v148, v219, v148
	v_mul_f32_e32 v149, v219, v149
	v_mul_f32_e32 v150, v219, v150
	v_mul_f32_e32 v151, v219, v151
	ds_write_b128 v209, v[148:151] offset:1024
	v_mul_f32_e32 v152, v220, v152
	v_mul_f32_e32 v153, v220, v153
	v_mul_f32_e32 v154, v220, v154
	v_mul_f32_e32 v155, v220, v155
	ds_write_b128 v209, v[152:155] offset:2048
	v_mul_f32_e32 v156, v221, v156
	v_mul_f32_e32 v157, v221, v157
	v_mul_f32_e32 v158, v221, v158
	v_mul_f32_e32 v159, v221, v159
	ds_write_b128 v209, v[156:159] offset:3072
	v_mul_f32_e32 v160, v222, v160
	v_mul_f32_e32 v161, v222, v161
	v_mul_f32_e32 v162, v222, v162
	v_mul_f32_e32 v163, v222, v163
	ds_write_b128 v209, v[160:163] offset:4096
	v_mul_f32_e32 v164, v223, v164
	v_mul_f32_e32 v165, v223, v165
	v_mul_f32_e32 v166, v223, v166
	v_mul_f32_e32 v167, v223, v167
	ds_write_b128 v209, v[164:167] offset:5120
	v_mul_f32_e32 v168, v224, v168
	v_mul_f32_e32 v169, v224, v169
	v_mul_f32_e32 v170, v224, v170
	v_mul_f32_e32 v171, v224, v171
	ds_write_b128 v209, v[168:171] offset:6144
	v_mul_f32_e32 v172, v225, v172
	v_mul_f32_e32 v173, v225, v173
	v_mul_f32_e32 v174, v225, v174
	v_mul_f32_e32 v175, v225, v175
	ds_write_b128 v209, v[172:175] offset:7168
	s_waitcnt lgkmcnt(0)
	s_barrier
; #define GAS __attribute__((address_space(1)))
; #define LAS __attribute__((address_space(3)))
; #define LDS_WAIT() asm volatile("s_waitcnt lgkmcnt(0)" ::: "memory")
; __device__ __forceinline__ int src_col_in(int c) {
;     if (c < 5120) { const int blk = c >> 7, p = c & 127; const bool rope = blk < 16 || ((((blk - 16) >> 2) & 1) == 0); const int d = rope ? (p >> 1) + 64 * (p & 1) : p; return blk * 128 + d; }
;     if (c < OFF_Z) return c + 2096;
;     if (c < OFF_G) return c - 4048;
;     if (c < OFF_DT) return 5120 + (c - OFF_G);
;     if (c < NSRC) return c;
;     return -1;
; }
;     const int pr = item >> 1, kb = 2 * (pr / nblk) + (item & 1), nb = pr % nblk, k0 = 64 * kb, n0 = 32 * nb;
;     const int nr = n0 + (lane & 31); const int sc = MAP == 1 ? src_col_in(nr) : nr;
;     float v[32];
; #pragma unroll
;     for (int i = 0; i < 32; ++i) v[i] = sc >= 0 ? W[(size_t)(k0 + 2 * i + (lane >> 5)) * Nsrc + sc] : 0.f;
; #pragma unroll
;     for (int i = 0; i < 32; ++i) { const int k = k0 + 2 * i + (lane >> 5); float x = v[i] * wscale; if (KS) x *= (k < ksplit ? ksA[k] : ksB[k - ksplit]); scr[(2 * i + (lane >> 5)) * 33 + (lane & 31)] = x; }
;     LDS_WAIT(); asm volatile("" ::: "memory");
;     const int c = lane & 7;
; #pragma unroll
;     for (int j = 0; j < 4; ++j) { const int n = (lane >> 3) + 8 * j; const LAS float* s = scr + (8 * c) * 33 + n;
;         const unsigned long long o = (unsigned long long)pg8::pk4_fp8(s[0 * 33], s[1 * 33], s[2 * 33], s[3 * 33]) | ((unsigned long long)pg8::pk4_fp8(s[4 * 33], s[5 * 33], s[6 * 33], s[7 * 33]) << 32);
;         *(GAS unsigned long long*)(WT + (size_t)(n0 + n) * K + k0 + 8 * c) = o; }
;     LDS_WAIT(); asm volatile("" ::: "memory");
; }
	s_lshl_b32 s20, s27, 7
	s_cmp_lt_u32 s27, 40
	s_cselect_b32 s21, 0, 0x830
	s_cmp_lt_u32 s27, 72
	s_cselect_b32 s21, s21, 0xfffff030
	s_add_i32 s20, s20, s21
	s_lshl_b32 s20, s20, 2
	s_add_u32 s8, s16, s20
	s_addc_u32 s9, s17, 0
	global_load_dwordx4 v[144:147], v208, s[8:9]
	s_add_u32 s8, s8, 0x16280
	s_addc_u32 s9, s9, 0
	global_load_dwordx4 v[148:151], v208, s[8:9]
	s_add_u32 s8, s8, 0x16280
	s_addc_u32 s9, s9, 0
	global_load_dwordx4 v[152:155], v208, s[8:9]
	s_add_u32 s8, s8, 0x16280
	s_addc_u32 s9, s9, 0
	global_load_dwordx4 v[156:159], v208, s[8:9]
	s_add_u32 s8, s8, 0x16280
	s_addc_u32 s9, s9, 0
	global_load_dwordx4 v[160:163], v208, s[8:9]
	s_add_u32 s8, s8, 0x16280
	s_addc_u32 s9, s9, 0
	global_load_dwordx4 v[164:167], v208, s[8:9]
	s_add_u32 s8, s8, 0x16280
	s_addc_u32 s9, s9, 0
	global_load_dwordx4 v[168:171], v208, s[8:9]
	s_add_u32 s8, s8, 0x16280
	s_addc_u32 s9, s9, 0
	global_load_dwordx4 v[172:175], v208, s[8:9]
	s_mul_i32 s20, s26, 0x80000
	s_add_u32 s6, s18, s20
	s_addc_u32 s7, s19, 0
	s_cmp_lt_u32 s26, 16
	s_cselect_b32 s20, 1, 0
	s_sub_i32 s21, s26, 16
	s_bitcmp0_b32 s21, 2
	s_cselect_b32 s21, 1, 0
	s_cmp_lt_u32 s26, 40
	s_cselect_b32 s21, s21, 0
	s_or_b32 s20, s20, s21
	s_cmp_lg_u32 s20, 0
	s_cselect_b64 s[20:21], -1, 0
	v_cndmask_b32_e64 v108, v100, v104, s[20:21]
	v_cndmask_b32_e64 v109, v101, v105, s[20:21]
	ds_read_b32 v226, v211
	ds_read_b32 v227, v211 offset:512
	ds_read_b32 v228, v211 offset:1024
	ds_read_b32 v229, v211 offset:1536
	ds_read_b32 v230, v211 offset:2048
	ds_read_b32 v231, v211 offset:2560
	ds_read_b32 v232, v211 offset:3072
	ds_read_b32 v233, v211 offset:3584
	ds_read_b32 v234, v211 offset:4096
	ds_read_b32 v235, v211 offset:4608
	ds_read_b32 v236, v211 offset:5120
	ds_read_b32 v237, v211 offset:5632
	ds_read_b32 v238, v211 offset:6144
	ds_read_b32 v239, v211 offset:6656
	ds_read_b32 v240, v211 offset:7168
	ds_read_b32 v241, v211 offset:7680
	s_waitcnt lgkmcnt(0)
	v_max_f32_e32 v226, v226, v226
	v_max_f32_e32 v227, v227, v227
	v_max_f32_e32 v228, v228, v228
	v_max_f32_e32 v229, v229, v229
	v_max_f32_e32 v230, v230, v230
	v_max_f32_e32 v231, v231, v231
	v_max_f32_e32 v232, v232, v232
	v_max_f32_e32 v233, v233, v233
	v_max_f32_e32 v234, v234, v234
	v_max_f32_e32 v235, v235, v235
	v_max_f32_e32 v236, v236, v236
	v_max_f32_e32 v237, v237, v237
	v_max_f32_e32 v238, v238, v238
	v_max_f32_e32 v239, v239, v239
	v_max_f32_e32 v240, v240, v240
	v_max_f32_e32 v241, v241, v241
	v_med3_f32 v226, v226, s44, v246
	v_med3_f32 v227, v227, s44, v246
	v_med3_f32 v228, v228, s44, v246
	v_med3_f32 v229, v229, s44, v246
	v_med3_f32 v230, v230, s44, v246
	v_med3_f32 v231, v231, s44, v246
	v_med3_f32 v232, v232, s44, v246
	v_med3_f32 v233, v233, s44, v246
	v_med3_f32 v234, v234, s44, v246
	v_med3_f32 v235, v235, s44, v246
	v_med3_f32 v236, v236, s44, v246
	v_med3_f32 v237, v237, s44, v246
	v_med3_f32 v238, v238, s44, v246
	v_med3_f32 v239, v239, s44, v246
	v_med3_f32 v240, v240, s44, v246
	v_med3_f32 v241, v241, s44, v246
	v_mov_b32_e32 v242, 0
	v_mov_b32_e32 v243, 0
	v_mov_b32_e32 v244, 0
	v_mov_b32_e32 v245, 0
	v_cvt_pk_fp8_f32 v242, v226, v227
	v_cvt_pk_fp8_f32 v243, v230, v231
	v_cvt_pk_fp8_f32 v244, v234, v235
	v_cvt_pk_fp8_f32 v245, v238, v239
	v_cvt_pk_fp8_f32 v242, v228, v229 op_sel:[0,0,1]
	v_cvt_pk_fp8_f32 v243, v232, v233 op_sel:[0,0,1]
	v_cvt_pk_fp8_f32 v244, v236, v237 op_sel:[0,0,1]
	v_cvt_pk_fp8_f32 v245, v240, v241 op_sel:[0,0,1]
	s_nop 0
	global_store_dwordx4 v108, v[242:245], s[6:7]
	ds_read_b32 v226, v213
	ds_read_b32 v227, v213 offset:512
	ds_read_b32 v228, v213 offset:1024
	ds_read_b32 v229, v213 offset:1536
	ds_read_b32 v230, v213 offset:2048
	ds_read_b32 v231, v213 offset:2560
	ds_read_b32 v232, v213 offset:3072
	ds_read_b32 v233, v213 offset:3584
	ds_read_b32 v234, v213 offset:4096
	ds_read_b32 v235, v213 offset:4608
	ds_read_b32 v236, v213 offset:5120
	ds_read_b32 v237, v213 offset:5632
	ds_read_b32 v238, v213 offset:6144
	ds_read_b32 v239, v213 offset:6656
	ds_read_b32 v240, v213 offset:7168
	ds_read_b32 v241, v213 offset:7680
	s_waitcnt lgkmcnt(0)
	v_max_f32_e32 v226, v226, v226
	v_max_f32_e32 v227, v227, v227
	v_max_f32_e32 v228, v228, v228
	v_max_f32_e32 v229, v229, v229
	v_max_f32_e32 v230, v230, v230
	v_max_f32_e32 v231, v231, v231
	v_max_f32_e32 v232, v232, v232
	v_max_f32_e32 v233, v233, v233
	v_max_f32_e32 v234, v234, v234
	v_max_f32_e32 v235, v235, v235
	v_max_f32_e32 v236, v236, v236
	v_max_f32_e32 v237, v237, v237
	v_max_f32_e32 v238, v238, v238
	v_max_f32_e32 v239, v239, v239
	v_max_f32_e32 v240, v240, v240
	v_max_f32_e32 v241, v241, v241
	v_med3_f32 v226, v226, s44, v246
	v_med3_f32 v227, v227, s44, v246
	v_med3_f32 v228, v228, s44, v246
	v_med3_f32 v229, v229, s44, v246
	v_med3_f32 v230, v230, s44, v246
	v_med3_f32 v231, v231, s44, v246
	v_med3_f32 v232, v232, s44, v246
	v_med3_f32 v233, v233, s44, v246
	v_med3_f32 v234, v234, s44, v246
	v_med3_f32 v235, v235, s44, v246
	v_med3_f32 v236, v236, s44, v246
	v_med3_f32 v237, v237, s44, v246
	v_med3_f32 v238, v238, s44, v246
	v_med3_f32 v239, v239, s44, v246
	v_med3_f32 v240, v240, s44, v246
	v_med3_f32 v241, v241, s44, v246
	v_mov_b32_e32 v242, 0
	v_mov_b32_e32 v243, 0
	v_mov_b32_e32 v244, 0
	v_mov_b32_e32 v245, 0
	v_cvt_pk_fp8_f32 v242, v226, v227
	v_cvt_pk_fp8_f32 v243, v230, v231
	v_cvt_pk_fp8_f32 v244, v234, v235
	v_cvt_pk_fp8_f32 v245, v238, v239
	v_cvt_pk_fp8_f32 v242, v228, v229 op_sel:[0,0,1]
	v_cvt_pk_fp8_f32 v243, v232, v233 op_sel:[0,0,1]
	v_cvt_pk_fp8_f32 v244, v236, v237 op_sel:[0,0,1]
	v_cvt_pk_fp8_f32 v245, v240, v241 op_sel:[0,0,1]
	s_nop 0
	global_store_dwordx4 v109, v[242:245], s[6:7]
	s_add_i32 s26, s23, 56
	s_add_i32 s27, s23, 72
	s_waitcnt vmcnt(12)
; #define GAS __attribute__((address_space(1)))
; #define LAS __attribute__((address_space(3)))
; #define LDS_WAIT() asm volatile("s_waitcnt lgkmcnt(0)" ::: "memory")
; __device__ __forceinline__ int src_col_in(int c) {
;     if (c < 5120) { const int blk = c >> 7, p = c & 127; const bool rope = blk < 16 || ((((blk - 16) >> 2) & 1) == 0); const int d = rope ? (p >> 1) + 64 * (p & 1) : p; return blk * 128 + d; }
;     if (c < OFF_Z) return c + 2096;
;     if (c < OFF_G) return c - 4048;
;     if (c < OFF_DT) return 5120 + (c - OFF_G);
;     if (c < NSRC) return c;
;     return -1;
; }
;     const int pr = item >> 1, kb = 2 * (pr / nblk) + (item & 1), nb = pr % nblk, k0 = 64 * kb, n0 = 32 * nb;
;     const int nr = n0 + (lane & 31); const int sc = MAP == 1 ? src_col_in(nr) : nr;
;     float v[32];
; #pragma unroll
;     for (int i = 0; i < 32; ++i) v[i] = sc >= 0 ? W[(size_t)(k0 + 2 * i + (lane >> 5)) * Nsrc + sc] : 0.f;
; #pragma unroll
;     for (int i = 0; i < 32; ++i) { const int k = k0 + 2 * i + (lane >> 5); float x = v[i] * wscale; if (KS) x *= (k < ksplit ? ksA[k] : ksB[k - ksplit]); scr[(2 * i + (lane >> 5)) * 33 + (lane & 31)] = x; }
;     LDS_WAIT(); asm volatile("" ::: "memory");
;     const int c = lane & 7;
; #pragma unroll
;     for (int j = 0; j < 4; ++j) { const int n = (lane >> 3) + 8 * j; const LAS float* s = scr + (8 * c) * 33 + n;
;         const unsigned long long o = (unsigned long long)pg8::pk4_fp8(s[0 * 33], s[1 * 33], s[2 * 33], s[3 * 33]) | ((unsigned long long)pg8::pk4_fp8(s[4 * 33], s[5 * 33], s[6 * 33], s[7 * 33]) << 32);
;         *(GAS unsigned long long*)(WT + (size_t)(n0 + n) * K + k0 + 8 * c) = o; }
;     LDS_WAIT(); asm volatile("" ::: "memory");
; }
	v_mul_f32_e32 v176, v218, v176
	v_mul_f32_e32 v177, v218, v177
	v_mul_f32_e32 v178, v218, v178
	v_mul_f32_e32 v179, v218, v179
	ds_write_b128 v210, v[176:179]
	v_mul_f32_e32 v180, v219, v180
	v_mul_f32_e32 v181, v219, v181
	v_mul_f32_e32 v182, v219, v182
	v_mul_f32_e32 v183, v219, v183
	ds_write_b128 v210, v[180:183] offset:1024
	v_mul_f32_e32 v184, v220, v184
	v_mul_f32_e32 v185, v220, v185
	v_mul_f32_e32 v186, v220, v186
	v_mul_f32_e32 v187, v220, v187
	ds_write_b128 v210, v[184:187] offset:2048
	v_mul_f32_e32 v188, v221, v188
	v_mul_f32_e32 v189, v221, v189
	v_mul_f32_e32 v190, v221, v190
	v_mul_f32_e32 v191, v221, v191
	ds_write_b128 v210, v[188:191] offset:3072
	v_mul_f32_e32 v192, v222, v192
	v_mul_f32_e32 v193, v222, v193
	v_mul_f32_e32 v194, v222, v194
	v_mul_f32_e32 v195, v222, v195
	ds_write_b128 v210, v[192:195] offset:4096
	v_mul_f32_e32 v196, v223, v196
	v_mul_f32_e32 v197, v223, v197
	v_mul_f32_e32 v198, v223, v198
	v_mul_f32_e32 v199, v223, v199
	ds_write_b128 v210, v[196:199] offset:5120
	v_mul_f32_e32 v200, v224, v200
	v_mul_f32_e32 v201, v224, v201
	v_mul_f32_e32 v202, v224, v202
	v_mul_f32_e32 v203, v224, v203
	ds_write_b128 v210, v[200:203] offset:6144
	v_mul_f32_e32 v204, v225, v204
	v_mul_f32_e32 v205, v225, v205
	v_mul_f32_e32 v206, v225, v206
	v_mul_f32_e32 v207, v225, v207
	ds_write_b128 v210, v[204:207] offset:7168
	s_waitcnt lgkmcnt(0)
	s_barrier
	s_lshl_b32 s20, s27, 7
	s_cmp_lt_u32 s27, 40
	s_cselect_b32 s21, 0, 0x830
	s_cmp_lt_u32 s27, 72
	s_cselect_b32 s21, s21, 0xfffff030
	s_add_i32 s20, s20, s21
	s_lshl_b32 s20, s20, 2
	s_add_u32 s8, s16, s20
	s_addc_u32 s9, s17, 0
	global_load_dwordx4 v[176:179], v208, s[8:9]
	s_add_u32 s8, s8, 0x16280
	s_addc_u32 s9, s9, 0
	global_load_dwordx4 v[180:183], v208, s[8:9]
	s_add_u32 s8, s8, 0x16280
	s_addc_u32 s9, s9, 0
	global_load_dwordx4 v[184:187], v208, s[8:9]
	s_add_u32 s8, s8, 0x16280
	s_addc_u32 s9, s9, 0
	global_load_dwordx4 v[188:191], v208, s[8:9]
	s_add_u32 s8, s8, 0x16280
	s_addc_u32 s9, s9, 0
	global_load_dwordx4 v[192:195], v208, s[8:9]
	s_add_u32 s8, s8, 0x16280
	s_addc_u32 s9, s9, 0
	global_load_dwordx4 v[196:199], v208, s[8:9]
	s_add_u32 s8, s8, 0x16280
	s_addc_u32 s9, s9, 0
	global_load_dwordx4 v[200:203], v208, s[8:9]
	s_add_u32 s8, s8, 0x16280
	s_addc_u32 s9, s9, 0
	global_load_dwordx4 v[204:207], v208, s[8:9]
	s_mul_i32 s20, s26, 0x80000
	s_add_u32 s6, s18, s20
	s_addc_u32 s7, s19, 0
	s_cmp_lt_u32 s26, 16
	s_cselect_b32 s20, 1, 0
	s_sub_i32 s21, s26, 16
	s_bitcmp0_b32 s21, 2
	s_cselect_b32 s21, 1, 0
	s_cmp_lt_u32 s26, 40
	s_cselect_b32 s21, s21, 0
	s_or_b32 s20, s20, s21
	s_cmp_lg_u32 s20, 0
	s_cselect_b64 s[20:21], -1, 0
	v_cndmask_b32_e64 v108, v100, v104, s[20:21]
	v_cndmask_b32_e64 v109, v101, v105, s[20:21]
	ds_read_b32 v226, v212
	ds_read_b32 v227, v212 offset:512
	ds_read_b32 v228, v212 offset:1024
	ds_read_b32 v229, v212 offset:1536
	ds_read_b32 v230, v212 offset:2048
	ds_read_b32 v231, v212 offset:2560
	ds_read_b32 v232, v212 offset:3072
	ds_read_b32 v233, v212 offset:3584
	ds_read_b32 v234, v212 offset:4096
	ds_read_b32 v235, v212 offset:4608
	ds_read_b32 v236, v212 offset:5120
	ds_read_b32 v237, v212 offset:5632
	ds_read_b32 v238, v212 offset:6144
	ds_read_b32 v239, v212 offset:6656
	ds_read_b32 v240, v212 offset:7168
	ds_read_b32 v241, v212 offset:7680
	s_waitcnt lgkmcnt(0)
	v_max_f32_e32 v226, v226, v226
	v_max_f32_e32 v227, v227, v227
	v_max_f32_e32 v228, v228, v228
	v_max_f32_e32 v229, v229, v229
	v_max_f32_e32 v230, v230, v230
	v_max_f32_e32 v231, v231, v231
	v_max_f32_e32 v232, v232, v232
	v_max_f32_e32 v233, v233, v233
	v_max_f32_e32 v234, v234, v234
	v_max_f32_e32 v235, v235, v235
	v_max_f32_e32 v236, v236, v236
	v_max_f32_e32 v237, v237, v237
	v_max_f32_e32 v238, v238, v238
	v_max_f32_e32 v239, v239, v239
	v_max_f32_e32 v240, v240, v240
	v_max_f32_e32 v241, v241, v241
	v_med3_f32 v226, v226, s44, v246
	v_med3_f32 v227, v227, s44, v246
	v_med3_f32 v228, v228, s44, v246
	v_med3_f32 v229, v229, s44, v246
	v_med3_f32 v230, v230, s44, v246
	v_med3_f32 v231, v231, s44, v246
	v_med3_f32 v232, v232, s44, v246
	v_med3_f32 v233, v233, s44, v246
	v_med3_f32 v234, v234, s44, v246
	v_med3_f32 v235, v235, s44, v246
	v_med3_f32 v236, v236, s44, v246
	v_med3_f32 v237, v237, s44, v246
	v_med3_f32 v238, v238, s44, v246
	v_med3_f32 v239, v239, s44, v246
	v_med3_f32 v240, v240, s44, v246
	v_med3_f32 v241, v241, s44, v246
	v_mov_b32_e32 v242, 0
	v_mov_b32_e32 v243, 0
	v_mov_b32_e32 v244, 0
	v_mov_b32_e32 v245, 0
	v_cvt_pk_fp8_f32 v242, v226, v227
	v_cvt_pk_fp8_f32 v243, v230, v231
	v_cvt_pk_fp8_f32 v244, v234, v235
	v_cvt_pk_fp8_f32 v245, v238, v239
	v_cvt_pk_fp8_f32 v242, v228, v229 op_sel:[0,0,1]
	v_cvt_pk_fp8_f32 v243, v232, v233 op_sel:[0,0,1]
	v_cvt_pk_fp8_f32 v244, v236, v237 op_sel:[0,0,1]
	v_cvt_pk_fp8_f32 v245, v240, v241 op_sel:[0,0,1]
	s_nop 0
	global_store_dwordx4 v108, v[242:245], s[6:7]
	ds_read_b32 v226, v214
	ds_read_b32 v227, v214 offset:512
	ds_read_b32 v228, v214 offset:1024
	ds_read_b32 v229, v214 offset:1536
	ds_read_b32 v230, v214 offset:2048
	ds_read_b32 v231, v214 offset:2560
	ds_read_b32 v232, v214 offset:3072
	ds_read_b32 v233, v214 offset:3584
	ds_read_b32 v234, v214 offset:4096
	ds_read_b32 v235, v214 offset:4608
	ds_read_b32 v236, v214 offset:5120
	ds_read_b32 v237, v214 offset:5632
	ds_read_b32 v238, v214 offset:6144
	ds_read_b32 v239, v214 offset:6656
	ds_read_b32 v240, v214 offset:7168
	ds_read_b32 v241, v214 offset:7680
	s_waitcnt lgkmcnt(0)
; #define GAS __attribute__((address_space(1)))
; #define LAS __attribute__((address_space(3)))
; #define LDS_WAIT() asm volatile("s_waitcnt lgkmcnt(0)" ::: "memory")
; __device__ __forceinline__ unsigned pk4_fp8(float a, float b, float c, float d) {
;     a = fminf(fmaxf(a, -448.f), 448.f); b = fminf(fmaxf(b, -448.f), 448.f); c = fminf(fmaxf(c, -448.f), 448.f); d = fminf(fmaxf(d, -448.f), 448.f);
;     int w = __builtin_amdgcn_cvt_pk_fp8_f32(a, b, 0, false); w = __builtin_amdgcn_cvt_pk_fp8_f32(c, d, w, true); return (unsigned)w; }
;     const int pr = item >> 1, kb = 2 * (pr / nblk) + (item & 1), nb = pr % nblk, k0 = 64 * kb, n0 = 32 * nb;
;     const int nr = n0 + (lane & 31); const int sc = MAP == 1 ? src_col_in(nr) : nr;
;     float v[32];
; #pragma unroll
;     for (int i = 0; i < 32; ++i) v[i] = sc >= 0 ? W[(size_t)(k0 + 2 * i + (lane >> 5)) * Nsrc + sc] : 0.f;
; #pragma unroll
;     for (int i = 0; i < 32; ++i) { const int k = k0 + 2 * i + (lane >> 5); float x = v[i] * wscale; if (KS) x *= (k < ksplit ? ksA[k] : ksB[k - ksplit]); scr[(2 * i + (lane >> 5)) * 33 + (lane & 31)] = x; }
;     LDS_WAIT(); asm volatile("" ::: "memory");
;     const int c = lane & 7;
; #pragma unroll
;     for (int j = 0; j < 4; ++j) { const int n = (lane >> 3) + 8 * j; const LAS float* s = scr + (8 * c) * 33 + n;
;         const unsigned long long o = (unsigned long long)pg8::pk4_fp8(s[0 * 33], s[1 * 33], s[2 * 33], s[3 * 33]) | ((unsigned long long)pg8::pk4_fp8(s[4 * 33], s[5 * 33], s[6 * 33], s[7 * 33]) << 32);
;         *(GAS unsigned long long*)(WT + (size_t)(n0 + n) * K + k0 + 8 * c) = o; }
;     LDS_WAIT(); asm volatile("" ::: "memory");
; }
	v_max_f32_e32 v226, v226, v226
	v_max_f32_e32 v227, v227, v227
	v_max_f32_e32 v228, v228, v228
	v_max_f32_e32 v229, v229, v229
	v_max_f32_e32 v230, v230, v230
	v_max_f32_e32 v231, v231, v231
	v_max_f32_e32 v232, v232, v232
	v_max_f32_e32 v233, v233, v233
	v_max_f32_e32 v234, v234, v234
	v_max_f32_e32 v235, v235, v235
	v_max_f32_e32 v236, v236, v236
	v_max_f32_e32 v237, v237, v237
	v_max_f32_e32 v238, v238, v238
	v_max_f32_e32 v239, v239, v239
	v_max_f32_e32 v240, v240, v240
	v_max_f32_e32 v241, v241, v241
	v_med3_f32 v226, v226, s44, v246
	v_med3_f32 v227, v227, s44, v246
	v_med3_f32 v228, v228, s44, v246
	v_med3_f32 v229, v229, s44, v246
	v_med3_f32 v230, v230, s44, v246
	v_med3_f32 v231, v231, s44, v246
	v_med3_f32 v232, v232, s44, v246
	v_med3_f32 v233, v233, s44, v246
	v_med3_f32 v234, v234, s44, v246
	v_med3_f32 v235, v235, s44, v246
	v_med3_f32 v236, v236, s44, v246
	v_med3_f32 v237, v237, s44, v246
	v_med3_f32 v238, v238, s44, v246
	v_med3_f32 v239, v239, s44, v246
	v_med3_f32 v240, v240, s44, v246
	v_med3_f32 v241, v241, s44, v246
	v_mov_b32_e32 v242, 0
	v_mov_b32_e32 v243, 0
	v_mov_b32_e32 v244, 0
	v_mov_b32_e32 v245, 0
	v_cvt_pk_fp8_f32 v242, v226, v227
	v_cvt_pk_fp8_f32 v243, v230, v231
	v_cvt_pk_fp8_f32 v244, v234, v235
	v_cvt_pk_fp8_f32 v245, v238, v239
	v_cvt_pk_fp8_f32 v242, v228, v229 op_sel:[0,0,1]
	v_cvt_pk_fp8_f32 v243, v232, v233 op_sel:[0,0,1]
	v_cvt_pk_fp8_f32 v244, v236, v237 op_sel:[0,0,1]
	v_cvt_pk_fp8_f32 v245, v240, v241 op_sel:[0,0,1]
	s_nop 0
	global_store_dwordx4 v109, v[242:245], s[6:7]
	s_add_i32 s26, s23, 64
	s_add_i32 s27, s23, 80
	s_waitcnt vmcnt(12)
	v_mul_f32_e32 v144, v218, v144
	v_mul_f32_e32 v145, v218, v145
	v_mul_f32_e32 v146, v218, v146
	v_mul_f32_e32 v147, v218, v147
	ds_write_b128 v209, v[144:147]
	v_mul_f32_e32 v148, v219, v148
	v_mul_f32_e32 v149, v219, v149
	v_mul_f32_e32 v150, v219, v150
	v_mul_f32_e32 v151, v219, v151
	ds_write_b128 v209, v[148:151] offset:1024
	v_mul_f32_e32 v152, v220, v152
	v_mul_f32_e32 v153, v220, v153
	v_mul_f32_e32 v154, v220, v154
	v_mul_f32_e32 v155, v220, v155
	ds_write_b128 v209, v[152:155] offset:2048
	v_mul_f32_e32 v156, v221, v156
	v_mul_f32_e32 v157, v221, v157
	v_mul_f32_e32 v158, v221, v158
	v_mul_f32_e32 v159, v221, v159
	ds_write_b128 v209, v[156:159] offset:3072
	v_mul_f32_e32 v160, v222, v160
	v_mul_f32_e32 v161, v222, v161
	v_mul_f32_e32 v162, v222, v162
	v_mul_f32_e32 v163, v222, v163
	ds_write_b128 v209, v[160:163] offset:4096
	v_mul_f32_e32 v164, v223, v164
	v_mul_f32_e32 v165, v223, v165
	v_mul_f32_e32 v166, v223, v166
	v_mul_f32_e32 v167, v223, v167
	ds_write_b128 v209, v[164:167] offset:5120
	v_mul_f32_e32 v168, v224, v168
	v_mul_f32_e32 v169, v224, v169
	v_mul_f32_e32 v170, v224, v170
	v_mul_f32_e32 v171, v224, v171
	ds_write_b128 v209, v[168:171] offset:6144
	v_mul_f32_e32 v172, v225, v172
	v_mul_f32_e32 v173, v225, v173
	v_mul_f32_e32 v174, v225, v174
	v_mul_f32_e32 v175, v225, v175
	ds_write_b128 v209, v[172:175] offset:7168
	s_waitcnt lgkmcnt(0)
	s_barrier
	s_lshl_b32 s20, s27, 7
	s_cmp_lt_u32 s27, 40
	s_cselect_b32 s21, 0, 0x830
	s_cmp_lt_u32 s27, 72
	s_cselect_b32 s21, s21, 0xfffff030
	s_add_i32 s20, s20, s21
	s_lshl_b32 s20, s20, 2
	s_add_u32 s8, s16, s20
	s_addc_u32 s9, s17, 0
	global_load_dwordx4 v[144:147], v208, s[8:9]
	s_add_u32 s8, s8, 0x16280
	s_addc_u32 s9, s9, 0
	global_load_dwordx4 v[148:151], v208, s[8:9]
	s_add_u32 s8, s8, 0x16280
	s_addc_u32 s9, s9, 0
	global_load_dwordx4 v[152:155], v208, s[8:9]
	s_add_u32 s8, s8, 0x16280
	s_addc_u32 s9, s9, 0
	global_load_dwordx4 v[156:159], v208, s[8:9]
	s_add_u32 s8, s8, 0x16280
	s_addc_u32 s9, s9, 0
	global_load_dwordx4 v[160:163], v208, s[8:9]
	s_add_u32 s8, s8, 0x16280
	s_addc_u32 s9, s9, 0
	global_load_dwordx4 v[164:167], v208, s[8:9]
	s_add_u32 s8, s8, 0x16280
	s_addc_u32 s9, s9, 0
	global_load_dwordx4 v[168:171], v208, s[8:9]
	s_add_u32 s8, s8, 0x16280
	s_addc_u32 s9, s9, 0
	global_load_dwordx4 v[172:175], v208, s[8:9]
	s_mul_i32 s20, s26, 0x80000
	s_add_u32 s6, s18, s20
	s_addc_u32 s7, s19, 0
	s_cmp_lt_u32 s26, 16
	s_cselect_b32 s20, 1, 0
	s_sub_i32 s21, s26, 16
	s_bitcmp0_b32 s21, 2
	s_cselect_b32 s21, 1, 0
	s_cmp_lt_u32 s26, 40
	s_cselect_b32 s21, s21, 0
	s_or_b32 s20, s20, s21
	s_cmp_lg_u32 s20, 0
	s_cselect_b64 s[20:21], -1, 0
	v_cndmask_b32_e64 v108, v100, v104, s[20:21]
	v_cndmask_b32_e64 v109, v101, v105, s[20:21]
	ds_read_b32 v226, v211
	ds_read_b32 v227, v211 offset:512
	ds_read_b32 v228, v211 offset:1024
	ds_read_b32 v229, v211 offset:1536
	ds_read_b32 v230, v211 offset:2048
	ds_read_b32 v231, v211 offset:2560
	ds_read_b32 v232, v211 offset:3072
	ds_read_b32 v233, v211 offset:3584
	ds_read_b32 v234, v211 offset:4096
	ds_read_b32 v235, v211 offset:4608
	ds_read_b32 v236, v211 offset:5120
	ds_read_b32 v237, v211 offset:5632
	ds_read_b32 v238, v211 offset:6144
	ds_read_b32 v239, v211 offset:6656
	ds_read_b32 v240, v211 offset:7168
	ds_read_b32 v241, v211 offset:7680
	s_waitcnt lgkmcnt(0)
; #define GAS __attribute__((address_space(1)))
; #define LAS __attribute__((address_space(3)))
; #define LDS_WAIT() asm volatile("s_waitcnt lgkmcnt(0)" ::: "memory")
; __device__ __forceinline__ unsigned pk4_fp8(float a, float b, float c, float d) {
;     a = fminf(fmaxf(a, -448.f), 448.f); b = fminf(fmaxf(b, -448.f), 448.f); c = fminf(fmaxf(c, -448.f), 448.f); d = fminf(fmaxf(d, -448.f), 448.f);
;     int w = __builtin_amdgcn_cvt_pk_fp8_f32(a, b, 0, false); w = __builtin_amdgcn_cvt_pk_fp8_f32(c, d, w, true); return (unsigned)w; }
;     const int pr = item >> 1, kb = 2 * (pr / nblk) + (item & 1), nb = pr % nblk, k0 = 64 * kb, n0 = 32 * nb;
;     const int nr = n0 + (lane & 31); const int sc = MAP == 1 ? src_col_in(nr) : nr;
;     float v[32];
; #pragma unroll
;     for (int i = 0; i < 32; ++i) v[i] = sc >= 0 ? W[(size_t)(k0 + 2 * i + (lane >> 5)) * Nsrc + sc] : 0.f;
; #pragma unroll
;     for (int i = 0; i < 32; ++i) { const int k = k0 + 2 * i + (lane >> 5); float x = v[i] * wscale; if (KS) x *= (k < ksplit ? ksA[k] : ksB[k - ksplit]); scr[(2 * i + (lane >> 5)) * 33 + (lane & 31)] = x; }
;     LDS_WAIT(); asm volatile("" ::: "memory");
;     const int c = lane & 7;
; #pragma unroll
;     for (int j = 0; j < 4; ++j) { const int n = (lane >> 3) + 8 * j; const LAS float* s = scr + (8 * c) * 33 + n;
;         const unsigned long long o = (unsigned long long)pg8::pk4_fp8(s[0 * 33], s[1 * 33], s[2 * 33], s[3 * 33]) | ((unsigned long long)pg8::pk4_fp8(s[4 * 33], s[5 * 33], s[6 * 33], s[7 * 33]) << 32);
;         *(GAS unsigned long long*)(WT + (size_t)(n0 + n) * K + k0 + 8 * c) = o; }
;     LDS_WAIT(); asm volatile("" ::: "memory");
; }
	v_max_f32_e32 v226, v226, v226
	v_max_f32_e32 v227, v227, v227
	v_max_f32_e32 v228, v228, v228
	v_max_f32_e32 v229, v229, v229
	v_max_f32_e32 v230, v230, v230
	v_max_f32_e32 v231, v231, v231
	v_max_f32_e32 v232, v232, v232
	v_max_f32_e32 v233, v233, v233
	v_max_f32_e32 v234, v234, v234
	v_max_f32_e32 v235, v235, v235
	v_max_f32_e32 v236, v236, v236
	v_max_f32_e32 v237, v237, v237
	v_max_f32_e32 v238, v238, v238
	v_max_f32_e32 v239, v239, v239
	v_max_f32_e32 v240, v240, v240
	v_max_f32_e32 v241, v241, v241
	v_med3_f32 v226, v226, s44, v246
	v_med3_f32 v227, v227, s44, v246
	v_med3_f32 v228, v228, s44, v246
	v_med3_f32 v229, v229, s44, v246
	v_med3_f32 v230, v230, s44, v246
	v_med3_f32 v231, v231, s44, v246
	v_med3_f32 v232, v232, s44, v246
	v_med3_f32 v233, v233, s44, v246
	v_med3_f32 v234, v234, s44, v246
	v_med3_f32 v235, v235, s44, v246
	v_med3_f32 v236, v236, s44, v246
	v_med3_f32 v237, v237, s44, v246
	v_med3_f32 v238, v238, s44, v246
	v_med3_f32 v239, v239, s44, v246
	v_med3_f32 v240, v240, s44, v246
	v_med3_f32 v241, v241, s44, v246
	v_mov_b32_e32 v242, 0
	v_mov_b32_e32 v243, 0
	v_mov_b32_e32 v244, 0
	v_mov_b32_e32 v245, 0
	v_cvt_pk_fp8_f32 v242, v226, v227
	v_cvt_pk_fp8_f32 v243, v230, v231
	v_cvt_pk_fp8_f32 v244, v234, v235
	v_cvt_pk_fp8_f32 v245, v238, v239
	v_cvt_pk_fp8_f32 v242, v228, v229 op_sel:[0,0,1]
	v_cvt_pk_fp8_f32 v243, v232, v233 op_sel:[0,0,1]
	v_cvt_pk_fp8_f32 v244, v236, v237 op_sel:[0,0,1]
	v_cvt_pk_fp8_f32 v245, v240, v241 op_sel:[0,0,1]
	s_nop 0
	global_store_dwordx4 v108, v[242:245], s[6:7]
	ds_read_b32 v226, v213
	ds_read_b32 v227, v213 offset:512
	ds_read_b32 v228, v213 offset:1024
	ds_read_b32 v229, v213 offset:1536
	ds_read_b32 v230, v213 offset:2048
	ds_read_b32 v231, v213 offset:2560
	ds_read_b32 v232, v213 offset:3072
	ds_read_b32 v233, v213 offset:3584
	ds_read_b32 v234, v213 offset:4096
	ds_read_b32 v235, v213 offset:4608
	ds_read_b32 v236, v213 offset:5120
	ds_read_b32 v237, v213 offset:5632
	ds_read_b32 v238, v213 offset:6144
	ds_read_b32 v239, v213 offset:6656
	ds_read_b32 v240, v213 offset:7168
	ds_read_b32 v241, v213 offset:7680
	s_waitcnt lgkmcnt(0)
	v_max_f32_e32 v226, v226, v226
	v_max_f32_e32 v227, v227, v227
	v_max_f32_e32 v228, v228, v228
	v_max_f32_e32 v229, v229, v229
	v_max_f32_e32 v230, v230, v230
	v_max_f32_e32 v231, v231, v231
	v_max_f32_e32 v232, v232, v232
	v_max_f32_e32 v233, v233, v233
	v_max_f32_e32 v234, v234, v234
	v_max_f32_e32 v235, v235, v235
	v_max_f32_e32 v236, v236, v236
	v_max_f32_e32 v237, v237, v237
	v_max_f32_e32 v238, v238, v238
	v_max_f32_e32 v239, v239, v239
	v_max_f32_e32 v240, v240, v240
	v_max_f32_e32 v241, v241, v241
	v_med3_f32 v226, v226, s44, v246
	v_med3_f32 v227, v227, s44, v246
	v_med3_f32 v228, v228, s44, v246
	v_med3_f32 v229, v229, s44, v246
	v_med3_f32 v230, v230, s44, v246
	v_med3_f32 v231, v231, s44, v246
	v_med3_f32 v232, v232, s44, v246
	v_med3_f32 v233, v233, s44, v246
	v_med3_f32 v234, v234, s44, v246
	v_med3_f32 v235, v235, s44, v246
	v_med3_f32 v236, v236, s44, v246
	v_med3_f32 v237, v237, s44, v246
	v_med3_f32 v238, v238, s44, v246
	v_med3_f32 v239, v239, s44, v246
	v_med3_f32 v240, v240, s44, v246
	v_med3_f32 v241, v241, s44, v246
	v_mov_b32_e32 v242, 0
	v_mov_b32_e32 v243, 0
	v_mov_b32_e32 v244, 0
	v_mov_b32_e32 v245, 0
	v_cvt_pk_fp8_f32 v242, v226, v227
	v_cvt_pk_fp8_f32 v243, v230, v231
	v_cvt_pk_fp8_f32 v244, v234, v235
	v_cvt_pk_fp8_f32 v245, v238, v239
	v_cvt_pk_fp8_f32 v242, v228, v229 op_sel:[0,0,1]
	v_cvt_pk_fp8_f32 v243, v232, v233 op_sel:[0,0,1]
	v_cvt_pk_fp8_f32 v244, v236, v237 op_sel:[0,0,1]
	v_cvt_pk_fp8_f32 v245, v240, v241 op_sel:[0,0,1]
	s_nop 0
	global_store_dwordx4 v109, v[242:245], s[6:7]
	s_add_i32 s26, s23, 72
	s_add_i32 s27, s23, 88
	s_waitcnt vmcnt(12)
	v_mul_f32_e32 v176, v218, v176
	v_mul_f32_e32 v177, v218, v177
	v_mul_f32_e32 v178, v218, v178
	v_mul_f32_e32 v179, v218, v179
	ds_write_b128 v210, v[176:179]
	v_mul_f32_e32 v180, v219, v180
	v_mul_f32_e32 v181, v219, v181
	v_mul_f32_e32 v182, v219, v182
	v_mul_f32_e32 v183, v219, v183
	ds_write_b128 v210, v[180:183] offset:1024
	v_mul_f32_e32 v184, v220, v184
	v_mul_f32_e32 v185, v220, v185
	v_mul_f32_e32 v186, v220, v186
	v_mul_f32_e32 v187, v220, v187
	ds_write_b128 v210, v[184:187] offset:2048
	v_mul_f32_e32 v188, v221, v188
	v_mul_f32_e32 v189, v221, v189
	v_mul_f32_e32 v190, v221, v190
	v_mul_f32_e32 v191, v221, v191
	ds_write_b128 v210, v[188:191] offset:3072
	v_mul_f32_e32 v192, v222, v192
	v_mul_f32_e32 v193, v222, v193
	v_mul_f32_e32 v194, v222, v194
	v_mul_f32_e32 v195, v222, v195
	ds_write_b128 v210, v[192:195] offset:4096
	v_mul_f32_e32 v196, v223, v196
	v_mul_f32_e32 v197, v223, v197
	v_mul_f32_e32 v198, v223, v198
	v_mul_f32_e32 v199, v223, v199
	ds_write_b128 v210, v[196:199] offset:5120
	v_mul_f32_e32 v200, v224, v200
	v_mul_f32_e32 v201, v224, v201
	v_mul_f32_e32 v202, v224, v202
	v_mul_f32_e32 v203, v224, v203
	ds_write_b128 v210, v[200:203] offset:6144
	v_mul_f32_e32 v204, v225, v204
	v_mul_f32_e32 v205, v225, v205
	v_mul_f32_e32 v206, v225, v206
	v_mul_f32_e32 v207, v225, v207
	ds_write_b128 v210, v[204:207] offset:7168
	s_waitcnt lgkmcnt(0)
	s_barrier
; #define GAS __attribute__((address_space(1)))
; #define LAS __attribute__((address_space(3)))
; #define LDS_WAIT() asm volatile("s_waitcnt lgkmcnt(0)" ::: "memory")
; __device__ __forceinline__ int src_col_in(int c) {
;     if (c < 5120) { const int blk = c >> 7, p = c & 127; const bool rope = blk < 16 || ((((blk - 16) >> 2) & 1) == 0); const int d = rope ? (p >> 1) + 64 * (p & 1) : p; return blk * 128 + d; }
;     if (c < OFF_Z) return c + 2096;
;     if (c < OFF_G) return c - 4048;
;     if (c < OFF_DT) return 5120 + (c - OFF_G);
;     if (c < NSRC) return c;
;     return -1;
; }
;     const int pr = item >> 1, kb = 2 * (pr / nblk) + (item & 1), nb = pr % nblk, k0 = 64 * kb, n0 = 32 * nb;
;     const int nr = n0 + (lane & 31); const int sc = MAP == 1 ? src_col_in(nr) : nr;
;     float v[32];
; #pragma unroll
;     for (int i = 0; i < 32; ++i) v[i] = sc >= 0 ? W[(size_t)(k0 + 2 * i + (lane >> 5)) * Nsrc + sc] : 0.f;
; #pragma unroll
;     for (int i = 0; i < 32; ++i) { const int k = k0 + 2 * i + (lane >> 5); float x = v[i] * wscale; if (KS) x *= (k < ksplit ? ksA[k] : ksB[k - ksplit]); scr[(2 * i + (lane >> 5)) * 33 + (lane & 31)] = x; }
;     LDS_WAIT(); asm volatile("" ::: "memory");
;     const int c = lane & 7;
; #pragma unroll
;     for (int j = 0; j < 4; ++j) { const int n = (lane >> 3) + 8 * j; const LAS float* s = scr + (8 * c) * 33 + n;
;         const unsigned long long o = (unsigned long long)pg8::pk4_fp8(s[0 * 33], s[1 * 33], s[2 * 33], s[3 * 33]) | ((unsigned long long)pg8::pk4_fp8(s[4 * 33], s[5 * 33], s[6 * 33], s[7 * 33]) << 32);
;         *(GAS unsigned long long*)(WT + (size_t)(n0 + n) * K + k0 + 8 * c) = o; }
;     LDS_WAIT(); asm volatile("" ::: "memory");
; }
	s_mul_i32 s20, s26, 0x80000
	s_add_u32 s6, s18, s20
	s_addc_u32 s7, s19, 0
	s_cmp_lt_u32 s26, 16
	s_cselect_b32 s20, 1, 0
	s_sub_i32 s21, s26, 16
	s_bitcmp0_b32 s21, 2
	s_cselect_b32 s21, 1, 0
	s_cmp_lt_u32 s26, 40
	s_cselect_b32 s21, s21, 0
	s_or_b32 s20, s20, s21
	s_cmp_lg_u32 s20, 0
	s_cselect_b64 s[20:21], -1, 0
	v_cndmask_b32_e64 v108, v100, v104, s[20:21]
	v_cndmask_b32_e64 v109, v101, v105, s[20:21]
	ds_read_b32 v226, v212
	ds_read_b32 v227, v212 offset:512
	ds_read_b32 v228, v212 offset:1024
	ds_read_b32 v229, v212 offset:1536
	ds_read_b32 v230, v212 offset:2048
	ds_read_b32 v231, v212 offset:2560
	ds_read_b32 v232, v212 offset:3072
	ds_read_b32 v233, v212 offset:3584
	ds_read_b32 v234, v212 offset:4096
	ds_read_b32 v235, v212 offset:4608
	ds_read_b32 v236, v212 offset:5120
	ds_read_b32 v237, v212 offset:5632
	ds_read_b32 v238, v212 offset:6144
	ds_read_b32 v239, v212 offset:6656
	ds_read_b32 v240, v212 offset:7168
	ds_read_b32 v241, v212 offset:7680
	s_waitcnt lgkmcnt(0)
	v_max_f32_e32 v226, v226, v226
	v_max_f32_e32 v227, v227, v227
	v_max_f32_e32 v228, v228, v228
	v_max_f32_e32 v229, v229, v229
	v_max_f32_e32 v230, v230, v230
	v_max_f32_e32 v231, v231, v231
	v_max_f32_e32 v232, v232, v232
	v_max_f32_e32 v233, v233, v233
	v_max_f32_e32 v234, v234, v234
	v_max_f32_e32 v235, v235, v235
	v_max_f32_e32 v236, v236, v236
	v_max_f32_e32 v237, v237, v237
	v_max_f32_e32 v238, v238, v238
	v_max_f32_e32 v239, v239, v239
	v_max_f32_e32 v240, v240, v240
	v_max_f32_e32 v241, v241, v241
	v_med3_f32 v226, v226, s44, v246
	v_med3_f32 v227, v227, s44, v246
	v_med3_f32 v228, v228, s44, v246
	v_med3_f32 v229, v229, s44, v246
	v_med3_f32 v230, v230, s44, v246
	v_med3_f32 v231, v231, s44, v246
	v_med3_f32 v232, v232, s44, v246
	v_med3_f32 v233, v233, s44, v246
	v_med3_f32 v234, v234, s44, v246
	v_med3_f32 v235, v235, s44, v246
	v_med3_f32 v236, v236, s44, v246
	v_med3_f32 v237, v237, s44, v246
	v_med3_f32 v238, v238, s44, v246
	v_med3_f32 v239, v239, s44, v246
	v_med3_f32 v240, v240, s44, v246
	v_med3_f32 v241, v241, s44, v246
	v_mov_b32_e32 v242, 0
	v_mov_b32_e32 v243, 0
	v_mov_b32_e32 v244, 0
	v_mov_b32_e32 v245, 0
	v_cvt_pk_fp8_f32 v242, v226, v227
	v_cvt_pk_fp8_f32 v243, v230, v231
	v_cvt_pk_fp8_f32 v244, v234, v235
	v_cvt_pk_fp8_f32 v245, v238, v239
	v_cvt_pk_fp8_f32 v242, v228, v229 op_sel:[0,0,1]
	v_cvt_pk_fp8_f32 v243, v232, v233 op_sel:[0,0,1]
	v_cvt_pk_fp8_f32 v244, v236, v237 op_sel:[0,0,1]
	v_cvt_pk_fp8_f32 v245, v240, v241 op_sel:[0,0,1]
	s_nop 0
	global_store_dwordx4 v108, v[242:245], s[6:7]
	ds_read_b32 v226, v214
	ds_read_b32 v227, v214 offset:512
	ds_read_b32 v228, v214 offset:1024
	ds_read_b32 v229, v214 offset:1536
	ds_read_b32 v230, v214 offset:2048
	ds_read_b32 v231, v214 offset:2560
	ds_read_b32 v232, v214 offset:3072
	ds_read_b32 v233, v214 offset:3584
	ds_read_b32 v234, v214 offset:4096
	ds_read_b32 v235, v214 offset:4608
	ds_read_b32 v236, v214 offset:5120
	ds_read_b32 v237, v214 offset:5632
	ds_read_b32 v238, v214 offset:6144
	ds_read_b32 v239, v214 offset:6656
	ds_read_b32 v240, v214 offset:7168
	ds_read_b32 v241, v214 offset:7680
	s_waitcnt lgkmcnt(0)
	v_max_f32_e32 v226, v226, v226
	v_max_f32_e32 v227, v227, v227
	v_max_f32_e32 v228, v228, v228
	v_max_f32_e32 v229, v229, v229
	v_max_f32_e32 v230, v230, v230
	v_max_f32_e32 v231, v231, v231
	v_max_f32_e32 v232, v232, v232
	v_max_f32_e32 v233, v233, v233
	v_max_f32_e32 v234, v234, v234
	v_max_f32_e32 v235, v235, v235
	v_max_f32_e32 v236, v236, v236
	v_max_f32_e32 v237, v237, v237
	v_max_f32_e32 v238, v238, v238
	v_max_f32_e32 v239, v239, v239
	v_max_f32_e32 v240, v240, v240
	v_max_f32_e32 v241, v241, v241
	v_med3_f32 v226, v226, s44, v246
	v_med3_f32 v227, v227, s44, v246
	v_med3_f32 v228, v228, s44, v246
	v_med3_f32 v229, v229, s44, v246
	v_med3_f32 v230, v230, s44, v246
	v_med3_f32 v231, v231, s44, v246
	v_med3_f32 v232, v232, s44, v246
	v_med3_f32 v233, v233, s44, v246
	v_med3_f32 v234, v234, s44, v246
	v_med3_f32 v235, v235, s44, v246
	v_med3_f32 v236, v236, s44, v246
	v_med3_f32 v237, v237, s44, v246
	v_med3_f32 v238, v238, s44, v246
	v_med3_f32 v239, v239, s44, v246
	v_med3_f32 v240, v240, s44, v246
	v_med3_f32 v241, v241, s44, v246
	v_mov_b32_e32 v242, 0
	v_mov_b32_e32 v243, 0
	v_mov_b32_e32 v244, 0
	v_mov_b32_e32 v245, 0
	v_cvt_pk_fp8_f32 v242, v226, v227
	v_cvt_pk_fp8_f32 v243, v230, v231
	v_cvt_pk_fp8_f32 v244, v234, v235
	v_cvt_pk_fp8_f32 v245, v238, v239
	v_cvt_pk_fp8_f32 v242, v228, v229 op_sel:[0,0,1]
	v_cvt_pk_fp8_f32 v243, v232, v233 op_sel:[0,0,1]
	v_cvt_pk_fp8_f32 v244, v236, v237 op_sel:[0,0,1]
	v_cvt_pk_fp8_f32 v245, v240, v241 op_sel:[0,0,1]
	s_nop 0
	global_store_dwordx4 v109, v[242:245], s[6:7]
	s_add_i32 s26, s23, 80
	s_add_i32 s27, s23, 96
	s_waitcnt vmcnt(4)
	v_mul_f32_e32 v144, v218, v144
	v_mul_f32_e32 v145, v218, v145
	v_mul_f32_e32 v146, v218, v146
	v_mul_f32_e32 v147, v218, v147
	ds_write_b128 v209, v[144:147]
	v_mul_f32_e32 v148, v219, v148
	v_mul_f32_e32 v149, v219, v149
	v_mul_f32_e32 v150, v219, v150
	v_mul_f32_e32 v151, v219, v151
	ds_write_b128 v209, v[148:151] offset:1024
	v_mul_f32_e32 v152, v220, v152
	v_mul_f32_e32 v153, v220, v153
	v_mul_f32_e32 v154, v220, v154
	v_mul_f32_e32 v155, v220, v155
	ds_write_b128 v209, v[152:155] offset:2048
	v_mul_f32_e32 v156, v221, v156
	v_mul_f32_e32 v157, v221, v157
	v_mul_f32_e32 v158, v221, v158
	v_mul_f32_e32 v159, v221, v159
	ds_write_b128 v209, v[156:159] offset:3072
	v_mul_f32_e32 v160, v222, v160
	v_mul_f32_e32 v161, v222, v161
	v_mul_f32_e32 v162, v222, v162
	v_mul_f32_e32 v163, v222, v163
	ds_write_b128 v209, v[160:163] offset:4096
	v_mul_f32_e32 v164, v223, v164
	v_mul_f32_e32 v165, v223, v165
	v_mul_f32_e32 v166, v223, v166
	v_mul_f32_e32 v167, v223, v167
	ds_write_b128 v209, v[164:167] offset:5120
	v_mul_f32_e32 v168, v224, v168
	v_mul_f32_e32 v169, v224, v169
	v_mul_f32_e32 v170, v224, v170
	v_mul_f32_e32 v171, v224, v171
	ds_write_b128 v209, v[168:171] offset:6144
	v_mul_f32_e32 v172, v225, v172
	v_mul_f32_e32 v173, v225, v173
	v_mul_f32_e32 v174, v225, v174
	v_mul_f32_e32 v175, v225, v175
	ds_write_b128 v209, v[172:175] offset:7168
	s_waitcnt lgkmcnt(0)
	s_barrier
; #define GAS __attribute__((address_space(1)))
; #define LAS __attribute__((address_space(3)))
; #define LDS_WAIT() asm volatile("s_waitcnt lgkmcnt(0)" ::: "memory")
; __device__ __forceinline__ unsigned pk4_fp8(float a, float b, float c, float d) {
;     a = fminf(fmaxf(a, -448.f), 448.f); b = fminf(fmaxf(b, -448.f), 448.f); c = fminf(fmaxf(c, -448.f), 448.f); d = fminf(fmaxf(d, -448.f), 448.f);
;     int w = __builtin_amdgcn_cvt_pk_fp8_f32(a, b, 0, false); w = __builtin_amdgcn_cvt_pk_fp8_f32(c, d, w, true); return (unsigned)w; }
;     const int pr = item >> 1, kb = 2 * (pr / nblk) + (item & 1), nb = pr % nblk, k0 = 64 * kb, n0 = 32 * nb;
;     const int nr = n0 + (lane & 31); const int sc = MAP == 1 ? src_col_in(nr) : nr;
;     float v[32];
; #pragma unroll
;     for (int i = 0; i < 32; ++i) v[i] = sc >= 0 ? W[(size_t)(k0 + 2 * i + (lane >> 5)) * Nsrc + sc] : 0.f;
; #pragma unroll
;     for (int i = 0; i < 32; ++i) { const int k = k0 + 2 * i + (lane >> 5); float x = v[i] * wscale; if (KS) x *= (k < ksplit ? ksA[k] : ksB[k - ksplit]); scr[(2 * i + (lane >> 5)) * 33 + (lane & 31)] = x; }
;     LDS_WAIT(); asm volatile("" ::: "memory");
;     const int c = lane & 7;
; #pragma unroll
;     for (int j = 0; j < 4; ++j) { const int n = (lane >> 3) + 8 * j; const LAS float* s = scr + (8 * c) * 33 + n;
;         const unsigned long long o = (unsigned long long)pg8::pk4_fp8(s[0 * 33], s[1 * 33], s[2 * 33], s[3 * 33]) | ((unsigned long long)pg8::pk4_fp8(s[4 * 33], s[5 * 33], s[6 * 33], s[7 * 33]) << 32);
;         *(GAS unsigned long long*)(WT + (size_t)(n0 + n) * K + k0 + 8 * c) = o; }
;     LDS_WAIT(); asm volatile("" ::: "memory");
; }
	s_mul_i32 s20, s26, 0x80000
	s_add_u32 s6, s18, s20
	s_addc_u32 s7, s19, 0
	s_cmp_lt_u32 s26, 16
	s_cselect_b32 s20, 1, 0
	s_sub_i32 s21, s26, 16
	s_bitcmp0_b32 s21, 2
	s_cselect_b32 s21, 1, 0
	s_cmp_lt_u32 s26, 40
	s_cselect_b32 s21, s21, 0
	s_or_b32 s20, s20, s21
	s_cmp_lg_u32 s20, 0
	s_cselect_b64 s[20:21], -1, 0
	v_cndmask_b32_e64 v108, v100, v104, s[20:21]
	v_cndmask_b32_e64 v109, v101, v105, s[20:21]
	ds_read_b32 v226, v211
	ds_read_b32 v227, v211 offset:512
	ds_read_b32 v228, v211 offset:1024
	ds_read_b32 v229, v211 offset:1536
	ds_read_b32 v230, v211 offset:2048
	ds_read_b32 v231, v211 offset:2560
	ds_read_b32 v232, v211 offset:3072
	ds_read_b32 v233, v211 offset:3584
	ds_read_b32 v234, v211 offset:4096
	ds_read_b32 v235, v211 offset:4608
	ds_read_b32 v236, v211 offset:5120
	ds_read_b32 v237, v211 offset:5632
	ds_read_b32 v238, v211 offset:6144
	ds_read_b32 v239, v211 offset:6656
	ds_read_b32 v240, v211 offset:7168
	ds_read_b32 v241, v211 offset:7680
	s_waitcnt lgkmcnt(0)
	v_max_f32_e32 v226, v226, v226
	v_max_f32_e32 v227, v227, v227
	v_max_f32_e32 v228, v228, v228
	v_max_f32_e32 v229, v229, v229
	v_max_f32_e32 v230, v230, v230
	v_max_f32_e32 v231, v231, v231
	v_max_f32_e32 v232, v232, v232
	v_max_f32_e32 v233, v233, v233
	v_max_f32_e32 v234, v234, v234
	v_max_f32_e32 v235, v235, v235
	v_max_f32_e32 v236, v236, v236
	v_max_f32_e32 v237, v237, v237
	v_max_f32_e32 v238, v238, v238
	v_max_f32_e32 v239, v239, v239
	v_max_f32_e32 v240, v240, v240
	v_max_f32_e32 v241, v241, v241
	v_med3_f32 v226, v226, s44, v246
	v_med3_f32 v227, v227, s44, v246
	v_med3_f32 v228, v228, s44, v246
	v_med3_f32 v229, v229, s44, v246
	v_med3_f32 v230, v230, s44, v246
	v_med3_f32 v231, v231, s44, v246
	v_med3_f32 v232, v232, s44, v246
	v_med3_f32 v233, v233, s44, v246
	v_med3_f32 v234, v234, s44, v246
	v_med3_f32 v235, v235, s44, v246
	v_med3_f32 v236, v236, s44, v246
	v_med3_f32 v237, v237, s44, v246
	v_med3_f32 v238, v238, s44, v246
	v_med3_f32 v239, v239, s44, v246
	v_med3_f32 v240, v240, s44, v246
	v_med3_f32 v241, v241, s44, v246
	v_mov_b32_e32 v242, 0
	v_mov_b32_e32 v243, 0
	v_mov_b32_e32 v244, 0
	v_mov_b32_e32 v245, 0
	v_cvt_pk_fp8_f32 v242, v226, v227
	v_cvt_pk_fp8_f32 v243, v230, v231
	v_cvt_pk_fp8_f32 v244, v234, v235
	v_cvt_pk_fp8_f32 v245, v238, v239
	v_cvt_pk_fp8_f32 v242, v228, v229 op_sel:[0,0,1]
	v_cvt_pk_fp8_f32 v243, v232, v233 op_sel:[0,0,1]
	v_cvt_pk_fp8_f32 v244, v236, v237 op_sel:[0,0,1]
	v_cvt_pk_fp8_f32 v245, v240, v241 op_sel:[0,0,1]
	s_nop 0
	global_store_dwordx4 v108, v[242:245], s[6:7]
	ds_read_b32 v226, v213
	ds_read_b32 v227, v213 offset:512
	ds_read_b32 v228, v213 offset:1024
	ds_read_b32 v229, v213 offset:1536
	ds_read_b32 v230, v213 offset:2048
	ds_read_b32 v231, v213 offset:2560
	ds_read_b32 v232, v213 offset:3072
	ds_read_b32 v233, v213 offset:3584
	ds_read_b32 v234, v213 offset:4096
	ds_read_b32 v235, v213 offset:4608
	ds_read_b32 v236, v213 offset:5120
	ds_read_b32 v237, v213 offset:5632
	ds_read_b32 v238, v213 offset:6144
	ds_read_b32 v239, v213 offset:6656
	ds_read_b32 v240, v213 offset:7168
	ds_read_b32 v241, v213 offset:7680
	s_waitcnt lgkmcnt(0)
	v_max_f32_e32 v226, v226, v226
	v_max_f32_e32 v227, v227, v227
	v_max_f32_e32 v228, v228, v228
	v_max_f32_e32 v229, v229, v229
	v_max_f32_e32 v230, v230, v230
	v_max_f32_e32 v231, v231, v231
	v_max_f32_e32 v232, v232, v232
	v_max_f32_e32 v233, v233, v233
	v_max_f32_e32 v234, v234, v234
	v_max_f32_e32 v235, v235, v235
	v_max_f32_e32 v236, v236, v236
	v_max_f32_e32 v237, v237, v237
	v_max_f32_e32 v238, v238, v238
	v_max_f32_e32 v239, v239, v239
	v_max_f32_e32 v240, v240, v240
	v_max_f32_e32 v241, v241, v241
	v_med3_f32 v226, v226, s44, v246
	v_med3_f32 v227, v227, s44, v246
	v_med3_f32 v228, v228, s44, v246
	v_med3_f32 v229, v229, s44, v246
	v_med3_f32 v230, v230, s44, v246
	v_med3_f32 v231, v231, s44, v246
	v_med3_f32 v232, v232, s44, v246
	v_med3_f32 v233, v233, s44, v246
	v_med3_f32 v234, v234, s44, v246
	v_med3_f32 v235, v235, s44, v246
	v_med3_f32 v236, v236, s44, v246
	v_med3_f32 v237, v237, s44, v246
	v_med3_f32 v238, v238, s44, v246
	v_med3_f32 v239, v239, s44, v246
	v_med3_f32 v240, v240, s44, v246
	v_med3_f32 v241, v241, s44, v246
	v_mov_b32_e32 v242, 0
	v_mov_b32_e32 v243, 0
	v_mov_b32_e32 v244, 0
	v_mov_b32_e32 v245, 0
	v_cvt_pk_fp8_f32 v242, v226, v227
	v_cvt_pk_fp8_f32 v243, v230, v231
	v_cvt_pk_fp8_f32 v244, v234, v235
	v_cvt_pk_fp8_f32 v245, v238, v239
	v_cvt_pk_fp8_f32 v242, v228, v229 op_sel:[0,0,1]
	v_cvt_pk_fp8_f32 v243, v232, v233 op_sel:[0,0,1]
	v_cvt_pk_fp8_f32 v244, v236, v237 op_sel:[0,0,1]
	v_cvt_pk_fp8_f32 v245, v240, v241 op_sel:[0,0,1]
	s_nop 0
	global_store_dwordx4 v109, v[242:245], s[6:7]
	s_waitcnt lgkmcnt(0)
	s_barrier
; #define LAS __attribute__((address_space(3)))
; __global__ void __launch_bounds__(NWAVES * 64, 2) hybrid_fwd(Args args) {
;     ...
;         LAS float* scr = (LAS float*)(F.lds + RING_OFF + wave * 16384);
;         constexpr int I_IN = (DM / 64) * (NPROJ / 32), I_O = (DM / 64) * (DM / 32), I_UP = (DM / 64) * (FF / 32), I_DN = (FF / 64) * (DM / 32);
;         constexpr int I_L = I_IN + I_O + I_UP + I_DN;
;         for (int rep = 0; rep < REP_PRO; ++rep)
;         for (int it = gw; it < DEPTH * I_L; it += NGW) {
;             const int l = it / I_L; int r = it % I_L;
;             if (r < I_IN) { if (l >= PROJ_F8_FROM) p0_transpose_item_f8<true, 1>(args.in[2] + (size_t)l * DM * NSRC, DM, NSRC, NPROJ / 32, (unsigned char*)(ws + WS_WIN + l * SZ_WIN), WUP8_SCALE, args.in[1] + l * DM, args.in[1] + l * DM, DM, scr, r, lane);
;                 else p0_transpose_item<1, true>(args.in[2] + (size_t)l * DM * NSRC, DM, NSRC, NPROJ / 32, (bf16*)(ws + WS_WIN + l * SZ_WIN), args.in[1] + l * DM, args.in[1] + l * DM, DM, scr, r, lane); continue; } r -= I_IN;
	v_readlane_b32 s12, v253, 35
	v_readlane_b32 s18, v253, 41
	v_readlane_b32 s19, v253, 42
	s_add_u32 s81, s18, 0x1f600000
	s_addc_u32 s94, s19, 0
	s_add_u32 s24, s18, 0xf600000
	v_or_b32_e32 v2, 2, v6
	v_mov_b32_e32 v3, 0x630
	v_readlane_b32 s13, v253, 36
	v_readlane_b32 s14, v253, 37
	v_readlane_b32 s15, v253, 38
	s_addc_u32 s25, s19, 0
	v_mad_u32_u24 v58, v2, s0, v3
	v_mov_b32_e32 v3, 0xc60
	s_add_u32 s26, s18, 0xb600000
	v_mad_u32_u24 v59, v2, s0, v3
	v_readlane_b32 s0, v253, 19
	s_addc_u32 s27, s19, 0
	v_readlane_b32 s2, v253, 21
	v_readlane_b32 s10, v253, 29
	v_readlane_b32 s3, v253, 22
	v_readlane_b32 s11, v253, 30
	s_add_u32 s2, s10, 0x4000000
	v_readlane_b32 s40, v253, 3
	s_addc_u32 s3, s11, 0
	v_readlane_b32 s52, v253, 15
	v_readlane_b32 s53, v253, 16
	s_add_u32 s22, s52, 0x2000
	v_readlane_b32 s8, v253, 27
	s_addc_u32 s23, s53, 0
	v_readlane_b32 s9, v253, 28
	s_add_u32 s84, s8, 0x2000
	s_addc_u32 s85, s9, 0
	s_add_u32 s33, s18, 0x200000
	v_readlane_b32 s44, v253, 7
	s_addc_u32 s38, s19, 0
	v_mov_b32_e32 v9, v11
	v_readlane_b32 s1, v253, 20
	v_readlane_b32 s45, v253, 8
	s_add_u32 s86, s44, 0xb140000
	v_mul_u32_u24_e32 v57, 0x84, v2
	v_readlane_b32 s42, v253, 5
	v_lshl_add_u64 v[2:3], s[18:19], 0, v[8:9]
	s_mov_b64 s[0:1], 0xd600000
	s_addc_u32 s87, s45, 0
	v_readlane_b32 s12, v253, 31
	v_readlane_b32 s13, v253, 32
	v_readlane_b32 s14, v253, 33
	v_readlane_b32 s15, v253, 34
	v_readlane_b32 s43, v253, 6
	v_readlane_b32 s54, v253, 17
	v_readlane_b32 s55, v253, 18
	v_lshl_add_u64 v[12:13], v[2:3], 0, s[0:1]
	s_add_u32 s88, s42, 0x4000
	s_mov_b64 s[0:1], 0x5c00000
	v_readlane_b32 s41, v253, 4
	v_readlane_b32 s46, v253, 9
	v_readlane_b32 s47, v253, 10
	v_readlane_b32 s48, v253, 11
	v_readlane_b32 s49, v253, 12
	v_readlane_b32 s50, v253, 13
	s_addc_u32 s89, s43, 0
	v_lshlrev_b32_e32 v4, 6, v18
	v_lshl_add_u64 v[14:15], v[2:3], 0, s[0:1]
	s_lshl_b32 s0, s80, 5
	s_movk_i32 s12, 0xe000
	s_movk_i32 s14, 0xe008
	s_movk_i32 s18, 0xe010
	s_movk_i32 s78, 0xe018
	s_movk_i32 s92, 0xe0d0
	s_movk_i32 s28, 0xe0d8
	s_movk_i32 s34, 0xe0e0
	s_movk_i32 s52, 0xe0e8
	s_movk_i32 s54, 0xe0f0
	s_movk_i32 s56, 0xe0f8
	v_or_b32_e32 v26, 0x2000, v18
	v_or_b32_e32 v27, 0x4000, v18
	v_or_b32_e32 v28, 0x6000, v18
	v_or_b32_e32 v29, 0x8000, v18
	v_or_b32_e32 v30, 0xa000, v18
	v_or_b32_e32 v31, 0xc000, v18
	v_or_b32_e32 v32, 0xe000, v18
	v_or_b32_e32 v33, 0x10000, v18
	v_or_b32_e32 v34, 0x12000, v18
	v_or_b32_e32 v35, 0x14000, v18
	v_or_b32_e32 v36, 0x16000, v18
	v_or_b32_e32 v37, 0x18000, v18
	v_or_b32_e32 v38, 0x1a000, v18
	v_or_b32_e32 v39, 0x1c000, v18
	v_or_b32_e32 v40, 0x1e000, v18
	v_or_b32_e32 v41, 0x20000, v18
	v_or_b32_e32 v42, 0x22000, v18
	v_or_b32_e32 v43, 0x24000, v18
	v_or_b32_e32 v44, 0x26000, v18
	v_or_b32_e32 v45, 0x28000, v18
	v_or_b32_e32 v46, 0x2a000, v18
	v_or_b32_e32 v47, 0x2c000, v18
	v_or_b32_e32 v48, 0x2e000, v18
	v_or_b32_e32 v49, 0x30000, v18
	v_or_b32_e32 v50, 0x32000, v18
	v_or_b32_e32 v51, 0x34000, v18
	v_or_b32_e32 v52, 0x36000, v18
	v_or_b32_e32 v53, 0x38000, v18
	v_or_b32_e32 v54, 0x3a000, v18
	v_or_b32_e32 v55, 0x3c000, v18
	v_or_b32_e32 v56, 0x3e000, v18
	v_and_b32_e32 v60, 64, v4
	v_mov_b32_e32 v7, v11
	s_lshl_b32 s39, s80, 6
	s_add_i32 s40, s0, 0xfff4c000
	s_lshl_b32 s41, s83, 8
	s_lshl_b32 s42, s80, 4
	s_lshl_b32 s43, s83, 7
	s_mov_b32 s91, 0
	s_mov_b32 s44, 0xc3e00000
	s_movk_i32 s45, 0x7fff
	s_mov_b32 s46, 0xffff0000
	s_movk_i32 s47, 0x2c2f
	s_movk_i32 s48, 0x2c50
	s_mov_b32 s49, 0xb140
	v_add_u32_e32 v61, 0x400, v19
	v_add_u32_e32 v62, 0x800, v19
	v_add_u32_e32 v63, 0xc00, v19
	v_mov_b32_e32 v64, 0x43e00000
	s_mov_b32 s50, s80
	s_mov_b32 s13, -1
	s_mov_b32 s15, -1
	s_mov_b32 s19, -1
	s_mov_b32 s79, -1
	s_mov_b32 s93, -1
	s_mov_b32 s29, -1
	s_mov_b32 s35, -1
	s_mov_b32 s53, -1
	s_mov_b32 s55, -1
	s_mov_b32 s57, -1
	v_readlane_b32 s16, v253, 39
	v_readlane_b32 s17, v253, 40
	v_readlane_b32 s4, v253, 23
	v_readlane_b32 s5, v253, 24
	v_readlane_b32 s6, v253, 25
	v_readlane_b32 s7, v253, 26
	v_readlane_b32 s51, v253, 14
	s_branch .LBB0_15

; __device__ __forceinline__ int src_col_in(int c) {
;     if (c < 5120) { const int blk = c >> 7, p = c & 127; const bool rope = blk < 16 || ((((blk - 16) >> 2) & 1) == 0); const int d = rope ? (p >> 1) + 64 * (p & 1) : p; return blk * 128 + d; }
;     if (c < OFF_Z) return c + 2096;
;     if (c < OFF_G) return c - 4048;
;     if (c < OFF_DT) return 5120 + (c - OFF_G);
;     if (c < NSRC) return c;
;     return -1;
; }
; __global__ void __launch_bounds__(NWAVES * 64, 2) hybrid_fwd(Args args) {
;     ...
;         for (int it = gw; it < DEPTH * I_L; it += NGW) {
;             const int l = it / I_L; int r = it % I_L;
;             if (r < I_IN) { if (l >= PROJ_F8_FROM) p0_transpose_item_f8<true, 1>(args.in[2] + (size_t)l * DM * NSRC, DM, NSRC, NPROJ / 32, (unsigned char*)(ws + WS_WIN + l * SZ_WIN), WUP8_SCALE, args.in[1] + l * DM, args.in[1] + l * DM, DM, scr, r, lane);
;                 else p0_transpose_item<1, true>(args.in[2] + (size_t)l * DM * NSRC, DM, NSRC, NPROJ / 32, (bf16*)(ws + WS_WIN + l * SZ_WIN), args.in[1] + l * DM, args.in[1] + l * DM, DM, scr, r, lane); continue; } r -= I_IN;
.LBB0_28:
	s_andn2_b64 vcc, exec, s[0:1]
	s_cbranch_vccnz .LBB0_14
	s_cmp_lt_i32 s50, 0x17a00
	s_mov_b64 s[0:1], -1
	s_cbranch_scc0 .LBB0_111
	s_mul_hi_i32 s1, s51, 0xb60b60b7
	s_add_i32 s1, s1, s51
	s_lshr_b32 s16, s1, 31
	s_ashr_i32 s30, s1, 8
	s_add_i32 s30, s30, s16
	s_mul_i32 s0, s58, 0x17a00
	s_mul_i32 s1, s30, 0xfffffe98
	s_sub_i32 s0, s1, s0
	s_add_i32 s31, s50, s0
	s_cmpk_lt_u32 s31, 0x160
	s_cbranch_scc1 .LBB0_14
	s_lshl_b32 s16, s31, 5
	v_or_b32_e32 v2, s16, v18
	s_movk_i32 s0, 0x13ff
	v_cmp_lt_i32_e32 vcc, s0, v2
	s_and_saveexec_b64 s[0:1], vcc
	s_xor_b64 s[0:1], exec, s[0:1]
	s_cbranch_execz .LBB0_44
	s_cmpk_gt_u32 s16, 0x23ff
	s_mov_b64 s[20:21], -1
	s_cbranch_scc0 .LBB0_41
	s_cmpk_gt_u32 s16, 0x2bff
	s_cbranch_scc0 .LBB0_38
	v_cmp_lt_u32_e32 vcc, s47, v2
	s_and_saveexec_b64 s[20:21], vcc
	s_xor_b64 s[20:21], exec, s[20:21]
	v_cmp_gt_u32_e32 vcc, s48, v2
	s_nop 1
	v_cndmask_b32_e32 v10, -1, v2, vcc
	s_andn2_saveexec_b64 s[20:21], s[20:21]
	v_add_u32_e32 v10, 0xffffe800, v2
	s_or_b64 exec, exec, s[20:21]
	s_mov_b64 s[20:21], 0

;     const int pr = item >> 1, kb = 2 * (pr / nblk) + (item & 1), nb = pr % nblk, k0 = 64 * kb, n0 = 32 * nb;
;     const int nr = n0 + (lane & 31); const int sc = MAP == 1 ? src_col_in(nr) : nr;
; __global__ void __launch_bounds__(NWAVES * 64, 2) hybrid_fwd(Args args) {
;     ...
;         for (int it = gw; it < DEPTH * I_L; it += NGW) {
;             const int l = it / I_L; int r = it % I_L;
;             if (r < I_IN) { if (l >= PROJ_F8_FROM) p0_transpose_item_f8<true, 1>(args.in[2] + (size_t)l * DM * NSRC, DM, NSRC, NPROJ / 32, (unsigned char*)(ws + WS_WIN + l * SZ_WIN), WUP8_SCALE, args.in[1] + l * DM, args.in[1] + l * DM, DM, scr, r, lane);
.LBB0_111:
	s_and_b64 vcc, exec, s[0:1]
	s_cbranch_vccz .LBB0_14
	s_lshr_b32 s0, s51, 1
	s_mul_hi_u32 s1, s0, 0xb60b60b7
	s_lshr_b32 s1, s1, 8
	s_mulk_i32 s1, 0x168
	s_sub_i32 s16, s0, s1
	s_cmpk_lt_u32 s16, 0x160
	s_cbranch_scc1 .LBB0_14
	s_lshl_b32 s20, s16, 5
	v_or_b32_e32 v2, s20, v18
	s_cmpk_gt_u32 s16, 0x9f
	s_mov_b64 s[0:1], -1
	s_cbranch_scc0 .LBB0_126
	s_cmpk_gt_u32 s16, 0x11f
	s_cbranch_scc0 .LBB0_123
	s_cmpk_gt_u32 s16, 0x15f
	s_cbranch_scc0 .LBB0_120
	v_cmp_lt_u32_e32 vcc, s47, v2
	s_and_saveexec_b64 s[0:1], vcc
	s_xor_b64 s[0:1], exec, s[0:1]
	v_cmp_gt_u32_e32 vcc, s48, v2
	s_nop 1
	v_cndmask_b32_e32 v10, -1, v2, vcc
	s_andn2_saveexec_b64 s[0:1], s[0:1]
	v_add_u32_e32 v10, 0xffffe800, v2
	s_or_b64 exec, exec, s[0:1]
	s_mov_b64 s[0:1], 0
